# cache policy: G1 epilogue P stores made non-temporal (92 stores) to keep operand tiles in L2
# baseline (speedup 1.0000x reference)
.LBB0_318:
	v_mov_b64_e32 v[130:131], s[8:9]
	s_movk_i32 s17, 0x2400
	v_mad_i64_i32 v[134:135], s[2:3], v189, s17, v[130:131]
	v_lshlrev_b64 v[132:133], 1, v[64:65]
	v_lshl_add_u64 v[134:135], v[134:135], 0, v[132:133]
	v_or_b32_e32 v64, 16, v189
	v_cvt_pk_bf16_f32 v126, v126, v127
	v_cvt_pk_bf16_f32 v127, v128, v129
	v_cvt_pk_bf16_f32 v128, v122, v123
	v_cvt_pk_bf16_f32 v129, v124, v125
	global_store_dwordx4 v[134:135], v[126:129], off nt
	v_cvt_pk_bf16_f32 v114, v114, v115
	v_cvt_pk_bf16_f32 v115, v116, v117
	v_cvt_pk_bf16_f32 v116, v106, v107
	v_mad_i64_i32 v[106:107], s[2:3], v64, s17, v[130:131]
	v_cvt_pk_bf16_f32 v117, v108, v109
	global_store_dwordx4 v[134:135], v[114:117], off offset:256 nt
	v_or_b32_e32 v64, 32, v189
	s_nop 0
	v_lshl_add_u64 v[114:115], v[106:107], 0, v[132:133]
	v_cvt_pk_bf16_f32 v106, v118, v119
	v_cvt_pk_bf16_f32 v107, v120, v121
	v_cvt_pk_bf16_f32 v108, v110, v111
	v_cvt_pk_bf16_f32 v109, v112, v113
	global_store_dwordx4 v[114:115], v[106:109], off nt
	v_cvt_pk_bf16_f32 v98, v98, v99
	v_cvt_pk_bf16_f32 v99, v100, v101
	v_cvt_pk_bf16_f32 v100, v90, v91
	v_mad_i64_i32 v[90:91], s[2:3], v64, s17, v[130:131]
	v_cvt_pk_bf16_f32 v101, v92, v93
	global_store_dwordx4 v[114:115], v[98:101], off offset:256 nt
	v_or_b32_e32 v64, 48, v189
	s_nop 0
	v_lshl_add_u64 v[98:99], v[90:91], 0, v[132:133]
	v_cvt_pk_bf16_f32 v90, v102, v103
	v_cvt_pk_bf16_f32 v91, v104, v105
	v_cvt_pk_bf16_f32 v92, v94, v95
	v_cvt_pk_bf16_f32 v93, v96, v97
	global_store_dwordx4 v[98:99], v[90:93], off nt
	v_cvt_pk_bf16_f32 v82, v82, v83
	v_cvt_pk_bf16_f32 v83, v84, v85
	v_cvt_pk_bf16_f32 v84, v74, v75
	v_mad_i64_i32 v[74:75], s[2:3], v64, s17, v[130:131]
	v_cvt_pk_bf16_f32 v85, v76, v77
	global_store_dwordx4 v[98:99], v[82:85], off offset:256 nt
	v_add_u32_e32 v64, 0x80, v189
	s_nop 0
	v_lshl_add_u64 v[82:83], v[74:75], 0, v[132:133]
	v_cvt_pk_bf16_f32 v74, v86, v87
	v_cvt_pk_bf16_f32 v75, v88, v89
	v_cvt_pk_bf16_f32 v76, v78, v79
	v_cvt_pk_bf16_f32 v77, v80, v81
	global_store_dwordx4 v[82:83], v[74:77], off nt
	v_cvt_pk_bf16_f32 v70, v70, v71
	v_cvt_pk_bf16_f32 v71, v72, v73
	v_cvt_pk_bf16_f32 v72, v66, v67
	v_mad_i64_i32 v[66:67], s[2:3], v64, s17, v[130:131]
	v_lshl_add_u64 v[66:67], v[66:67], 0, v[132:133]
	v_cvt_pk_bf16_f32 v73, v68, v69
	global_store_dwordx4 v[82:83], v[70:73], off offset:256 nt
	v_cvt_pk_bf16_f32 v60, v60, v61
	v_cvt_pk_bf16_f32 v61, v62, v63
	v_cvt_pk_bf16_f32 v62, v56, v57
	v_cvt_pk_bf16_f32 v63, v58, v59
	global_store_dwordx4 v[66:67], v[60:63], off nt
	v_cvt_pk_bf16_f32 v48, v48, v49
	v_cvt_pk_bf16_f32 v49, v50, v51
	v_cvt_pk_bf16_f32 v50, v40, v41
	v_add_u32_e32 v40, 0x90, v189
	v_mad_i64_i32 v[40:41], s[2:3], v40, s17, v[130:131]
	v_cvt_pk_bf16_f32 v51, v42, v43
	global_store_dwordx4 v[66:67], v[48:51], off offset:256 nt
	s_nop 1
	v_lshl_add_u64 v[48:49], v[40:41], 0, v[132:133]
	v_cvt_pk_bf16_f32 v40, v52, v53
	v_cvt_pk_bf16_f32 v41, v54, v55
	v_cvt_pk_bf16_f32 v42, v44, v45
	v_cvt_pk_bf16_f32 v43, v46, v47
	global_store_dwordx4 v[48:49], v[40:43], off nt
	v_cvt_pk_bf16_f32 v32, v32, v33
	v_cvt_pk_bf16_f32 v33, v34, v35
	v_cvt_pk_bf16_f32 v34, v24, v25
	v_add_u32_e32 v24, 0xa0, v189
	v_mad_i64_i32 v[24:25], s[2:3], v24, s17, v[130:131]
	v_cvt_pk_bf16_f32 v35, v26, v27
	global_store_dwordx4 v[48:49], v[32:35], off offset:256 nt
	s_nop 1
	v_lshl_add_u64 v[32:33], v[24:25], 0, v[132:133]
	v_cvt_pk_bf16_f32 v24, v36, v37
	v_cvt_pk_bf16_f32 v25, v38, v39
	v_cvt_pk_bf16_f32 v26, v28, v29
	v_cvt_pk_bf16_f32 v27, v30, v31
	global_store_dwordx4 v[32:33], v[24:27], off nt
	v_cvt_pk_bf16_f32 v16, v16, v17
	v_cvt_pk_bf16_f32 v17, v18, v19
	v_cvt_pk_bf16_f32 v18, v8, v9
	v_add_u32_e32 v8, 0xb0, v189
	v_mad_i64_i32 v[8:9], s[2:3], v8, s17, v[130:131]
	v_lshl_add_u64 v[162:163], v[8:9], 0, v[132:133]
	v_cvt_pk_bf16_f32 v19, v10, v11
	global_store_dwordx4 v[32:33], v[16:19], off offset:256 nt
	v_cvt_pk_bf16_f32 v8, v20, v21
	v_cvt_pk_bf16_f32 v9, v22, v23
	v_cvt_pk_bf16_f32 v10, v12, v13
	v_cvt_pk_bf16_f32 v11, v14, v15
	global_store_dwordx4 v[162:163], v[8:11], off nt
	v_cvt_pk_bf16_f32 v130, v4, v5
	v_cvt_pk_bf16_f32 v131, v6, v7
	v_cvt_pk_bf16_f32 v132, v0, v1
	v_cvt_pk_bf16_f32 v133, v2, v3
	s_andn2_b64 vcc, exec, s[6:7]
	s_mov_b64 s[6:7], -1
	global_store_dwordx4 v[162:163], v[130:133], off offset:256 nt
	s_cbranch_vccnz .LBB0_302
	s_branch .LBB0_330

.LBB0_321:
	s_andn2_b64 vcc, exec, s[26:27]
	s_cbranch_vccnz .LBB0_323
	s_branch .Lg1rope_fast
	s_cselect_b64 vcc, -1, 0
	s_movk_i32 s3, 0x40ff
	v_cndmask_b32_e32 v134, 1.0, v202, vcc
	v_ashrrev_i32_e32 v133, 31, v64
	v_mov_b32_e32 v132, v64
	v_mov_b64_e32 v[130:131], s[8:9]
	s_movk_i32 s19, 0x2400
	v_cmp_lt_i32_e32 vcc, s3, v189
	v_add_u32_e32 v135, 0xffffbf00, v189
	v_mad_i64_i32 v[136:137], s[24:25], v189, s19, v[130:131]
	v_lshlrev_b64 v[132:133], 1, v[132:133]
	v_cndmask_b32_e32 v135, v189, v135, vcc
	v_lshl_add_u64 v[144:145], v[136:137], 0, v[132:133]
	s_movk_i32 s17, 0xff
	v_add_u32_e32 v136, 0xffffff00, v135
	v_cmp_lt_i32_e32 vcc, s17, v135
	v_lshrrev_b32_e32 v136, 6, v136
	v_and_b32_e32 v135, 15, v135
	v_cndmask_b32_e64 v135, v135, v136, s[4:5]
	v_lshlrev_b32_e32 v135, 6, v135
	v_cndmask_b32_e32 v135, 0, v135, vcc
	v_or_b32_e32 v136, v135, v187
	v_mov_b32_e32 v137, v65
	v_lshl_add_u64 v[140:141], v[136:137], 2, s[12:13]
	global_load_dwordx4 v[136:139], v[140:141], off offset:16
	s_nop 0
	global_load_dwordx4 v[140:143], v[140:141], off
	v_pk_mul_f32 v[160:161], v[134:135], v[126:127] op_sel_hi:[0,1]
	v_pk_mul_f32 v[158:159], v[134:135], v[128:129] op_sel_hi:[0,1]
	v_pk_mul_f32 v[162:163], v[134:135], v[124:125] op_sel_hi:[0,1]
	v_pk_mul_f32 v[164:165], v[134:135], v[122:123] op_sel_hi:[0,1]
	s_waitcnt vmcnt(0)
	v_pk_mul_f32 v[166:167], v[160:161], v[140:141]
	v_pk_mul_f32 v[160:161], v[160:161], v[140:141] op_sel:[0,1] op_sel_hi:[1,0]
	v_sub_f32_e32 v135, v166, v167
	v_add_f32_e32 v166, v160, v161
	v_pk_mul_f32 v[160:161], v[158:159], v[142:143]
	v_pk_mul_f32 v[158:159], v[158:159], v[142:143] op_sel:[0,1] op_sel_hi:[1,0]
	v_sub_f32_e32 v160, v160, v161
	v_add_f32_e32 v161, v158, v159
	v_pk_mul_f32 v[158:159], v[164:165], v[136:137]
	s_nop 0
	v_sub_f32_e32 v167, v158, v159
	v_pk_mul_f32 v[158:159], v[164:165], v[136:137] op_sel:[0,1] op_sel_hi:[1,0]
	s_nop 0
	v_add_f32_e32 v164, v158, v159
	v_pk_mul_f32 v[158:159], v[162:163], v[138:139]
	s_nop 0
	v_sub_f32_e32 v165, v158, v159
	v_pk_mul_f32 v[158:159], v[162:163], v[138:139] op_sel:[0,1] op_sel_hi:[1,0]
	s_nop 0
	v_add_f32_e32 v162, v158, v159
	v_cvt_pk_bf16_f32 v158, v135, v166
	v_cvt_pk_bf16_f32 v159, v160, v161
	v_cvt_pk_bf16_f32 v160, v167, v164
	v_cvt_pk_bf16_f32 v161, v165, v162
	global_store_dwordx4 v[144:145], v[158:161], off nt
	v_pk_mul_f32 v[164:165], v[134:135], v[106:107] op_sel_hi:[0,1]
	v_pk_mul_f32 v[162:163], v[134:135], v[108:109] op_sel_hi:[0,1]
	v_pk_mul_f32 v[160:161], v[134:135], v[114:115] op_sel_hi:[0,1]
	v_pk_mul_f32 v[158:159], v[134:135], v[116:117] op_sel_hi:[0,1]
	v_pk_mul_f32 v[166:167], v[160:161], v[140:141]
	v_pk_mul_f32 v[140:141], v[160:161], v[140:141] op_sel:[0,1] op_sel_hi:[1,0]
	v_sub_f32_e32 v135, v166, v167
	v_add_f32_e32 v160, v140, v141
	v_pk_mul_f32 v[140:141], v[158:159], v[142:143]
	s_nop 0
	v_sub_f32_e32 v161, v140, v141
	v_pk_mul_f32 v[140:141], v[158:159], v[142:143] op_sel:[0,1] op_sel_hi:[1,0]
	s_nop 0
	v_add_f32_e32 v142, v140, v141
	v_pk_mul_f32 v[140:141], v[164:165], v[136:137]
	v_pk_mul_f32 v[136:137], v[164:165], v[136:137] op_sel:[0,1] op_sel_hi:[1,0]
	v_sub_f32_e32 v140, v140, v141
	v_add_f32_e32 v141, v136, v137
	v_pk_mul_f32 v[136:137], v[162:163], v[138:139]
	s_nop 0
	v_sub_f32_e32 v143, v136, v137
	v_pk_mul_f32 v[136:137], v[162:163], v[138:139] op_sel:[0,1] op_sel_hi:[1,0]
	s_nop 0
	v_add_f32_e32 v139, v136, v137
	v_cvt_pk_bf16_f32 v136, v135, v160
	v_cvt_pk_bf16_f32 v137, v161, v142
	v_cvt_pk_bf16_f32 v138, v140, v141
	v_or_b32_e32 v135, 16, v189
	v_cvt_pk_bf16_f32 v139, v143, v139
	global_store_dwordx4 v[144:145], v[136:139], off offset:256 nt
	v_cmp_lt_i32_e32 vcc, s3, v135
	s_nop 0
	v_add_u32_e32 v138, 0xffffbf10, v189
	v_mad_i64_i32 v[136:137], s[24:25], v135, s19, v[130:131]
	v_cndmask_b32_e32 v135, v135, v138, vcc
	v_add_u32_e32 v138, 0xffffff00, v135
	v_cmp_lt_i32_e32 vcc, s17, v135
	v_lshrrev_b32_e32 v138, 6, v138
	v_and_b32_e32 v135, 31, v135
	v_cndmask_b32_e64 v135, v135, v138, s[4:5]
	v_lshlrev_b32_e32 v135, 6, v135
	v_cndmask_b32_e32 v135, 0, v135, vcc
	v_or_b32_e32 v138, v135, v187
	v_mov_b32_e32 v139, v65
	v_lshl_add_u64 v[142:143], v[138:139], 2, s[12:13]
	global_load_dwordx4 v[138:141], v[142:143], off offset:16
	s_nop 0
	global_load_dwordx4 v[142:145], v[142:143], off
	v_pk_mul_f32 v[160:161], v[134:135], v[118:119] op_sel_hi:[0,1]
	v_pk_mul_f32 v[158:159], v[134:135], v[120:121] op_sel_hi:[0,1]
	v_pk_mul_f32 v[162:163], v[134:135], v[112:113] op_sel_hi:[0,1]
	v_pk_mul_f32 v[164:165], v[134:135], v[110:111] op_sel_hi:[0,1]
	v_lshl_add_u64 v[136:137], v[136:137], 0, v[132:133]
	s_waitcnt vmcnt(0)
	v_pk_mul_f32 v[166:167], v[160:161], v[142:143]
	v_pk_mul_f32 v[160:161], v[160:161], v[142:143] op_sel:[0,1] op_sel_hi:[1,0]
	v_sub_f32_e32 v135, v166, v167
	v_add_f32_e32 v166, v160, v161
	v_pk_mul_f32 v[160:161], v[158:159], v[144:145]
	v_pk_mul_f32 v[158:159], v[158:159], v[144:145] op_sel:[0,1] op_sel_hi:[1,0]
	v_sub_f32_e32 v160, v160, v161
	v_add_f32_e32 v161, v158, v159
	v_pk_mul_f32 v[158:159], v[164:165], v[138:139]
	s_nop 0
	v_sub_f32_e32 v167, v158, v159
	v_pk_mul_f32 v[158:159], v[164:165], v[138:139] op_sel:[0,1] op_sel_hi:[1,0]
	s_nop 0
	v_add_f32_e32 v164, v158, v159
	v_pk_mul_f32 v[158:159], v[162:163], v[140:141]
	s_nop 0
	v_sub_f32_e32 v165, v158, v159
	v_pk_mul_f32 v[158:159], v[162:163], v[140:141] op_sel:[0,1] op_sel_hi:[1,0]
	s_nop 0
	v_add_f32_e32 v162, v158, v159
	v_cvt_pk_bf16_f32 v158, v135, v166
	v_cvt_pk_bf16_f32 v159, v160, v161
	v_cvt_pk_bf16_f32 v160, v167, v164
	v_cvt_pk_bf16_f32 v161, v165, v162
	global_store_dwordx4 v[136:137], v[158:161], off nt
	v_pk_mul_f32 v[164:165], v[134:135], v[90:91] op_sel_hi:[0,1]
	v_pk_mul_f32 v[162:163], v[134:135], v[92:93] op_sel_hi:[0,1]
	v_pk_mul_f32 v[160:161], v[134:135], v[98:99] op_sel_hi:[0,1]
	v_pk_mul_f32 v[158:159], v[134:135], v[100:101] op_sel_hi:[0,1]
	v_pk_mul_f32 v[166:167], v[160:161], v[142:143]
	v_pk_mul_f32 v[142:143], v[160:161], v[142:143] op_sel:[0,1] op_sel_hi:[1,0]
	v_sub_f32_e32 v135, v166, v167
	v_add_f32_e32 v160, v142, v143
	v_pk_mul_f32 v[142:143], v[158:159], v[144:145]
	s_nop 0
	v_sub_f32_e32 v161, v142, v143
	v_pk_mul_f32 v[142:143], v[158:159], v[144:145] op_sel:[0,1] op_sel_hi:[1,0]
	s_nop 0
	v_add_f32_e32 v144, v142, v143
	v_pk_mul_f32 v[142:143], v[164:165], v[138:139]
	v_pk_mul_f32 v[138:139], v[164:165], v[138:139] op_sel:[0,1] op_sel_hi:[1,0]
	v_sub_f32_e32 v142, v142, v143
	v_add_f32_e32 v143, v138, v139
	v_pk_mul_f32 v[138:139], v[162:163], v[140:141]
	s_nop 0
	v_sub_f32_e32 v145, v138, v139
	v_pk_mul_f32 v[138:139], v[162:163], v[140:141] op_sel:[0,1] op_sel_hi:[1,0]
	s_nop 0
	v_add_f32_e32 v141, v138, v139
	v_cvt_pk_bf16_f32 v138, v135, v160
	v_or_b32_e32 v135, 32, v189
	v_cvt_pk_bf16_f32 v139, v161, v144
	v_cvt_pk_bf16_f32 v140, v142, v143
	v_cvt_pk_bf16_f32 v141, v145, v141
	global_store_dwordx4 v[136:137], v[138:141], off offset:256 nt
	v_cmp_lt_i32_e32 vcc, s3, v135
	v_mad_i64_i32 v[136:137], s[24:25], v135, s19, v[130:131]
	v_add_u32_e32 v138, 0xffffbf20, v189
	v_cndmask_b32_e32 v135, v135, v138, vcc
	v_add_u32_e32 v138, 0xffffff00, v135
	v_cmp_lt_i32_e32 vcc, s17, v135
	v_lshrrev_b32_e32 v138, 6, v138
	v_and_b32_e32 v135, 47, v135
	v_cndmask_b32_e64 v135, v135, v138, s[4:5]
	v_lshlrev_b32_e32 v135, 6, v135
	v_cndmask_b32_e32 v135, 0, v135, vcc
	v_or_b32_e32 v138, v135, v187
	v_mov_b32_e32 v139, v65
	v_lshl_add_u64 v[142:143], v[138:139], 2, s[12:13]
	global_load_dwordx4 v[138:141], v[142:143], off offset:16
	s_nop 0
	global_load_dwordx4 v[142:145], v[142:143], off
	v_pk_mul_f32 v[160:161], v[134:135], v[102:103] op_sel_hi:[0,1]
	v_pk_mul_f32 v[158:159], v[134:135], v[104:105] op_sel_hi:[0,1]
	v_pk_mul_f32 v[162:163], v[134:135], v[96:97] op_sel_hi:[0,1]
	v_pk_mul_f32 v[164:165], v[134:135], v[94:95] op_sel_hi:[0,1]
	v_lshl_add_u64 v[136:137], v[136:137], 0, v[132:133]
	s_waitcnt vmcnt(0)
	v_pk_mul_f32 v[166:167], v[160:161], v[142:143]
	v_pk_mul_f32 v[160:161], v[160:161], v[142:143] op_sel:[0,1] op_sel_hi:[1,0]
	v_sub_f32_e32 v135, v166, v167
	v_add_f32_e32 v166, v160, v161
	v_pk_mul_f32 v[160:161], v[158:159], v[144:145]
	v_pk_mul_f32 v[158:159], v[158:159], v[144:145] op_sel:[0,1] op_sel_hi:[1,0]
	v_sub_f32_e32 v160, v160, v161
	v_add_f32_e32 v161, v158, v159
	v_pk_mul_f32 v[158:159], v[164:165], v[138:139]
	s_nop 0
	v_sub_f32_e32 v167, v158, v159
	v_pk_mul_f32 v[158:159], v[164:165], v[138:139] op_sel:[0,1] op_sel_hi:[1,0]
	s_nop 0
	v_add_f32_e32 v164, v158, v159
	v_pk_mul_f32 v[158:159], v[162:163], v[140:141]
	s_nop 0
	v_sub_f32_e32 v165, v158, v159
	v_pk_mul_f32 v[158:159], v[162:163], v[140:141] op_sel:[0,1] op_sel_hi:[1,0]
	s_nop 0
	v_add_f32_e32 v162, v158, v159
	v_cvt_pk_bf16_f32 v158, v135, v166
	v_cvt_pk_bf16_f32 v159, v160, v161
	v_cvt_pk_bf16_f32 v160, v167, v164
	v_cvt_pk_bf16_f32 v161, v165, v162
	global_store_dwordx4 v[136:137], v[158:161], off nt
	v_pk_mul_f32 v[164:165], v[134:135], v[74:75] op_sel_hi:[0,1]
	v_pk_mul_f32 v[162:163], v[134:135], v[76:77] op_sel_hi:[0,1]
	v_pk_mul_f32 v[160:161], v[134:135], v[82:83] op_sel_hi:[0,1]
	v_pk_mul_f32 v[158:159], v[134:135], v[84:85] op_sel_hi:[0,1]
	v_pk_mul_f32 v[166:167], v[160:161], v[142:143]
	v_pk_mul_f32 v[142:143], v[160:161], v[142:143] op_sel:[0,1] op_sel_hi:[1,0]
	v_sub_f32_e32 v135, v166, v167
	v_add_f32_e32 v160, v142, v143
	v_pk_mul_f32 v[142:143], v[158:159], v[144:145]
	s_nop 0
	v_sub_f32_e32 v161, v142, v143
	v_pk_mul_f32 v[142:143], v[158:159], v[144:145] op_sel:[0,1] op_sel_hi:[1,0]
	s_nop 0
	v_add_f32_e32 v144, v142, v143
	v_pk_mul_f32 v[142:143], v[164:165], v[138:139]
	v_pk_mul_f32 v[138:139], v[164:165], v[138:139] op_sel:[0,1] op_sel_hi:[1,0]
	v_sub_f32_e32 v142, v142, v143
	v_add_f32_e32 v143, v138, v139
	v_pk_mul_f32 v[138:139], v[162:163], v[140:141]
	s_nop 0
	v_sub_f32_e32 v145, v138, v139
	v_pk_mul_f32 v[138:139], v[162:163], v[140:141] op_sel:[0,1] op_sel_hi:[1,0]
	s_nop 0
	v_add_f32_e32 v141, v138, v139
	v_cvt_pk_bf16_f32 v138, v135, v160
	v_or_b32_e32 v135, 48, v189
	v_cvt_pk_bf16_f32 v139, v161, v144
	v_cvt_pk_bf16_f32 v140, v142, v143
	v_cvt_pk_bf16_f32 v141, v145, v141
	global_store_dwordx4 v[136:137], v[138:141], off offset:256 nt
	v_cmp_lt_i32_e32 vcc, s3, v135
	v_mad_i64_i32 v[136:137], s[24:25], v135, s19, v[130:131]
	v_add_u32_e32 v138, 0xffffbf30, v189
	v_cndmask_b32_e32 v135, v135, v138, vcc
	v_add_u32_e32 v138, 0xffffff00, v135
	v_cmp_lt_i32_e32 vcc, s17, v135
	v_lshrrev_b32_e32 v138, 6, v138
	v_and_b32_e32 v135, 63, v135
	v_cndmask_b32_e64 v135, v135, v138, s[4:5]
	v_lshlrev_b32_e32 v135, 6, v135
	v_cndmask_b32_e32 v135, 0, v135, vcc
	v_or_b32_e32 v138, v135, v187
	v_mov_b32_e32 v139, v65
	v_lshl_add_u64 v[142:143], v[138:139], 2, s[12:13]
	global_load_dwordx4 v[138:141], v[142:143], off offset:16
	s_nop 0
	global_load_dwordx4 v[142:145], v[142:143], off
	v_pk_mul_f32 v[160:161], v[134:135], v[86:87] op_sel_hi:[0,1]
	v_pk_mul_f32 v[158:159], v[134:135], v[88:89] op_sel_hi:[0,1]
	v_pk_mul_f32 v[162:163], v[134:135], v[80:81] op_sel_hi:[0,1]
	v_pk_mul_f32 v[164:165], v[134:135], v[78:79] op_sel_hi:[0,1]
	v_lshl_add_u64 v[136:137], v[136:137], 0, v[132:133]
	s_movk_i32 s3, 0x407f
	v_cmp_lt_i32_e32 vcc, s3, v189
	s_movk_i32 s3, 0x406f
	s_waitcnt vmcnt(0)
	v_pk_mul_f32 v[166:167], v[160:161], v[142:143]
	v_pk_mul_f32 v[160:161], v[160:161], v[142:143] op_sel:[0,1] op_sel_hi:[1,0]
	v_sub_f32_e32 v135, v166, v167
	v_add_f32_e32 v166, v160, v161
	v_pk_mul_f32 v[160:161], v[158:159], v[144:145]
	v_pk_mul_f32 v[158:159], v[158:159], v[144:145] op_sel:[0,1] op_sel_hi:[1,0]
	v_sub_f32_e32 v160, v160, v161
	v_add_f32_e32 v161, v158, v159
	v_pk_mul_f32 v[158:159], v[164:165], v[138:139]
	s_nop 0
	v_sub_f32_e32 v167, v158, v159
	v_pk_mul_f32 v[158:159], v[164:165], v[138:139] op_sel:[0,1] op_sel_hi:[1,0]
	s_nop 0
	v_add_f32_e32 v164, v158, v159
	v_pk_mul_f32 v[158:159], v[162:163], v[140:141]
	s_nop 0
	v_sub_f32_e32 v165, v158, v159
	v_pk_mul_f32 v[158:159], v[162:163], v[140:141] op_sel:[0,1] op_sel_hi:[1,0]
	s_nop 0
	v_add_f32_e32 v162, v158, v159
	v_cvt_pk_bf16_f32 v158, v135, v166
	v_cvt_pk_bf16_f32 v159, v160, v161
	v_cvt_pk_bf16_f32 v160, v167, v164
	v_cvt_pk_bf16_f32 v161, v165, v162
	global_store_dwordx4 v[136:137], v[158:161], off nt
	v_pk_mul_f32 v[164:165], v[134:135], v[66:67] op_sel_hi:[0,1]
	v_pk_mul_f32 v[162:163], v[134:135], v[68:69] op_sel_hi:[0,1]
	v_pk_mul_f32 v[160:161], v[134:135], v[70:71] op_sel_hi:[0,1]
	v_pk_mul_f32 v[158:159], v[134:135], v[72:73] op_sel_hi:[0,1]
	v_pk_mul_f32 v[166:167], v[160:161], v[142:143]
	v_pk_mul_f32 v[142:143], v[160:161], v[142:143] op_sel:[0,1] op_sel_hi:[1,0]
	v_sub_f32_e32 v135, v166, v167
	v_add_f32_e32 v160, v142, v143
	v_pk_mul_f32 v[142:143], v[158:159], v[144:145]
	s_nop 0
	v_sub_f32_e32 v161, v142, v143
	v_pk_mul_f32 v[142:143], v[158:159], v[144:145] op_sel:[0,1] op_sel_hi:[1,0]
	s_nop 0
	v_add_f32_e32 v144, v142, v143
	v_pk_mul_f32 v[142:143], v[164:165], v[138:139]
	v_pk_mul_f32 v[138:139], v[164:165], v[138:139] op_sel:[0,1] op_sel_hi:[1,0]
	v_sub_f32_e32 v142, v142, v143
	v_add_f32_e32 v143, v138, v139
	v_pk_mul_f32 v[138:139], v[162:163], v[140:141]
	s_nop 0
	v_sub_f32_e32 v145, v138, v139
	v_pk_mul_f32 v[138:139], v[162:163], v[140:141] op_sel:[0,1] op_sel_hi:[1,0]
	s_nop 0
	v_add_f32_e32 v141, v138, v139
	v_cvt_pk_bf16_f32 v138, v135, v160
	v_cvt_pk_bf16_f32 v139, v161, v144
	v_cvt_pk_bf16_f32 v140, v142, v143
	v_cvt_pk_bf16_f32 v141, v145, v141
	global_store_dwordx4 v[136:137], v[138:141], off offset:256 nt
	v_add_u32_e32 v135, 0x80, v189
	v_mad_i64_i32 v[136:137], s[24:25], v135, s19, v[130:131]
	v_add_u32_e32 v138, 0xffffbf80, v189
	v_cndmask_b32_e32 v135, v135, v138, vcc
	v_add_u32_e32 v138, 0xffffff00, v135
	v_cmp_lt_i32_e32 vcc, s17, v135
	v_lshrrev_b32_e32 v138, 6, v138
	v_and_b32_e32 v135, 15, v135
	v_cndmask_b32_e64 v135, v135, v138, s[4:5]
	v_lshlrev_b32_e32 v135, 6, v135
	v_cndmask_b32_e32 v135, 0, v135, vcc
	v_or_b32_e32 v138, v135, v187
	v_mov_b32_e32 v139, v65
	v_lshl_add_u64 v[142:143], v[138:139], 2, s[12:13]
	global_load_dwordx4 v[138:141], v[142:143], off offset:16
	s_nop 0
	global_load_dwordx4 v[142:145], v[142:143], off
	v_pk_mul_f32 v[160:161], v[134:135], v[60:61] op_sel_hi:[0,1]
	v_pk_mul_f32 v[158:159], v[134:135], v[62:63] op_sel_hi:[0,1]
	v_pk_mul_f32 v[162:163], v[134:135], v[58:59] op_sel_hi:[0,1]
	v_pk_mul_f32 v[164:165], v[134:135], v[56:57] op_sel_hi:[0,1]
	v_lshl_add_u64 v[136:137], v[136:137], 0, v[132:133]
	v_cmp_lt_i32_e32 vcc, s3, v189
	s_movk_i32 s3, 0x405f
	s_waitcnt vmcnt(0)
	v_pk_mul_f32 v[166:167], v[160:161], v[142:143]
	v_pk_mul_f32 v[160:161], v[160:161], v[142:143] op_sel:[0,1] op_sel_hi:[1,0]
	v_sub_f32_e32 v135, v166, v167
	v_add_f32_e32 v166, v160, v161
	v_pk_mul_f32 v[160:161], v[158:159], v[144:145]
	v_pk_mul_f32 v[158:159], v[158:159], v[144:145] op_sel:[0,1] op_sel_hi:[1,0]
	v_sub_f32_e32 v160, v160, v161
	v_add_f32_e32 v161, v158, v159
	v_pk_mul_f32 v[158:159], v[164:165], v[138:139]
	s_nop 0
	v_sub_f32_e32 v167, v158, v159
	v_pk_mul_f32 v[158:159], v[164:165], v[138:139] op_sel:[0,1] op_sel_hi:[1,0]
	s_nop 0
	v_add_f32_e32 v164, v158, v159
	v_pk_mul_f32 v[158:159], v[162:163], v[140:141]
	s_nop 0
	v_sub_f32_e32 v165, v158, v159
	v_pk_mul_f32 v[158:159], v[162:163], v[140:141] op_sel:[0,1] op_sel_hi:[1,0]
	s_nop 0
	v_add_f32_e32 v162, v158, v159
	v_cvt_pk_bf16_f32 v158, v135, v166
	v_cvt_pk_bf16_f32 v159, v160, v161
	v_cvt_pk_bf16_f32 v160, v167, v164
	v_cvt_pk_bf16_f32 v161, v165, v162
	global_store_dwordx4 v[136:137], v[158:161], off nt
	v_pk_mul_f32 v[164:165], v[134:135], v[40:41] op_sel_hi:[0,1]
	v_pk_mul_f32 v[162:163], v[134:135], v[42:43] op_sel_hi:[0,1]
	v_pk_mul_f32 v[160:161], v[134:135], v[48:49] op_sel_hi:[0,1]
	v_pk_mul_f32 v[158:159], v[134:135], v[50:51] op_sel_hi:[0,1]
	v_pk_mul_f32 v[166:167], v[160:161], v[142:143]
	v_pk_mul_f32 v[142:143], v[160:161], v[142:143] op_sel:[0,1] op_sel_hi:[1,0]
	v_sub_f32_e32 v135, v166, v167
	v_add_f32_e32 v160, v142, v143
	v_pk_mul_f32 v[142:143], v[158:159], v[144:145]
	s_nop 0
	v_sub_f32_e32 v161, v142, v143
	v_pk_mul_f32 v[142:143], v[158:159], v[144:145] op_sel:[0,1] op_sel_hi:[1,0]
	s_nop 0
	v_add_f32_e32 v144, v142, v143
	v_pk_mul_f32 v[142:143], v[164:165], v[138:139]
	v_pk_mul_f32 v[138:139], v[164:165], v[138:139] op_sel:[0,1] op_sel_hi:[1,0]
	v_sub_f32_e32 v142, v142, v143
	v_add_f32_e32 v143, v138, v139
	v_pk_mul_f32 v[138:139], v[162:163], v[140:141]
	s_nop 0
	v_sub_f32_e32 v145, v138, v139
	v_pk_mul_f32 v[138:139], v[162:163], v[140:141] op_sel:[0,1] op_sel_hi:[1,0]
	s_nop 0
	v_add_f32_e32 v141, v138, v139
	v_cvt_pk_bf16_f32 v138, v135, v160
	v_cvt_pk_bf16_f32 v139, v161, v144
	v_cvt_pk_bf16_f32 v140, v142, v143
	v_cvt_pk_bf16_f32 v141, v145, v141
	global_store_dwordx4 v[136:137], v[138:141], off offset:256 nt
	v_add_u32_e32 v135, 0x90, v189
	v_mad_i64_i32 v[136:137], s[24:25], v135, s19, v[130:131]
	v_add_u32_e32 v138, 0xffffbf90, v189
	v_cndmask_b32_e32 v135, v135, v138, vcc
	v_add_u32_e32 v138, 0xffffff00, v135
	v_cmp_lt_i32_e32 vcc, s17, v135
	v_lshrrev_b32_e32 v138, 6, v138
	v_and_b32_e32 v135, 31, v135
	v_cndmask_b32_e64 v135, v135, v138, s[4:5]
	v_lshlrev_b32_e32 v135, 6, v135
	v_cndmask_b32_e32 v135, 0, v135, vcc
	v_or_b32_e32 v138, v135, v187
	v_mov_b32_e32 v139, v65
	v_lshl_add_u64 v[142:143], v[138:139], 2, s[12:13]
	global_load_dwordx4 v[138:141], v[142:143], off offset:16
	s_nop 0
	global_load_dwordx4 v[142:145], v[142:143], off
	v_pk_mul_f32 v[160:161], v[134:135], v[52:53] op_sel_hi:[0,1]
	v_pk_mul_f32 v[158:159], v[134:135], v[54:55] op_sel_hi:[0,1]
	v_pk_mul_f32 v[162:163], v[134:135], v[46:47] op_sel_hi:[0,1]
	v_pk_mul_f32 v[164:165], v[134:135], v[44:45] op_sel_hi:[0,1]
	v_lshl_add_u64 v[136:137], v[136:137], 0, v[132:133]
	v_cmp_lt_i32_e32 vcc, s3, v189
	s_movk_i32 s3, 0x404f
	s_waitcnt vmcnt(0)
	v_pk_mul_f32 v[166:167], v[160:161], v[142:143]
	v_pk_mul_f32 v[160:161], v[160:161], v[142:143] op_sel:[0,1] op_sel_hi:[1,0]
	v_sub_f32_e32 v135, v166, v167
	v_add_f32_e32 v166, v160, v161
	v_pk_mul_f32 v[160:161], v[158:159], v[144:145]
	v_pk_mul_f32 v[158:159], v[158:159], v[144:145] op_sel:[0,1] op_sel_hi:[1,0]
	v_sub_f32_e32 v160, v160, v161
	v_add_f32_e32 v161, v158, v159
	v_pk_mul_f32 v[158:159], v[164:165], v[138:139]
	s_nop 0
	v_sub_f32_e32 v167, v158, v159
	v_pk_mul_f32 v[158:159], v[164:165], v[138:139] op_sel:[0,1] op_sel_hi:[1,0]
	s_nop 0
	v_add_f32_e32 v164, v158, v159
	v_pk_mul_f32 v[158:159], v[162:163], v[140:141]
	s_nop 0
	v_sub_f32_e32 v165, v158, v159
	v_pk_mul_f32 v[158:159], v[162:163], v[140:141] op_sel:[0,1] op_sel_hi:[1,0]
	s_nop 0
	v_add_f32_e32 v162, v158, v159
	v_cvt_pk_bf16_f32 v158, v135, v166
	v_cvt_pk_bf16_f32 v159, v160, v161
	v_cvt_pk_bf16_f32 v160, v167, v164
	v_cvt_pk_bf16_f32 v161, v165, v162
	global_store_dwordx4 v[136:137], v[158:161], off nt
	v_pk_mul_f32 v[164:165], v[134:135], v[24:25] op_sel_hi:[0,1]
	v_pk_mul_f32 v[162:163], v[134:135], v[26:27] op_sel_hi:[0,1]
	v_pk_mul_f32 v[160:161], v[134:135], v[32:33] op_sel_hi:[0,1]
	v_pk_mul_f32 v[158:159], v[134:135], v[34:35] op_sel_hi:[0,1]
	v_pk_mul_f32 v[166:167], v[160:161], v[142:143]
	v_pk_mul_f32 v[142:143], v[160:161], v[142:143] op_sel:[0,1] op_sel_hi:[1,0]
	v_sub_f32_e32 v135, v166, v167
	v_add_f32_e32 v160, v142, v143
	v_pk_mul_f32 v[142:143], v[158:159], v[144:145]
	s_nop 0
	v_sub_f32_e32 v161, v142, v143
	v_pk_mul_f32 v[142:143], v[158:159], v[144:145] op_sel:[0,1] op_sel_hi:[1,0]
	s_nop 0
	v_add_f32_e32 v144, v142, v143
	v_pk_mul_f32 v[142:143], v[164:165], v[138:139]
	v_pk_mul_f32 v[138:139], v[164:165], v[138:139] op_sel:[0,1] op_sel_hi:[1,0]
	v_sub_f32_e32 v142, v142, v143
	v_add_f32_e32 v143, v138, v139
	v_pk_mul_f32 v[138:139], v[162:163], v[140:141]
	s_nop 0
	v_sub_f32_e32 v145, v138, v139
	v_pk_mul_f32 v[138:139], v[162:163], v[140:141] op_sel:[0,1] op_sel_hi:[1,0]
	s_nop 0
	v_add_f32_e32 v141, v138, v139
	v_cvt_pk_bf16_f32 v138, v135, v160
	v_cvt_pk_bf16_f32 v139, v161, v144
	v_cvt_pk_bf16_f32 v140, v142, v143
	v_cvt_pk_bf16_f32 v141, v145, v141
	global_store_dwordx4 v[136:137], v[138:141], off offset:256 nt
	v_add_u32_e32 v135, 0xa0, v189
	v_mad_i64_i32 v[136:137], s[24:25], v135, s19, v[130:131]
	v_add_u32_e32 v138, 0xffffbfa0, v189
	v_cndmask_b32_e32 v135, v135, v138, vcc
	v_add_u32_e32 v138, 0xffffff00, v135
	v_cmp_lt_i32_e32 vcc, s17, v135
	v_lshrrev_b32_e32 v138, 6, v138
	v_and_b32_e32 v135, 47, v135
	v_cndmask_b32_e64 v135, v135, v138, s[4:5]
	v_lshlrev_b32_e32 v135, 6, v135
	v_cndmask_b32_e32 v135, 0, v135, vcc
	v_or_b32_e32 v138, v135, v187
	v_mov_b32_e32 v139, v65
	v_lshl_add_u64 v[142:143], v[138:139], 2, s[12:13]
	global_load_dwordx4 v[138:141], v[142:143], off offset:16
	s_nop 0
	global_load_dwordx4 v[142:145], v[142:143], off
	v_pk_mul_f32 v[160:161], v[134:135], v[36:37] op_sel_hi:[0,1]
	v_pk_mul_f32 v[158:159], v[134:135], v[38:39] op_sel_hi:[0,1]
	v_pk_mul_f32 v[162:163], v[134:135], v[30:31] op_sel_hi:[0,1]
	v_pk_mul_f32 v[164:165], v[134:135], v[28:29] op_sel_hi:[0,1]
	v_lshl_add_u64 v[136:137], v[136:137], 0, v[132:133]
	v_cmp_lt_i32_e32 vcc, s3, v189
	s_waitcnt vmcnt(0)
	v_pk_mul_f32 v[166:167], v[160:161], v[142:143]
	v_pk_mul_f32 v[160:161], v[160:161], v[142:143] op_sel:[0,1] op_sel_hi:[1,0]
	v_sub_f32_e32 v135, v166, v167
	v_add_f32_e32 v166, v160, v161
	v_pk_mul_f32 v[160:161], v[158:159], v[144:145]
	v_pk_mul_f32 v[158:159], v[158:159], v[144:145] op_sel:[0,1] op_sel_hi:[1,0]
	v_sub_f32_e32 v160, v160, v161
	v_add_f32_e32 v161, v158, v159
	v_pk_mul_f32 v[158:159], v[164:165], v[138:139]
	s_nop 0
	v_sub_f32_e32 v167, v158, v159
	v_pk_mul_f32 v[158:159], v[164:165], v[138:139] op_sel:[0,1] op_sel_hi:[1,0]
	s_nop 0
	v_add_f32_e32 v164, v158, v159
	v_pk_mul_f32 v[158:159], v[162:163], v[140:141]
	s_nop 0
	v_sub_f32_e32 v165, v158, v159
	v_pk_mul_f32 v[158:159], v[162:163], v[140:141] op_sel:[0,1] op_sel_hi:[1,0]
	s_nop 0
	v_add_f32_e32 v162, v158, v159
	v_cvt_pk_bf16_f32 v158, v135, v166
	v_cvt_pk_bf16_f32 v159, v160, v161
	v_cvt_pk_bf16_f32 v160, v167, v164
	v_cvt_pk_bf16_f32 v161, v165, v162
	global_store_dwordx4 v[136:137], v[158:161], off nt
	v_pk_mul_f32 v[164:165], v[134:135], v[8:9] op_sel_hi:[0,1]
	v_pk_mul_f32 v[162:163], v[134:135], v[10:11] op_sel_hi:[0,1]
	v_pk_mul_f32 v[160:161], v[134:135], v[16:17] op_sel_hi:[0,1]
	v_pk_mul_f32 v[158:159], v[134:135], v[18:19] op_sel_hi:[0,1]
	v_pk_mul_f32 v[166:167], v[160:161], v[142:143]
	v_pk_mul_f32 v[142:143], v[160:161], v[142:143] op_sel:[0,1] op_sel_hi:[1,0]
	v_sub_f32_e32 v135, v166, v167
	v_add_f32_e32 v160, v142, v143
	v_pk_mul_f32 v[142:143], v[158:159], v[144:145]
	s_nop 0
	v_sub_f32_e32 v161, v142, v143
	v_pk_mul_f32 v[142:143], v[158:159], v[144:145] op_sel:[0,1] op_sel_hi:[1,0]
	s_nop 0
	v_add_f32_e32 v144, v142, v143
	v_pk_mul_f32 v[142:143], v[164:165], v[138:139]
	v_pk_mul_f32 v[138:139], v[164:165], v[138:139] op_sel:[0,1] op_sel_hi:[1,0]
	v_sub_f32_e32 v142, v142, v143
	v_add_f32_e32 v143, v138, v139
	v_pk_mul_f32 v[138:139], v[162:163], v[140:141]
	s_nop 0
	v_sub_f32_e32 v145, v138, v139
	v_pk_mul_f32 v[138:139], v[162:163], v[140:141] op_sel:[0,1] op_sel_hi:[1,0]
	s_nop 0
	v_add_f32_e32 v141, v138, v139
	v_cvt_pk_bf16_f32 v138, v135, v160
	v_add_u32_e32 v135, 0xb0, v189
	v_mad_i64_i32 v[130:131], s[24:25], v135, s19, v[130:131]
	v_lshl_add_u64 v[162:163], v[130:131], 0, v[132:133]
	v_add_u32_e32 v130, 0xffffbfb0, v189
	v_cndmask_b32_e32 v130, v135, v130, vcc
	v_add_u32_e32 v131, 0xffffff00, v130
	v_cmp_lt_i32_e32 vcc, s17, v130
	v_lshrrev_b32_e32 v131, 6, v131
	v_and_b32_e32 v130, 63, v130
	v_cndmask_b32_e64 v130, v130, v131, s[4:5]
	v_lshlrev_b32_e32 v130, 6, v130
	v_cndmask_b32_e32 v130, 0, v130, vcc
	v_or_b32_e32 v130, v130, v187
	v_mov_b32_e32 v131, v65
	v_cvt_pk_bf16_f32 v139, v161, v144
	v_cvt_pk_bf16_f32 v140, v142, v143
	v_cvt_pk_bf16_f32 v141, v145, v141
	global_store_dwordx4 v[136:137], v[138:141], off offset:256 nt
	v_lshl_add_u64 v[136:137], v[130:131], 2, s[12:13]
	global_load_dwordx4 v[130:133], v[136:137], off offset:16
	s_nop 0
	global_load_dwordx4 v[136:139], v[136:137], off
	v_pk_mul_f32 v[142:143], v[134:135], v[20:21] op_sel_hi:[0,1]
	v_pk_mul_f32 v[140:141], v[134:135], v[22:23] op_sel_hi:[0,1]
	v_pk_mul_f32 v[144:145], v[134:135], v[14:15] op_sel_hi:[0,1]
	v_pk_mul_f32 v[158:159], v[134:135], v[12:13] op_sel_hi:[0,1]
	s_waitcnt vmcnt(0)
	v_pk_mul_f32 v[160:161], v[142:143], v[136:137]
	v_pk_mul_f32 v[142:143], v[142:143], v[136:137] op_sel:[0,1] op_sel_hi:[1,0]
	v_sub_f32_e32 v135, v160, v161
	v_add_f32_e32 v160, v142, v143
	v_pk_mul_f32 v[142:143], v[140:141], v[138:139]
	v_pk_mul_f32 v[140:141], v[140:141], v[138:139] op_sel:[0,1] op_sel_hi:[1,0]
	v_sub_f32_e32 v142, v142, v143
	v_add_f32_e32 v143, v140, v141
	v_pk_mul_f32 v[140:141], v[158:159], v[130:131]
	s_nop 0
	v_sub_f32_e32 v161, v140, v141
	v_pk_mul_f32 v[140:141], v[158:159], v[130:131] op_sel:[0,1] op_sel_hi:[1,0]
	s_nop 0
	v_add_f32_e32 v158, v140, v141
	v_pk_mul_f32 v[140:141], v[144:145], v[132:133]
	s_nop 0
	v_sub_f32_e32 v159, v140, v141
	v_pk_mul_f32 v[140:141], v[144:145], v[132:133] op_sel:[0,1] op_sel_hi:[1,0]
	s_nop 0
	v_add_f32_e32 v144, v140, v141
	v_cvt_pk_bf16_f32 v140, v135, v160
	v_cvt_pk_bf16_f32 v141, v142, v143
	v_cvt_pk_bf16_f32 v142, v161, v158
	v_cvt_pk_bf16_f32 v143, v159, v144
	global_store_dwordx4 v[162:163], v[140:143], off nt
	v_pk_mul_f32 v[144:145], v[134:135], v[2:3] op_sel_hi:[0,1]
	s_nop 0
	v_pk_mul_f32 v[142:143], v[134:135], v[4:5] op_sel_hi:[0,1]
	v_pk_mul_f32 v[140:141], v[134:135], v[6:7] op_sel_hi:[0,1]
	v_pk_mul_f32 v[158:159], v[142:143], v[136:137]
	v_pk_mul_f32 v[136:137], v[142:143], v[136:137] op_sel:[0,1] op_sel_hi:[1,0]
	v_pk_mul_f32 v[134:135], v[134:135], v[0:1] op_sel_hi:[0,1]
	v_add_f32_e32 v142, v136, v137
	v_pk_mul_f32 v[136:137], v[140:141], v[138:139]
	v_sub_f32_e32 v158, v158, v159
	v_sub_f32_e32 v143, v136, v137
	v_pk_mul_f32 v[136:137], v[140:141], v[138:139] op_sel:[0,1] op_sel_hi:[1,0]
	s_nop 0
	v_add_f32_e32 v138, v136, v137
	v_pk_mul_f32 v[136:137], v[134:135], v[130:131]
	v_pk_mul_f32 v[130:131], v[134:135], v[130:131] op_sel:[0,1] op_sel_hi:[1,0]
	v_sub_f32_e32 v136, v136, v137
	v_add_f32_e32 v134, v130, v131
	v_pk_mul_f32 v[130:131], v[144:145], v[132:133]
	s_nop 0
	v_sub_f32_e32 v135, v130, v131
	v_pk_mul_f32 v[130:131], v[144:145], v[132:133] op_sel:[0,1] op_sel_hi:[1,0]
	s_nop 0
	v_add_f32_e32 v133, v130, v131
	v_cvt_pk_bf16_f32 v130, v158, v142
	v_cvt_pk_bf16_f32 v131, v143, v138
	v_cvt_pk_bf16_f32 v132, v136, v134
	v_cvt_pk_bf16_f32 v133, v135, v133
	s_cbranch_execz .LBB0_324
	s_branch .LBB0_325
.Lg1rope_fast:
	s_cmp_eq_u32 s2, 6
	s_cselect_b64 vcc, -1, 0
	s_movk_i32 s3, 0x40ff
	v_cndmask_b32_e32 v134, 1.0, v202, vcc
	v_ashrrev_i32_e32 v139, 31, v64
	v_mov_b32_e32 v138, v64
	v_mov_b64_e32 v[136:137], s[8:9]
	s_movk_i32 s19, 0x2400
	s_movk_i32 s17, 0xff
	v_lshlrev_b64 v[138:139], 1, v[138:139]
	v_mov_b32_e32 v158, v189
	v_cmp_lt_i32_e32 vcc, s3, v158
	v_add_u32_e32 v159, 0xffffbf00, v158
	s_nop 1
	v_cndmask_b32_e32 v158, v158, v159, vcc
	v_add_u32_e32 v159, 0xffffff00, v158
	v_cmp_lt_i32_e32 vcc, s17, v158
	v_lshrrev_b32_e32 v159, 6, v159
	v_and_b32_e32 v158, 63, v158
	v_cndmask_b32_e64 v158, v158, v159, s[4:5]
	v_lshlrev_b32_e32 v158, 6, v158
	v_cndmask_b32_e32 v158, 0, v158, vcc
	v_or_b32_e32 v158, v158, v187
	v_mov_b32_e32 v159, v65
	v_lshl_add_u64 v[160:161], v[158:159], 2, s[12:13]
	global_load_dwordx4 v[216:219], v[160:161], off offset:16
	global_load_dwordx4 v[212:215], v[160:161], off
	v_add_u32_e32 v158, 16, v189
	v_cmp_lt_i32_e32 vcc, s3, v158
	v_add_u32_e32 v159, 0xffffbf00, v158
	s_nop 1
	v_cndmask_b32_e32 v158, v158, v159, vcc
	v_add_u32_e32 v159, 0xffffff00, v158
	v_cmp_lt_i32_e32 vcc, s17, v158
	v_lshrrev_b32_e32 v159, 6, v159
	v_and_b32_e32 v158, 63, v158
	v_cndmask_b32_e64 v158, v158, v159, s[4:5]
	v_lshlrev_b32_e32 v158, 6, v158
	v_cndmask_b32_e32 v158, 0, v158, vcc
	v_or_b32_e32 v158, v158, v187
	v_mov_b32_e32 v159, v65
	v_lshl_add_u64 v[160:161], v[158:159], 2, s[12:13]
	global_load_dwordx4 v[224:227], v[160:161], off offset:16
	global_load_dwordx4 v[220:223], v[160:161], off
	v_add_u32_e32 v158, 32, v189
	v_cmp_lt_i32_e32 vcc, s3, v158
	v_add_u32_e32 v159, 0xffffbf00, v158
	s_nop 1
	v_cndmask_b32_e32 v158, v158, v159, vcc
	v_add_u32_e32 v159, 0xffffff00, v158
	v_cmp_lt_i32_e32 vcc, s17, v158
	v_lshrrev_b32_e32 v159, 6, v159
	v_and_b32_e32 v158, 63, v158
	v_cndmask_b32_e64 v158, v158, v159, s[4:5]
	v_lshlrev_b32_e32 v158, 6, v158
	v_cndmask_b32_e32 v158, 0, v158, vcc
	v_or_b32_e32 v158, v158, v187
	v_mov_b32_e32 v159, v65
	v_lshl_add_u64 v[160:161], v[158:159], 2, s[12:13]
	global_load_dwordx4 v[232:235], v[160:161], off offset:16
	global_load_dwordx4 v[228:231], v[160:161], off
	v_add_u32_e32 v158, 48, v189
	v_cmp_lt_i32_e32 vcc, s3, v158
	v_add_u32_e32 v159, 0xffffbf00, v158
	s_nop 1
	v_cndmask_b32_e32 v158, v158, v159, vcc
	v_add_u32_e32 v159, 0xffffff00, v158
	v_cmp_lt_i32_e32 vcc, s17, v158
	v_lshrrev_b32_e32 v159, 6, v159
	v_and_b32_e32 v158, 63, v158
	v_cndmask_b32_e64 v158, v158, v159, s[4:5]
	v_lshlrev_b32_e32 v158, 6, v158
	v_cndmask_b32_e32 v158, 0, v158, vcc
	v_or_b32_e32 v158, v158, v187
	v_mov_b32_e32 v159, v65
	v_lshl_add_u64 v[160:161], v[158:159], 2, s[12:13]
	global_load_dwordx4 v[180:183], v[160:161], off offset:16
	global_load_dwordx4 v[176:179], v[160:161], off
	s_waitcnt vmcnt(6)
	v_mov_b32_e32 v158, v189
	v_mad_i64_i32 v[236:237], s[24:25], v158, s19, v[136:137]
	v_lshl_add_u64 v[236:237], v[236:237], 0, v[138:139]
	v_pk_mul_f32 v[164:165], v[134:135], v[126:127] op_sel_hi:[0,1]
	v_pk_mul_f32 v[166:167], v[134:135], v[128:129] op_sel_hi:[0,1]
	v_pk_mul_f32 v[168:169], v[134:135], v[122:123] op_sel_hi:[0,1]
	v_pk_mul_f32 v[170:171], v[134:135], v[124:125] op_sel_hi:[0,1]
	v_pk_mul_f32 v[172:173], v[164:165], v[212:213]
	v_pk_mul_f32 v[174:175], v[164:165], v[212:213] op_sel:[0,1] op_sel_hi:[1,0]
	v_sub_f32_e32 v140, v172, v173
	v_add_f32_e32 v141, v174, v175
	v_pk_mul_f32 v[172:173], v[166:167], v[214:215]
	v_pk_mul_f32 v[174:175], v[166:167], v[214:215] op_sel:[0,1] op_sel_hi:[1,0]
	v_sub_f32_e32 v142, v172, v173
	v_add_f32_e32 v143, v174, v175
	v_pk_mul_f32 v[172:173], v[168:169], v[216:217]
	v_pk_mul_f32 v[174:175], v[168:169], v[216:217] op_sel:[0,1] op_sel_hi:[1,0]
	v_sub_f32_e32 v144, v172, v173
	v_add_f32_e32 v145, v174, v175
	v_pk_mul_f32 v[172:173], v[170:171], v[218:219]
	v_pk_mul_f32 v[174:175], v[170:171], v[218:219] op_sel:[0,1] op_sel_hi:[1,0]
	v_sub_f32_e32 v190, v172, v173
	v_add_f32_e32 v191, v174, v175
	v_cvt_pk_bf16_f32 v192, v140, v141
	v_cvt_pk_bf16_f32 v193, v142, v143
	v_cvt_pk_bf16_f32 v194, v144, v145
	v_cvt_pk_bf16_f32 v195, v190, v191
	global_store_dwordx4 v[236:237], v[192:195], off nt
	s_nop 1
	v_pk_mul_f32 v[164:165], v[134:135], v[114:115] op_sel_hi:[0,1]
	v_pk_mul_f32 v[166:167], v[134:135], v[116:117] op_sel_hi:[0,1]
	v_pk_mul_f32 v[168:169], v[134:135], v[106:107] op_sel_hi:[0,1]
	v_pk_mul_f32 v[170:171], v[134:135], v[108:109] op_sel_hi:[0,1]
	v_pk_mul_f32 v[172:173], v[164:165], v[212:213]
	v_pk_mul_f32 v[174:175], v[164:165], v[212:213] op_sel:[0,1] op_sel_hi:[1,0]
	v_sub_f32_e32 v140, v172, v173
	v_add_f32_e32 v141, v174, v175
	v_pk_mul_f32 v[172:173], v[166:167], v[214:215]
	v_pk_mul_f32 v[174:175], v[166:167], v[214:215] op_sel:[0,1] op_sel_hi:[1,0]
	v_sub_f32_e32 v142, v172, v173
	v_add_f32_e32 v143, v174, v175
	v_pk_mul_f32 v[172:173], v[168:169], v[216:217]
	v_pk_mul_f32 v[174:175], v[168:169], v[216:217] op_sel:[0,1] op_sel_hi:[1,0]
	v_sub_f32_e32 v144, v172, v173
	v_add_f32_e32 v145, v174, v175
	v_pk_mul_f32 v[172:173], v[170:171], v[218:219]
	v_pk_mul_f32 v[174:175], v[170:171], v[218:219] op_sel:[0,1] op_sel_hi:[1,0]
	v_sub_f32_e32 v190, v172, v173
	v_add_f32_e32 v191, v174, v175
	v_cvt_pk_bf16_f32 v192, v140, v141
	v_cvt_pk_bf16_f32 v193, v142, v143
	v_cvt_pk_bf16_f32 v194, v144, v145
	v_cvt_pk_bf16_f32 v195, v190, v191
	global_store_dwordx4 v[236:237], v[192:195], off offset:256 nt
	s_nop 1
	v_add_u32_e32 v158, 128, v189
	v_cmp_lt_i32_e32 vcc, s3, v158
	v_add_u32_e32 v159, 0xffffbf00, v158
	s_nop 1
	v_cndmask_b32_e32 v158, v158, v159, vcc
	v_add_u32_e32 v159, 0xffffff00, v158
	v_cmp_lt_i32_e32 vcc, s17, v158
	v_lshrrev_b32_e32 v159, 6, v159
	v_and_b32_e32 v158, 63, v158
	v_cndmask_b32_e64 v158, v158, v159, s[4:5]
	v_lshlrev_b32_e32 v158, 6, v158
	v_cndmask_b32_e32 v158, 0, v158, vcc
	v_or_b32_e32 v158, v158, v187
	v_mov_b32_e32 v159, v65
	v_lshl_add_u64 v[160:161], v[158:159], 2, s[12:13]
	global_load_dwordx4 v[216:219], v[160:161], off offset:16
	global_load_dwordx4 v[212:215], v[160:161], off
	s_waitcnt vmcnt(8)
	v_add_u32_e32 v158, 16, v189
	v_mad_i64_i32 v[236:237], s[24:25], v158, s19, v[136:137]
	v_lshl_add_u64 v[236:237], v[236:237], 0, v[138:139]
	v_pk_mul_f32 v[164:165], v[134:135], v[118:119] op_sel_hi:[0,1]
	v_pk_mul_f32 v[166:167], v[134:135], v[120:121] op_sel_hi:[0,1]
	v_pk_mul_f32 v[168:169], v[134:135], v[110:111] op_sel_hi:[0,1]
	v_pk_mul_f32 v[170:171], v[134:135], v[112:113] op_sel_hi:[0,1]
	v_pk_mul_f32 v[172:173], v[164:165], v[220:221]
	v_pk_mul_f32 v[174:175], v[164:165], v[220:221] op_sel:[0,1] op_sel_hi:[1,0]
	v_sub_f32_e32 v140, v172, v173
	v_add_f32_e32 v141, v174, v175
	v_pk_mul_f32 v[172:173], v[166:167], v[222:223]
	v_pk_mul_f32 v[174:175], v[166:167], v[222:223] op_sel:[0,1] op_sel_hi:[1,0]
	v_sub_f32_e32 v142, v172, v173
	v_add_f32_e32 v143, v174, v175
	v_pk_mul_f32 v[172:173], v[168:169], v[224:225]
	v_pk_mul_f32 v[174:175], v[168:169], v[224:225] op_sel:[0,1] op_sel_hi:[1,0]
	v_sub_f32_e32 v144, v172, v173
	v_add_f32_e32 v145, v174, v175
	v_pk_mul_f32 v[172:173], v[170:171], v[226:227]
	v_pk_mul_f32 v[174:175], v[170:171], v[226:227] op_sel:[0,1] op_sel_hi:[1,0]
	v_sub_f32_e32 v190, v172, v173
	v_add_f32_e32 v191, v174, v175
	v_cvt_pk_bf16_f32 v192, v140, v141
	v_cvt_pk_bf16_f32 v193, v142, v143
	v_cvt_pk_bf16_f32 v194, v144, v145
	v_cvt_pk_bf16_f32 v195, v190, v191
	global_store_dwordx4 v[236:237], v[192:195], off nt
	s_nop 1
	v_pk_mul_f32 v[164:165], v[134:135], v[98:99] op_sel_hi:[0,1]
	v_pk_mul_f32 v[166:167], v[134:135], v[100:101] op_sel_hi:[0,1]
	v_pk_mul_f32 v[168:169], v[134:135], v[90:91] op_sel_hi:[0,1]
	v_pk_mul_f32 v[170:171], v[134:135], v[92:93] op_sel_hi:[0,1]
	v_pk_mul_f32 v[172:173], v[164:165], v[220:221]
	v_pk_mul_f32 v[174:175], v[164:165], v[220:221] op_sel:[0,1] op_sel_hi:[1,0]
	v_sub_f32_e32 v140, v172, v173
	v_add_f32_e32 v141, v174, v175
	v_pk_mul_f32 v[172:173], v[166:167], v[222:223]
	v_pk_mul_f32 v[174:175], v[166:167], v[222:223] op_sel:[0,1] op_sel_hi:[1,0]
	v_sub_f32_e32 v142, v172, v173
	v_add_f32_e32 v143, v174, v175
	v_pk_mul_f32 v[172:173], v[168:169], v[224:225]
	v_pk_mul_f32 v[174:175], v[168:169], v[224:225] op_sel:[0,1] op_sel_hi:[1,0]
	v_sub_f32_e32 v144, v172, v173
	v_add_f32_e32 v145, v174, v175
	v_pk_mul_f32 v[172:173], v[170:171], v[226:227]
	v_pk_mul_f32 v[174:175], v[170:171], v[226:227] op_sel:[0,1] op_sel_hi:[1,0]
	v_sub_f32_e32 v190, v172, v173
	v_add_f32_e32 v191, v174, v175
	v_cvt_pk_bf16_f32 v192, v140, v141
	v_cvt_pk_bf16_f32 v193, v142, v143
	v_cvt_pk_bf16_f32 v194, v144, v145
	v_cvt_pk_bf16_f32 v195, v190, v191
	global_store_dwordx4 v[236:237], v[192:195], off offset:256 nt
	s_nop 1
	v_add_u32_e32 v158, 144, v189
	v_cmp_lt_i32_e32 vcc, s3, v158
	v_add_u32_e32 v159, 0xffffbf00, v158
	s_nop 1
	v_cndmask_b32_e32 v158, v158, v159, vcc
	v_add_u32_e32 v159, 0xffffff00, v158
	v_cmp_lt_i32_e32 vcc, s17, v158
	v_lshrrev_b32_e32 v159, 6, v159
	v_and_b32_e32 v158, 63, v158
	v_cndmask_b32_e64 v158, v158, v159, s[4:5]
	v_lshlrev_b32_e32 v158, 6, v158
	v_cndmask_b32_e32 v158, 0, v158, vcc
	v_or_b32_e32 v158, v158, v187
	v_mov_b32_e32 v159, v65
	v_lshl_add_u64 v[160:161], v[158:159], 2, s[12:13]
	global_load_dwordx4 v[224:227], v[160:161], off offset:16
	global_load_dwordx4 v[220:223], v[160:161], off
	s_waitcnt vmcnt(10)
	v_add_u32_e32 v158, 32, v189
	v_mad_i64_i32 v[236:237], s[24:25], v158, s19, v[136:137]
	v_lshl_add_u64 v[236:237], v[236:237], 0, v[138:139]
	v_pk_mul_f32 v[164:165], v[134:135], v[102:103] op_sel_hi:[0,1]
	v_pk_mul_f32 v[166:167], v[134:135], v[104:105] op_sel_hi:[0,1]
	v_pk_mul_f32 v[168:169], v[134:135], v[94:95] op_sel_hi:[0,1]
	v_pk_mul_f32 v[170:171], v[134:135], v[96:97] op_sel_hi:[0,1]
	v_pk_mul_f32 v[172:173], v[164:165], v[228:229]
	v_pk_mul_f32 v[174:175], v[164:165], v[228:229] op_sel:[0,1] op_sel_hi:[1,0]
	v_sub_f32_e32 v140, v172, v173
	v_add_f32_e32 v141, v174, v175
	v_pk_mul_f32 v[172:173], v[166:167], v[230:231]
	v_pk_mul_f32 v[174:175], v[166:167], v[230:231] op_sel:[0,1] op_sel_hi:[1,0]
	v_sub_f32_e32 v142, v172, v173
	v_add_f32_e32 v143, v174, v175
	v_pk_mul_f32 v[172:173], v[168:169], v[232:233]
	v_pk_mul_f32 v[174:175], v[168:169], v[232:233] op_sel:[0,1] op_sel_hi:[1,0]
	v_sub_f32_e32 v144, v172, v173
	v_add_f32_e32 v145, v174, v175
	v_pk_mul_f32 v[172:173], v[170:171], v[234:235]
	v_pk_mul_f32 v[174:175], v[170:171], v[234:235] op_sel:[0,1] op_sel_hi:[1,0]
	v_sub_f32_e32 v190, v172, v173
	v_add_f32_e32 v191, v174, v175
	v_cvt_pk_bf16_f32 v192, v140, v141
	v_cvt_pk_bf16_f32 v193, v142, v143
	v_cvt_pk_bf16_f32 v194, v144, v145
	v_cvt_pk_bf16_f32 v195, v190, v191
	global_store_dwordx4 v[236:237], v[192:195], off nt
	s_nop 1
	v_pk_mul_f32 v[164:165], v[134:135], v[82:83] op_sel_hi:[0,1]
	v_pk_mul_f32 v[166:167], v[134:135], v[84:85] op_sel_hi:[0,1]
	v_pk_mul_f32 v[168:169], v[134:135], v[74:75] op_sel_hi:[0,1]
	v_pk_mul_f32 v[170:171], v[134:135], v[76:77] op_sel_hi:[0,1]
	v_pk_mul_f32 v[172:173], v[164:165], v[228:229]
	v_pk_mul_f32 v[174:175], v[164:165], v[228:229] op_sel:[0,1] op_sel_hi:[1,0]
	v_sub_f32_e32 v140, v172, v173
	v_add_f32_e32 v141, v174, v175
	v_pk_mul_f32 v[172:173], v[166:167], v[230:231]
	v_pk_mul_f32 v[174:175], v[166:167], v[230:231] op_sel:[0,1] op_sel_hi:[1,0]
	v_sub_f32_e32 v142, v172, v173
	v_add_f32_e32 v143, v174, v175
	v_pk_mul_f32 v[172:173], v[168:169], v[232:233]
	v_pk_mul_f32 v[174:175], v[168:169], v[232:233] op_sel:[0,1] op_sel_hi:[1,0]
	v_sub_f32_e32 v144, v172, v173
	v_add_f32_e32 v145, v174, v175
	v_pk_mul_f32 v[172:173], v[170:171], v[234:235]
	v_pk_mul_f32 v[174:175], v[170:171], v[234:235] op_sel:[0,1] op_sel_hi:[1,0]
	v_sub_f32_e32 v190, v172, v173
	v_add_f32_e32 v191, v174, v175
	v_cvt_pk_bf16_f32 v192, v140, v141
	v_cvt_pk_bf16_f32 v193, v142, v143
	v_cvt_pk_bf16_f32 v194, v144, v145
	v_cvt_pk_bf16_f32 v195, v190, v191
	global_store_dwordx4 v[236:237], v[192:195], off offset:256 nt
	s_nop 1
	v_add_u32_e32 v158, 160, v189
	v_cmp_lt_i32_e32 vcc, s3, v158
	v_add_u32_e32 v159, 0xffffbf00, v158
	s_nop 1
	v_cndmask_b32_e32 v158, v158, v159, vcc
	v_add_u32_e32 v159, 0xffffff00, v158
	v_cmp_lt_i32_e32 vcc, s17, v158
	v_lshrrev_b32_e32 v159, 6, v159
	v_and_b32_e32 v158, 63, v158
	v_cndmask_b32_e64 v158, v158, v159, s[4:5]
	v_lshlrev_b32_e32 v158, 6, v158
	v_cndmask_b32_e32 v158, 0, v158, vcc
	v_or_b32_e32 v158, v158, v187
	v_mov_b32_e32 v159, v65
	v_lshl_add_u64 v[160:161], v[158:159], 2, s[12:13]
	global_load_dwordx4 v[232:235], v[160:161], off offset:16
	global_load_dwordx4 v[228:231], v[160:161], off
	s_waitcnt vmcnt(12)
	v_add_u32_e32 v158, 48, v189
	v_mad_i64_i32 v[236:237], s[24:25], v158, s19, v[136:137]
	v_lshl_add_u64 v[236:237], v[236:237], 0, v[138:139]
	v_pk_mul_f32 v[164:165], v[134:135], v[86:87] op_sel_hi:[0,1]
	v_pk_mul_f32 v[166:167], v[134:135], v[88:89] op_sel_hi:[0,1]
	v_pk_mul_f32 v[168:169], v[134:135], v[78:79] op_sel_hi:[0,1]
	v_pk_mul_f32 v[170:171], v[134:135], v[80:81] op_sel_hi:[0,1]
	v_pk_mul_f32 v[172:173], v[164:165], v[176:177]
	v_pk_mul_f32 v[174:175], v[164:165], v[176:177] op_sel:[0,1] op_sel_hi:[1,0]
	v_sub_f32_e32 v140, v172, v173
	v_add_f32_e32 v141, v174, v175
	v_pk_mul_f32 v[172:173], v[166:167], v[178:179]
	v_pk_mul_f32 v[174:175], v[166:167], v[178:179] op_sel:[0,1] op_sel_hi:[1,0]
	v_sub_f32_e32 v142, v172, v173
	v_add_f32_e32 v143, v174, v175
	v_pk_mul_f32 v[172:173], v[168:169], v[180:181]
	v_pk_mul_f32 v[174:175], v[168:169], v[180:181] op_sel:[0,1] op_sel_hi:[1,0]
	v_sub_f32_e32 v144, v172, v173
	v_add_f32_e32 v145, v174, v175
	v_pk_mul_f32 v[172:173], v[170:171], v[182:183]
	v_pk_mul_f32 v[174:175], v[170:171], v[182:183] op_sel:[0,1] op_sel_hi:[1,0]
	v_sub_f32_e32 v190, v172, v173
	v_add_f32_e32 v191, v174, v175
	v_cvt_pk_bf16_f32 v192, v140, v141
	v_cvt_pk_bf16_f32 v193, v142, v143
	v_cvt_pk_bf16_f32 v194, v144, v145
	v_cvt_pk_bf16_f32 v195, v190, v191
	global_store_dwordx4 v[236:237], v[192:195], off nt
	s_nop 1
	v_pk_mul_f32 v[164:165], v[134:135], v[70:71] op_sel_hi:[0,1]
	v_pk_mul_f32 v[166:167], v[134:135], v[72:73] op_sel_hi:[0,1]
	v_pk_mul_f32 v[168:169], v[134:135], v[66:67] op_sel_hi:[0,1]
	v_pk_mul_f32 v[170:171], v[134:135], v[68:69] op_sel_hi:[0,1]
	v_pk_mul_f32 v[172:173], v[164:165], v[176:177]
	v_pk_mul_f32 v[174:175], v[164:165], v[176:177] op_sel:[0,1] op_sel_hi:[1,0]
	v_sub_f32_e32 v140, v172, v173
	v_add_f32_e32 v141, v174, v175
	v_pk_mul_f32 v[172:173], v[166:167], v[178:179]
	v_pk_mul_f32 v[174:175], v[166:167], v[178:179] op_sel:[0,1] op_sel_hi:[1,0]
	v_sub_f32_e32 v142, v172, v173
	v_add_f32_e32 v143, v174, v175
	v_pk_mul_f32 v[172:173], v[168:169], v[180:181]
	v_pk_mul_f32 v[174:175], v[168:169], v[180:181] op_sel:[0,1] op_sel_hi:[1,0]
	v_sub_f32_e32 v144, v172, v173
	v_add_f32_e32 v145, v174, v175
	v_pk_mul_f32 v[172:173], v[170:171], v[182:183]
	v_pk_mul_f32 v[174:175], v[170:171], v[182:183] op_sel:[0,1] op_sel_hi:[1,0]
	v_sub_f32_e32 v190, v172, v173
	v_add_f32_e32 v191, v174, v175
	v_cvt_pk_bf16_f32 v192, v140, v141
	v_cvt_pk_bf16_f32 v193, v142, v143
	v_cvt_pk_bf16_f32 v194, v144, v145
	v_cvt_pk_bf16_f32 v195, v190, v191
	global_store_dwordx4 v[236:237], v[192:195], off offset:256 nt
	s_nop 1
	v_add_u32_e32 v158, 176, v189
	v_cmp_lt_i32_e32 vcc, s3, v158
	v_add_u32_e32 v159, 0xffffbf00, v158
	s_nop 1
	v_cndmask_b32_e32 v158, v158, v159, vcc
	v_add_u32_e32 v159, 0xffffff00, v158
	v_cmp_lt_i32_e32 vcc, s17, v158
	v_lshrrev_b32_e32 v159, 6, v159
	v_and_b32_e32 v158, 63, v158
	v_cndmask_b32_e64 v158, v158, v159, s[4:5]
	v_lshlrev_b32_e32 v158, 6, v158
	v_cndmask_b32_e32 v158, 0, v158, vcc
	v_or_b32_e32 v158, v158, v187
	v_mov_b32_e32 v159, v65
	v_lshl_add_u64 v[160:161], v[158:159], 2, s[12:13]
	global_load_dwordx4 v[180:183], v[160:161], off offset:16
	global_load_dwordx4 v[176:179], v[160:161], off
	s_waitcnt vmcnt(12)
	v_add_u32_e32 v158, 128, v189
	v_mad_i64_i32 v[236:237], s[24:25], v158, s19, v[136:137]
	v_lshl_add_u64 v[236:237], v[236:237], 0, v[138:139]
	v_pk_mul_f32 v[164:165], v[134:135], v[60:61] op_sel_hi:[0,1]
	v_pk_mul_f32 v[166:167], v[134:135], v[62:63] op_sel_hi:[0,1]
	v_pk_mul_f32 v[168:169], v[134:135], v[56:57] op_sel_hi:[0,1]
	v_pk_mul_f32 v[170:171], v[134:135], v[58:59] op_sel_hi:[0,1]
	v_pk_mul_f32 v[172:173], v[164:165], v[212:213]
	v_pk_mul_f32 v[174:175], v[164:165], v[212:213] op_sel:[0,1] op_sel_hi:[1,0]
	v_sub_f32_e32 v140, v172, v173
	v_add_f32_e32 v141, v174, v175
	v_pk_mul_f32 v[172:173], v[166:167], v[214:215]
	v_pk_mul_f32 v[174:175], v[166:167], v[214:215] op_sel:[0,1] op_sel_hi:[1,0]
	v_sub_f32_e32 v142, v172, v173
	v_add_f32_e32 v143, v174, v175
	v_pk_mul_f32 v[172:173], v[168:169], v[216:217]
	v_pk_mul_f32 v[174:175], v[168:169], v[216:217] op_sel:[0,1] op_sel_hi:[1,0]
	v_sub_f32_e32 v144, v172, v173
	v_add_f32_e32 v145, v174, v175
	v_pk_mul_f32 v[172:173], v[170:171], v[218:219]
	v_pk_mul_f32 v[174:175], v[170:171], v[218:219] op_sel:[0,1] op_sel_hi:[1,0]
	v_sub_f32_e32 v190, v172, v173
	v_add_f32_e32 v191, v174, v175
	v_cvt_pk_bf16_f32 v192, v140, v141
	v_cvt_pk_bf16_f32 v193, v142, v143
	v_cvt_pk_bf16_f32 v194, v144, v145
	v_cvt_pk_bf16_f32 v195, v190, v191
	global_store_dwordx4 v[236:237], v[192:195], off nt
	s_nop 1
	v_pk_mul_f32 v[164:165], v[134:135], v[48:49] op_sel_hi:[0,1]
	v_pk_mul_f32 v[166:167], v[134:135], v[50:51] op_sel_hi:[0,1]
	v_pk_mul_f32 v[168:169], v[134:135], v[40:41] op_sel_hi:[0,1]
	v_pk_mul_f32 v[170:171], v[134:135], v[42:43] op_sel_hi:[0,1]
	v_pk_mul_f32 v[172:173], v[164:165], v[212:213]
	v_pk_mul_f32 v[174:175], v[164:165], v[212:213] op_sel:[0,1] op_sel_hi:[1,0]
	v_sub_f32_e32 v140, v172, v173
	v_add_f32_e32 v141, v174, v175
	v_pk_mul_f32 v[172:173], v[166:167], v[214:215]
	v_pk_mul_f32 v[174:175], v[166:167], v[214:215] op_sel:[0,1] op_sel_hi:[1,0]
	v_sub_f32_e32 v142, v172, v173
	v_add_f32_e32 v143, v174, v175
	v_pk_mul_f32 v[172:173], v[168:169], v[216:217]
	v_pk_mul_f32 v[174:175], v[168:169], v[216:217] op_sel:[0,1] op_sel_hi:[1,0]
	v_sub_f32_e32 v144, v172, v173
	v_add_f32_e32 v145, v174, v175
	v_pk_mul_f32 v[172:173], v[170:171], v[218:219]
	v_pk_mul_f32 v[174:175], v[170:171], v[218:219] op_sel:[0,1] op_sel_hi:[1,0]
	v_sub_f32_e32 v190, v172, v173
	v_add_f32_e32 v191, v174, v175
	v_cvt_pk_bf16_f32 v192, v140, v141
	v_cvt_pk_bf16_f32 v193, v142, v143
	v_cvt_pk_bf16_f32 v194, v144, v145
	v_cvt_pk_bf16_f32 v195, v190, v191
	global_store_dwordx4 v[236:237], v[192:195], off offset:256 nt
	s_nop 1
	s_waitcnt vmcnt(10)
	v_add_u32_e32 v158, 144, v189
	v_mad_i64_i32 v[236:237], s[24:25], v158, s19, v[136:137]
	v_lshl_add_u64 v[236:237], v[236:237], 0, v[138:139]
	v_pk_mul_f32 v[164:165], v[134:135], v[52:53] op_sel_hi:[0,1]
	v_pk_mul_f32 v[166:167], v[134:135], v[54:55] op_sel_hi:[0,1]
	v_pk_mul_f32 v[168:169], v[134:135], v[44:45] op_sel_hi:[0,1]
	v_pk_mul_f32 v[170:171], v[134:135], v[46:47] op_sel_hi:[0,1]
	v_pk_mul_f32 v[172:173], v[164:165], v[220:221]
	v_pk_mul_f32 v[174:175], v[164:165], v[220:221] op_sel:[0,1] op_sel_hi:[1,0]
	v_sub_f32_e32 v140, v172, v173
	v_add_f32_e32 v141, v174, v175
	v_pk_mul_f32 v[172:173], v[166:167], v[222:223]
	v_pk_mul_f32 v[174:175], v[166:167], v[222:223] op_sel:[0,1] op_sel_hi:[1,0]
	v_sub_f32_e32 v142, v172, v173
	v_add_f32_e32 v143, v174, v175
	v_pk_mul_f32 v[172:173], v[168:169], v[224:225]
	v_pk_mul_f32 v[174:175], v[168:169], v[224:225] op_sel:[0,1] op_sel_hi:[1,0]
	v_sub_f32_e32 v144, v172, v173
	v_add_f32_e32 v145, v174, v175
	v_pk_mul_f32 v[172:173], v[170:171], v[226:227]
	v_pk_mul_f32 v[174:175], v[170:171], v[226:227] op_sel:[0,1] op_sel_hi:[1,0]
	v_sub_f32_e32 v190, v172, v173
	v_add_f32_e32 v191, v174, v175
	v_cvt_pk_bf16_f32 v192, v140, v141
	v_cvt_pk_bf16_f32 v193, v142, v143
	v_cvt_pk_bf16_f32 v194, v144, v145
	v_cvt_pk_bf16_f32 v195, v190, v191
	global_store_dwordx4 v[236:237], v[192:195], off nt
	s_nop 1
	v_pk_mul_f32 v[164:165], v[134:135], v[32:33] op_sel_hi:[0,1]
	v_pk_mul_f32 v[166:167], v[134:135], v[34:35] op_sel_hi:[0,1]
	v_pk_mul_f32 v[168:169], v[134:135], v[24:25] op_sel_hi:[0,1]
	v_pk_mul_f32 v[170:171], v[134:135], v[26:27] op_sel_hi:[0,1]
	v_pk_mul_f32 v[172:173], v[164:165], v[220:221]
	v_pk_mul_f32 v[174:175], v[164:165], v[220:221] op_sel:[0,1] op_sel_hi:[1,0]
	v_sub_f32_e32 v140, v172, v173
	v_add_f32_e32 v141, v174, v175
	v_pk_mul_f32 v[172:173], v[166:167], v[222:223]
	v_pk_mul_f32 v[174:175], v[166:167], v[222:223] op_sel:[0,1] op_sel_hi:[1,0]
	v_sub_f32_e32 v142, v172, v173
	v_add_f32_e32 v143, v174, v175
	v_pk_mul_f32 v[172:173], v[168:169], v[224:225]
	v_pk_mul_f32 v[174:175], v[168:169], v[224:225] op_sel:[0,1] op_sel_hi:[1,0]
	v_sub_f32_e32 v144, v172, v173
	v_add_f32_e32 v145, v174, v175
	v_pk_mul_f32 v[172:173], v[170:171], v[226:227]
	v_pk_mul_f32 v[174:175], v[170:171], v[226:227] op_sel:[0,1] op_sel_hi:[1,0]
	v_sub_f32_e32 v190, v172, v173
	v_add_f32_e32 v191, v174, v175
	v_cvt_pk_bf16_f32 v192, v140, v141
	v_cvt_pk_bf16_f32 v193, v142, v143
	v_cvt_pk_bf16_f32 v194, v144, v145
	v_cvt_pk_bf16_f32 v195, v190, v191
	global_store_dwordx4 v[236:237], v[192:195], off offset:256 nt
	s_nop 1
	s_waitcnt vmcnt(8)
	v_add_u32_e32 v158, 160, v189
	v_mad_i64_i32 v[236:237], s[24:25], v158, s19, v[136:137]
	v_lshl_add_u64 v[236:237], v[236:237], 0, v[138:139]
	v_pk_mul_f32 v[164:165], v[134:135], v[36:37] op_sel_hi:[0,1]
	v_pk_mul_f32 v[166:167], v[134:135], v[38:39] op_sel_hi:[0,1]
	v_pk_mul_f32 v[168:169], v[134:135], v[28:29] op_sel_hi:[0,1]
	v_pk_mul_f32 v[170:171], v[134:135], v[30:31] op_sel_hi:[0,1]
	v_pk_mul_f32 v[172:173], v[164:165], v[228:229]
	v_pk_mul_f32 v[174:175], v[164:165], v[228:229] op_sel:[0,1] op_sel_hi:[1,0]
	v_sub_f32_e32 v140, v172, v173
	v_add_f32_e32 v141, v174, v175
	v_pk_mul_f32 v[172:173], v[166:167], v[230:231]
	v_pk_mul_f32 v[174:175], v[166:167], v[230:231] op_sel:[0,1] op_sel_hi:[1,0]
	v_sub_f32_e32 v142, v172, v173
	v_add_f32_e32 v143, v174, v175
	v_pk_mul_f32 v[172:173], v[168:169], v[232:233]
	v_pk_mul_f32 v[174:175], v[168:169], v[232:233] op_sel:[0,1] op_sel_hi:[1,0]
	v_sub_f32_e32 v144, v172, v173
	v_add_f32_e32 v145, v174, v175
	v_pk_mul_f32 v[172:173], v[170:171], v[234:235]
	v_pk_mul_f32 v[174:175], v[170:171], v[234:235] op_sel:[0,1] op_sel_hi:[1,0]
	v_sub_f32_e32 v190, v172, v173
	v_add_f32_e32 v191, v174, v175
	v_cvt_pk_bf16_f32 v192, v140, v141
	v_cvt_pk_bf16_f32 v193, v142, v143
	v_cvt_pk_bf16_f32 v194, v144, v145
	v_cvt_pk_bf16_f32 v195, v190, v191
	global_store_dwordx4 v[236:237], v[192:195], off nt
	s_nop 1
	v_pk_mul_f32 v[164:165], v[134:135], v[16:17] op_sel_hi:[0,1]
	v_pk_mul_f32 v[166:167], v[134:135], v[18:19] op_sel_hi:[0,1]
	v_pk_mul_f32 v[168:169], v[134:135], v[8:9] op_sel_hi:[0,1]
	v_pk_mul_f32 v[170:171], v[134:135], v[10:11] op_sel_hi:[0,1]
	v_pk_mul_f32 v[172:173], v[164:165], v[228:229]
	v_pk_mul_f32 v[174:175], v[164:165], v[228:229] op_sel:[0,1] op_sel_hi:[1,0]
	v_sub_f32_e32 v140, v172, v173
	v_add_f32_e32 v141, v174, v175
	v_pk_mul_f32 v[172:173], v[166:167], v[230:231]
	v_pk_mul_f32 v[174:175], v[166:167], v[230:231] op_sel:[0,1] op_sel_hi:[1,0]
	v_sub_f32_e32 v142, v172, v173
	v_add_f32_e32 v143, v174, v175
	v_pk_mul_f32 v[172:173], v[168:169], v[232:233]
	v_pk_mul_f32 v[174:175], v[168:169], v[232:233] op_sel:[0,1] op_sel_hi:[1,0]
	v_sub_f32_e32 v144, v172, v173
	v_add_f32_e32 v145, v174, v175
	v_pk_mul_f32 v[172:173], v[170:171], v[234:235]
	v_pk_mul_f32 v[174:175], v[170:171], v[234:235] op_sel:[0,1] op_sel_hi:[1,0]
	v_sub_f32_e32 v190, v172, v173
	v_add_f32_e32 v191, v174, v175
	v_cvt_pk_bf16_f32 v192, v140, v141
	v_cvt_pk_bf16_f32 v193, v142, v143
	v_cvt_pk_bf16_f32 v194, v144, v145
	v_cvt_pk_bf16_f32 v195, v190, v191
	global_store_dwordx4 v[236:237], v[192:195], off offset:256 nt
	s_nop 1
	s_waitcnt vmcnt(6)
	v_add_u32_e32 v158, 176, v189
	v_mad_i64_i32 v[162:163], s[24:25], v158, s19, v[136:137]
	v_lshl_add_u64 v[162:163], v[162:163], 0, v[138:139]
	v_pk_mul_f32 v[164:165], v[134:135], v[20:21] op_sel_hi:[0,1]
	v_pk_mul_f32 v[166:167], v[134:135], v[22:23] op_sel_hi:[0,1]
	v_pk_mul_f32 v[168:169], v[134:135], v[12:13] op_sel_hi:[0,1]
	v_pk_mul_f32 v[170:171], v[134:135], v[14:15] op_sel_hi:[0,1]
	v_pk_mul_f32 v[172:173], v[164:165], v[176:177]
	v_pk_mul_f32 v[174:175], v[164:165], v[176:177] op_sel:[0,1] op_sel_hi:[1,0]
	v_sub_f32_e32 v140, v172, v173
	v_add_f32_e32 v141, v174, v175
	v_pk_mul_f32 v[172:173], v[166:167], v[178:179]
	v_pk_mul_f32 v[174:175], v[166:167], v[178:179] op_sel:[0,1] op_sel_hi:[1,0]
	v_sub_f32_e32 v142, v172, v173
	v_add_f32_e32 v143, v174, v175
	v_pk_mul_f32 v[172:173], v[168:169], v[180:181]
	v_pk_mul_f32 v[174:175], v[168:169], v[180:181] op_sel:[0,1] op_sel_hi:[1,0]
	v_sub_f32_e32 v144, v172, v173
	v_add_f32_e32 v145, v174, v175
	v_pk_mul_f32 v[172:173], v[170:171], v[182:183]
	v_pk_mul_f32 v[174:175], v[170:171], v[182:183] op_sel:[0,1] op_sel_hi:[1,0]
	v_sub_f32_e32 v190, v172, v173
	v_add_f32_e32 v191, v174, v175
	v_cvt_pk_bf16_f32 v192, v140, v141
	v_cvt_pk_bf16_f32 v193, v142, v143
	v_cvt_pk_bf16_f32 v194, v144, v145
	v_cvt_pk_bf16_f32 v195, v190, v191
	global_store_dwordx4 v[162:163], v[192:195], off nt
	s_nop 1
	v_pk_mul_f32 v[164:165], v[134:135], v[4:5] op_sel_hi:[0,1]
	v_pk_mul_f32 v[166:167], v[134:135], v[6:7] op_sel_hi:[0,1]
	v_pk_mul_f32 v[168:169], v[134:135], v[0:1] op_sel_hi:[0,1]
	v_pk_mul_f32 v[170:171], v[134:135], v[2:3] op_sel_hi:[0,1]
	v_pk_mul_f32 v[172:173], v[164:165], v[176:177]
	v_pk_mul_f32 v[174:175], v[164:165], v[176:177] op_sel:[0,1] op_sel_hi:[1,0]
	v_sub_f32_e32 v140, v172, v173
	v_add_f32_e32 v141, v174, v175
	v_pk_mul_f32 v[172:173], v[166:167], v[178:179]
	v_pk_mul_f32 v[174:175], v[166:167], v[178:179] op_sel:[0,1] op_sel_hi:[1,0]
	v_sub_f32_e32 v142, v172, v173
	v_add_f32_e32 v143, v174, v175
	v_pk_mul_f32 v[172:173], v[168:169], v[180:181]
	v_pk_mul_f32 v[174:175], v[168:169], v[180:181] op_sel:[0,1] op_sel_hi:[1,0]
	v_sub_f32_e32 v144, v172, v173
	v_add_f32_e32 v145, v174, v175
	v_pk_mul_f32 v[172:173], v[170:171], v[182:183]
	v_pk_mul_f32 v[174:175], v[170:171], v[182:183] op_sel:[0,1] op_sel_hi:[1,0]
	v_sub_f32_e32 v190, v172, v173
	v_add_f32_e32 v191, v174, v175
	v_cvt_pk_bf16_f32 v130, v140, v141
	v_cvt_pk_bf16_f32 v131, v142, v143
	v_cvt_pk_bf16_f32 v132, v144, v145
	v_cvt_pk_bf16_f32 v133, v190, v191
	s_branch .LBB0_325

.LBB0_324:
	v_mov_b64_e32 v[130:131], s[8:9]
	s_movk_i32 s3, 0x2400
	v_mad_i64_i32 v[134:135], s[24:25], v189, s3, v[130:131]
	v_lshlrev_b64 v[132:133], 1, v[64:65]
	s_mov_b32 s26, 0xbfb8aa3b
	v_lshl_add_u64 v[138:139], v[134:135], 0, v[132:133]
	v_pk_mul_f32 v[134:135], v[126:127], s[26:27] op_sel_hi:[1,0]
	v_pk_mul_f32 v[136:137], v[128:129], s[26:27] op_sel_hi:[1,0]
	v_exp_f32_e32 v134, v134
	v_exp_f32_e32 v135, v135
	v_exp_f32_e32 v136, v136
	v_exp_f32_e32 v137, v137
	v_pk_mul_f32 v[140:141], v[122:123], s[26:27] op_sel_hi:[1,0]
	v_pk_mul_f32 v[142:143], v[124:125], s[26:27] op_sel_hi:[1,0]
	v_exp_f32_e32 v140, v140
	v_exp_f32_e32 v141, v141
	v_exp_f32_e32 v142, v142
	v_exp_f32_e32 v143, v143
	v_pk_add_f32 v[134:135], v[134:135], 1.0 op_sel_hi:[1,0]
	v_pk_add_f32 v[136:137], v[136:137], 1.0 op_sel_hi:[1,0]
	v_rcp_f32_e32 v134, v134
	v_rcp_f32_e32 v135, v135
	v_rcp_f32_e32 v136, v136
	v_rcp_f32_e32 v137, v137
	v_pk_add_f32 v[140:141], v[140:141], 1.0 op_sel_hi:[1,0]
	v_pk_add_f32 v[142:143], v[142:143], 1.0 op_sel_hi:[1,0]
	v_rcp_f32_e32 v140, v140
	v_rcp_f32_e32 v141, v141
	v_rcp_f32_e32 v142, v142
	v_rcp_f32_e32 v143, v143
	v_pk_mul_f32 v[134:135], v[126:127], v[134:135]
	v_pk_mul_f32 v[136:137], v[128:129], v[136:137]
	v_cvt_pk_bf16_f32 v134, v134, v135
	v_pk_mul_f32 v[140:141], v[122:123], v[140:141]
	v_cvt_pk_bf16_f32 v135, v136, v137
	v_pk_mul_f32 v[142:143], v[124:125], v[142:143]
	v_cvt_pk_bf16_f32 v136, v140, v141
	v_pk_mul_f32 v[140:141], v[106:107], s[26:27] op_sel_hi:[1,0]
	v_cvt_pk_bf16_f32 v137, v142, v143
	global_store_dwordx4 v[138:139], v[134:137], off nt
	v_pk_mul_f32 v[142:143], v[108:109], s[26:27] op_sel_hi:[1,0]
	v_exp_f32_e32 v140, v140
	v_pk_mul_f32 v[134:135], v[114:115], s[26:27] op_sel_hi:[1,0]
	v_pk_mul_f32 v[136:137], v[116:117], s[26:27] op_sel_hi:[1,0]
	v_exp_f32_e32 v134, v134
	v_exp_f32_e32 v135, v135
	v_exp_f32_e32 v136, v136
	v_exp_f32_e32 v137, v137
	v_exp_f32_e32 v141, v141
	v_exp_f32_e32 v142, v142
	v_exp_f32_e32 v143, v143
	v_pk_add_f32 v[134:135], v[134:135], 1.0 op_sel_hi:[1,0]
	v_pk_add_f32 v[136:137], v[136:137], 1.0 op_sel_hi:[1,0]
	v_rcp_f32_e32 v134, v134
	v_rcp_f32_e32 v135, v135
	v_rcp_f32_e32 v136, v136
	v_rcp_f32_e32 v137, v137
	v_pk_add_f32 v[140:141], v[140:141], 1.0 op_sel_hi:[1,0]
	v_pk_add_f32 v[142:143], v[142:143], 1.0 op_sel_hi:[1,0]
	v_rcp_f32_e32 v140, v140
	v_rcp_f32_e32 v141, v141
	v_rcp_f32_e32 v142, v142
	v_rcp_f32_e32 v143, v143
	v_pk_mul_f32 v[134:135], v[114:115], v[134:135]
	v_pk_mul_f32 v[136:137], v[116:117], v[136:137]
	v_cvt_pk_bf16_f32 v134, v134, v135
	v_pk_mul_f32 v[140:141], v[106:107], v[140:141]
	v_pk_mul_f32 v[142:143], v[108:109], v[142:143]
	v_cvt_pk_bf16_f32 v135, v136, v137
	v_cvt_pk_bf16_f32 v136, v140, v141
	v_pk_mul_f32 v[140:141], v[110:111], s[26:27] op_sel_hi:[1,0]
	v_cvt_pk_bf16_f32 v137, v142, v143
	global_store_dwordx4 v[138:139], v[134:137], off offset:256 nt
	v_pk_mul_f32 v[142:143], v[112:113], s[26:27] op_sel_hi:[1,0]
	v_exp_f32_e32 v140, v140
	v_or_b32_e32 v134, 16, v189
	v_mad_i64_i32 v[134:135], s[24:25], v134, s3, v[130:131]
	v_lshl_add_u64 v[138:139], v[134:135], 0, v[132:133]
	v_pk_mul_f32 v[134:135], v[118:119], s[26:27] op_sel_hi:[1,0]
	v_pk_mul_f32 v[136:137], v[120:121], s[26:27] op_sel_hi:[1,0]
	v_exp_f32_e32 v134, v134
	v_exp_f32_e32 v135, v135
	v_exp_f32_e32 v136, v136
	v_exp_f32_e32 v137, v137
	v_exp_f32_e32 v141, v141
	v_exp_f32_e32 v142, v142
	v_exp_f32_e32 v143, v143
	v_pk_add_f32 v[134:135], v[134:135], 1.0 op_sel_hi:[1,0]
	v_pk_add_f32 v[136:137], v[136:137], 1.0 op_sel_hi:[1,0]
	v_rcp_f32_e32 v134, v134
	v_rcp_f32_e32 v135, v135
	v_rcp_f32_e32 v136, v136
	v_rcp_f32_e32 v137, v137
	v_pk_add_f32 v[140:141], v[140:141], 1.0 op_sel_hi:[1,0]
	v_pk_add_f32 v[142:143], v[142:143], 1.0 op_sel_hi:[1,0]
	v_rcp_f32_e32 v140, v140
	v_rcp_f32_e32 v141, v141
	v_rcp_f32_e32 v142, v142
	v_rcp_f32_e32 v143, v143
	v_pk_mul_f32 v[134:135], v[118:119], v[134:135]
	v_pk_mul_f32 v[136:137], v[120:121], v[136:137]
	v_cvt_pk_bf16_f32 v134, v134, v135
	v_pk_mul_f32 v[140:141], v[110:111], v[140:141]
	v_cvt_pk_bf16_f32 v135, v136, v137
	v_pk_mul_f32 v[142:143], v[112:113], v[142:143]
	v_cvt_pk_bf16_f32 v136, v140, v141
	v_pk_mul_f32 v[140:141], v[90:91], s[26:27] op_sel_hi:[1,0]
	v_cvt_pk_bf16_f32 v137, v142, v143
	global_store_dwordx4 v[138:139], v[134:137], off nt
	v_pk_mul_f32 v[142:143], v[92:93], s[26:27] op_sel_hi:[1,0]
	v_exp_f32_e32 v140, v140
	v_pk_mul_f32 v[134:135], v[98:99], s[26:27] op_sel_hi:[1,0]
	v_pk_mul_f32 v[136:137], v[100:101], s[26:27] op_sel_hi:[1,0]
	v_exp_f32_e32 v134, v134
	v_exp_f32_e32 v135, v135
	v_exp_f32_e32 v136, v136
	v_exp_f32_e32 v137, v137
	v_exp_f32_e32 v141, v141
	v_exp_f32_e32 v142, v142
	v_exp_f32_e32 v143, v143
	v_pk_add_f32 v[134:135], v[134:135], 1.0 op_sel_hi:[1,0]
	v_pk_add_f32 v[136:137], v[136:137], 1.0 op_sel_hi:[1,0]
	v_rcp_f32_e32 v134, v134
	v_rcp_f32_e32 v135, v135
	v_rcp_f32_e32 v136, v136
	v_rcp_f32_e32 v137, v137
	v_pk_add_f32 v[140:141], v[140:141], 1.0 op_sel_hi:[1,0]
	v_pk_add_f32 v[142:143], v[142:143], 1.0 op_sel_hi:[1,0]
	v_rcp_f32_e32 v140, v140
	v_rcp_f32_e32 v141, v141
	v_rcp_f32_e32 v142, v142
	v_rcp_f32_e32 v143, v143
	v_pk_mul_f32 v[134:135], v[98:99], v[134:135]
	v_pk_mul_f32 v[136:137], v[100:101], v[136:137]
	v_cvt_pk_bf16_f32 v134, v134, v135
	v_pk_mul_f32 v[140:141], v[90:91], v[140:141]
	v_pk_mul_f32 v[142:143], v[92:93], v[142:143]
	v_cvt_pk_bf16_f32 v135, v136, v137
	v_cvt_pk_bf16_f32 v136, v140, v141
	v_pk_mul_f32 v[140:141], v[94:95], s[26:27] op_sel_hi:[1,0]
	v_cvt_pk_bf16_f32 v137, v142, v143
	global_store_dwordx4 v[138:139], v[134:137], off offset:256 nt
	v_pk_mul_f32 v[142:143], v[96:97], s[26:27] op_sel_hi:[1,0]
	v_exp_f32_e32 v140, v140
	v_or_b32_e32 v134, 32, v189
	v_mad_i64_i32 v[134:135], s[24:25], v134, s3, v[130:131]
	v_lshl_add_u64 v[138:139], v[134:135], 0, v[132:133]
	v_pk_mul_f32 v[134:135], v[102:103], s[26:27] op_sel_hi:[1,0]
	v_pk_mul_f32 v[136:137], v[104:105], s[26:27] op_sel_hi:[1,0]
	v_exp_f32_e32 v134, v134
	v_exp_f32_e32 v135, v135
	v_exp_f32_e32 v136, v136
	v_exp_f32_e32 v137, v137
	v_exp_f32_e32 v141, v141
	v_exp_f32_e32 v142, v142
	v_exp_f32_e32 v143, v143
	v_pk_add_f32 v[134:135], v[134:135], 1.0 op_sel_hi:[1,0]
	v_pk_add_f32 v[136:137], v[136:137], 1.0 op_sel_hi:[1,0]
	v_rcp_f32_e32 v134, v134
	v_rcp_f32_e32 v135, v135
	v_rcp_f32_e32 v136, v136
	v_rcp_f32_e32 v137, v137
	v_pk_add_f32 v[140:141], v[140:141], 1.0 op_sel_hi:[1,0]
	v_pk_add_f32 v[142:143], v[142:143], 1.0 op_sel_hi:[1,0]
	v_rcp_f32_e32 v140, v140
	v_rcp_f32_e32 v141, v141
	v_rcp_f32_e32 v142, v142
	v_rcp_f32_e32 v143, v143
	v_pk_mul_f32 v[134:135], v[102:103], v[134:135]
	v_pk_mul_f32 v[136:137], v[104:105], v[136:137]
	v_cvt_pk_bf16_f32 v134, v134, v135
	v_pk_mul_f32 v[140:141], v[94:95], v[140:141]
	v_cvt_pk_bf16_f32 v135, v136, v137
	v_pk_mul_f32 v[142:143], v[96:97], v[142:143]
	v_cvt_pk_bf16_f32 v136, v140, v141
	v_pk_mul_f32 v[140:141], v[74:75], s[26:27] op_sel_hi:[1,0]
	v_cvt_pk_bf16_f32 v137, v142, v143
	global_store_dwordx4 v[138:139], v[134:137], off nt
	v_pk_mul_f32 v[142:143], v[76:77], s[26:27] op_sel_hi:[1,0]
	v_exp_f32_e32 v140, v140
	v_pk_mul_f32 v[134:135], v[82:83], s[26:27] op_sel_hi:[1,0]
	v_pk_mul_f32 v[136:137], v[84:85], s[26:27] op_sel_hi:[1,0]
	v_exp_f32_e32 v134, v134
	v_exp_f32_e32 v135, v135
	v_exp_f32_e32 v136, v136
	v_exp_f32_e32 v137, v137
	v_exp_f32_e32 v141, v141
	v_exp_f32_e32 v142, v142
	v_exp_f32_e32 v143, v143
	v_pk_add_f32 v[134:135], v[134:135], 1.0 op_sel_hi:[1,0]
	v_pk_add_f32 v[136:137], v[136:137], 1.0 op_sel_hi:[1,0]
	v_rcp_f32_e32 v134, v134
	v_rcp_f32_e32 v135, v135
	v_rcp_f32_e32 v136, v136
	v_rcp_f32_e32 v137, v137
	v_pk_add_f32 v[140:141], v[140:141], 1.0 op_sel_hi:[1,0]
	v_pk_add_f32 v[142:143], v[142:143], 1.0 op_sel_hi:[1,0]
	v_rcp_f32_e32 v140, v140
	v_rcp_f32_e32 v141, v141
	v_rcp_f32_e32 v142, v142
	v_rcp_f32_e32 v143, v143
	v_pk_mul_f32 v[134:135], v[82:83], v[134:135]
	v_pk_mul_f32 v[136:137], v[84:85], v[136:137]
	v_cvt_pk_bf16_f32 v134, v134, v135
	v_pk_mul_f32 v[140:141], v[74:75], v[140:141]
	v_pk_mul_f32 v[142:143], v[76:77], v[142:143]
	v_cvt_pk_bf16_f32 v135, v136, v137
	v_cvt_pk_bf16_f32 v136, v140, v141
	v_pk_mul_f32 v[140:141], v[78:79], s[26:27] op_sel_hi:[1,0]
	v_cvt_pk_bf16_f32 v137, v142, v143
	global_store_dwordx4 v[138:139], v[134:137], off offset:256 nt
	v_pk_mul_f32 v[142:143], v[80:81], s[26:27] op_sel_hi:[1,0]
	v_exp_f32_e32 v140, v140
	v_or_b32_e32 v134, 48, v189
	v_mad_i64_i32 v[134:135], s[24:25], v134, s3, v[130:131]
	v_lshl_add_u64 v[138:139], v[134:135], 0, v[132:133]
	v_pk_mul_f32 v[134:135], v[86:87], s[26:27] op_sel_hi:[1,0]
	v_pk_mul_f32 v[136:137], v[88:89], s[26:27] op_sel_hi:[1,0]
	v_exp_f32_e32 v134, v134
	v_exp_f32_e32 v135, v135
	v_exp_f32_e32 v136, v136
	v_exp_f32_e32 v137, v137
	v_exp_f32_e32 v141, v141
	v_exp_f32_e32 v142, v142
	v_exp_f32_e32 v143, v143
	v_pk_add_f32 v[134:135], v[134:135], 1.0 op_sel_hi:[1,0]
	v_pk_add_f32 v[136:137], v[136:137], 1.0 op_sel_hi:[1,0]
	v_rcp_f32_e32 v134, v134
	v_rcp_f32_e32 v135, v135
	v_rcp_f32_e32 v136, v136
	v_rcp_f32_e32 v137, v137
	v_pk_add_f32 v[140:141], v[140:141], 1.0 op_sel_hi:[1,0]
	v_pk_add_f32 v[142:143], v[142:143], 1.0 op_sel_hi:[1,0]
	v_rcp_f32_e32 v140, v140
	v_rcp_f32_e32 v141, v141
	v_rcp_f32_e32 v142, v142
	v_rcp_f32_e32 v143, v143
	v_pk_mul_f32 v[134:135], v[86:87], v[134:135]
	v_pk_mul_f32 v[136:137], v[88:89], v[136:137]
	v_cvt_pk_bf16_f32 v134, v134, v135
	v_pk_mul_f32 v[140:141], v[78:79], v[140:141]
	v_cvt_pk_bf16_f32 v135, v136, v137
	v_pk_mul_f32 v[142:143], v[80:81], v[142:143]
	v_cvt_pk_bf16_f32 v136, v140, v141
	v_pk_mul_f32 v[140:141], v[66:67], s[26:27] op_sel_hi:[1,0]
	v_cvt_pk_bf16_f32 v137, v142, v143
	global_store_dwordx4 v[138:139], v[134:137], off nt
	v_pk_mul_f32 v[142:143], v[68:69], s[26:27] op_sel_hi:[1,0]
	v_exp_f32_e32 v140, v140
	v_pk_mul_f32 v[134:135], v[70:71], s[26:27] op_sel_hi:[1,0]
	v_pk_mul_f32 v[136:137], v[72:73], s[26:27] op_sel_hi:[1,0]
	v_exp_f32_e32 v134, v134
	v_exp_f32_e32 v135, v135
	v_exp_f32_e32 v136, v136
	v_exp_f32_e32 v137, v137
	v_exp_f32_e32 v141, v141
	v_exp_f32_e32 v142, v142
	v_exp_f32_e32 v143, v143
	v_pk_add_f32 v[134:135], v[134:135], 1.0 op_sel_hi:[1,0]
	v_pk_add_f32 v[136:137], v[136:137], 1.0 op_sel_hi:[1,0]
	v_rcp_f32_e32 v134, v134
	v_rcp_f32_e32 v135, v135
	v_rcp_f32_e32 v136, v136
	v_rcp_f32_e32 v137, v137
	v_pk_add_f32 v[140:141], v[140:141], 1.0 op_sel_hi:[1,0]
	v_pk_add_f32 v[142:143], v[142:143], 1.0 op_sel_hi:[1,0]
	v_rcp_f32_e32 v140, v140
	v_rcp_f32_e32 v141, v141
	v_rcp_f32_e32 v142, v142
	v_rcp_f32_e32 v143, v143
	v_pk_mul_f32 v[134:135], v[70:71], v[134:135]
	v_pk_mul_f32 v[136:137], v[72:73], v[136:137]
	v_cvt_pk_bf16_f32 v134, v134, v135
	v_pk_mul_f32 v[140:141], v[66:67], v[140:141]
	v_pk_mul_f32 v[142:143], v[68:69], v[142:143]
	v_cvt_pk_bf16_f32 v135, v136, v137
	v_cvt_pk_bf16_f32 v136, v140, v141
	v_pk_mul_f32 v[140:141], v[56:57], s[26:27] op_sel_hi:[1,0]
	v_cvt_pk_bf16_f32 v137, v142, v143
	global_store_dwordx4 v[138:139], v[134:137], off offset:256 nt
	v_pk_mul_f32 v[142:143], v[58:59], s[26:27] op_sel_hi:[1,0]
	v_exp_f32_e32 v140, v140
	v_add_u32_e32 v134, 0x80, v189
	v_mad_i64_i32 v[134:135], s[24:25], v134, s3, v[130:131]
	v_lshl_add_u64 v[138:139], v[134:135], 0, v[132:133]
	v_pk_mul_f32 v[134:135], v[60:61], s[26:27] op_sel_hi:[1,0]
	v_pk_mul_f32 v[136:137], v[62:63], s[26:27] op_sel_hi:[1,0]
	v_exp_f32_e32 v134, v134
	v_exp_f32_e32 v135, v135
	v_exp_f32_e32 v136, v136
	v_exp_f32_e32 v137, v137
	v_exp_f32_e32 v141, v141
	v_exp_f32_e32 v142, v142
	v_exp_f32_e32 v143, v143
	v_pk_add_f32 v[134:135], v[134:135], 1.0 op_sel_hi:[1,0]
	v_pk_add_f32 v[136:137], v[136:137], 1.0 op_sel_hi:[1,0]
	v_rcp_f32_e32 v134, v134
	v_rcp_f32_e32 v135, v135
	v_rcp_f32_e32 v136, v136
	v_rcp_f32_e32 v137, v137
	v_pk_add_f32 v[140:141], v[140:141], 1.0 op_sel_hi:[1,0]
	v_pk_add_f32 v[142:143], v[142:143], 1.0 op_sel_hi:[1,0]
	v_rcp_f32_e32 v140, v140
	v_rcp_f32_e32 v141, v141
	v_rcp_f32_e32 v142, v142
	v_rcp_f32_e32 v143, v143
	v_pk_mul_f32 v[134:135], v[60:61], v[134:135]
	v_pk_mul_f32 v[136:137], v[62:63], v[136:137]
	v_cvt_pk_bf16_f32 v134, v134, v135
	v_pk_mul_f32 v[140:141], v[56:57], v[140:141]
	v_cvt_pk_bf16_f32 v135, v136, v137
	v_pk_mul_f32 v[142:143], v[58:59], v[142:143]
	v_cvt_pk_bf16_f32 v136, v140, v141
	v_pk_mul_f32 v[140:141], v[40:41], s[26:27] op_sel_hi:[1,0]
	v_cvt_pk_bf16_f32 v137, v142, v143
	global_store_dwordx4 v[138:139], v[134:137], off nt
	v_pk_mul_f32 v[142:143], v[42:43], s[26:27] op_sel_hi:[1,0]
	v_exp_f32_e32 v140, v140
	v_pk_mul_f32 v[134:135], v[48:49], s[26:27] op_sel_hi:[1,0]
	v_pk_mul_f32 v[136:137], v[50:51], s[26:27] op_sel_hi:[1,0]
	v_exp_f32_e32 v134, v134
	v_exp_f32_e32 v135, v135
	v_exp_f32_e32 v136, v136
	v_exp_f32_e32 v137, v137
	v_exp_f32_e32 v141, v141
	v_exp_f32_e32 v142, v142
	v_exp_f32_e32 v143, v143
	v_pk_add_f32 v[134:135], v[134:135], 1.0 op_sel_hi:[1,0]
	v_pk_add_f32 v[136:137], v[136:137], 1.0 op_sel_hi:[1,0]
	v_rcp_f32_e32 v134, v134
	v_rcp_f32_e32 v135, v135
	v_rcp_f32_e32 v136, v136
	v_rcp_f32_e32 v137, v137
	v_pk_add_f32 v[140:141], v[140:141], 1.0 op_sel_hi:[1,0]
	v_pk_add_f32 v[142:143], v[142:143], 1.0 op_sel_hi:[1,0]
	v_rcp_f32_e32 v140, v140
	v_rcp_f32_e32 v141, v141
	v_rcp_f32_e32 v142, v142
	v_rcp_f32_e32 v143, v143
	v_pk_mul_f32 v[134:135], v[48:49], v[134:135]
	v_pk_mul_f32 v[136:137], v[50:51], v[136:137]
	v_cvt_pk_bf16_f32 v134, v134, v135
	v_pk_mul_f32 v[140:141], v[40:41], v[140:141]
	v_pk_mul_f32 v[142:143], v[42:43], v[142:143]
	v_cvt_pk_bf16_f32 v135, v136, v137
	v_cvt_pk_bf16_f32 v136, v140, v141
	v_pk_mul_f32 v[140:141], v[44:45], s[26:27] op_sel_hi:[1,0]
	v_cvt_pk_bf16_f32 v137, v142, v143
	global_store_dwordx4 v[138:139], v[134:137], off offset:256 nt
	v_pk_mul_f32 v[142:143], v[46:47], s[26:27] op_sel_hi:[1,0]
	v_exp_f32_e32 v140, v140
	v_add_u32_e32 v134, 0x90, v189
	v_mad_i64_i32 v[134:135], s[24:25], v134, s3, v[130:131]
	v_lshl_add_u64 v[138:139], v[134:135], 0, v[132:133]
	v_pk_mul_f32 v[134:135], v[52:53], s[26:27] op_sel_hi:[1,0]
	v_pk_mul_f32 v[136:137], v[54:55], s[26:27] op_sel_hi:[1,0]
	v_exp_f32_e32 v134, v134
	v_exp_f32_e32 v135, v135
	v_exp_f32_e32 v136, v136
	v_exp_f32_e32 v137, v137
	v_exp_f32_e32 v141, v141
	v_exp_f32_e32 v142, v142
	v_exp_f32_e32 v143, v143
	v_pk_add_f32 v[134:135], v[134:135], 1.0 op_sel_hi:[1,0]
	v_pk_add_f32 v[136:137], v[136:137], 1.0 op_sel_hi:[1,0]
	v_rcp_f32_e32 v134, v134
	v_rcp_f32_e32 v135, v135
	v_rcp_f32_e32 v136, v136
	v_rcp_f32_e32 v137, v137
	v_pk_add_f32 v[140:141], v[140:141], 1.0 op_sel_hi:[1,0]
	v_pk_add_f32 v[142:143], v[142:143], 1.0 op_sel_hi:[1,0]
	v_rcp_f32_e32 v140, v140
	v_rcp_f32_e32 v141, v141
	v_rcp_f32_e32 v142, v142
	v_rcp_f32_e32 v143, v143
	v_pk_mul_f32 v[134:135], v[52:53], v[134:135]
	v_pk_mul_f32 v[136:137], v[54:55], v[136:137]
	v_cvt_pk_bf16_f32 v134, v134, v135
	v_pk_mul_f32 v[140:141], v[44:45], v[140:141]
	v_cvt_pk_bf16_f32 v135, v136, v137
	v_pk_mul_f32 v[142:143], v[46:47], v[142:143]
	v_cvt_pk_bf16_f32 v136, v140, v141
	v_pk_mul_f32 v[140:141], v[24:25], s[26:27] op_sel_hi:[1,0]
	v_cvt_pk_bf16_f32 v137, v142, v143
	global_store_dwordx4 v[138:139], v[134:137], off nt
	v_pk_mul_f32 v[142:143], v[26:27], s[26:27] op_sel_hi:[1,0]
	v_exp_f32_e32 v140, v140
	v_pk_mul_f32 v[134:135], v[32:33], s[26:27] op_sel_hi:[1,0]
	v_pk_mul_f32 v[136:137], v[34:35], s[26:27] op_sel_hi:[1,0]
	v_exp_f32_e32 v134, v134
	v_exp_f32_e32 v135, v135
	v_exp_f32_e32 v136, v136
	v_exp_f32_e32 v137, v137
	v_exp_f32_e32 v141, v141
	v_exp_f32_e32 v142, v142
	v_exp_f32_e32 v143, v143
	v_pk_add_f32 v[134:135], v[134:135], 1.0 op_sel_hi:[1,0]
	v_pk_add_f32 v[136:137], v[136:137], 1.0 op_sel_hi:[1,0]
	v_rcp_f32_e32 v134, v134
	v_rcp_f32_e32 v135, v135
	v_rcp_f32_e32 v136, v136
	v_rcp_f32_e32 v137, v137
	v_pk_add_f32 v[140:141], v[140:141], 1.0 op_sel_hi:[1,0]
	v_pk_add_f32 v[142:143], v[142:143], 1.0 op_sel_hi:[1,0]
	v_rcp_f32_e32 v140, v140
	v_rcp_f32_e32 v141, v141
	v_rcp_f32_e32 v142, v142
	v_rcp_f32_e32 v143, v143
	v_pk_mul_f32 v[134:135], v[32:33], v[134:135]
	v_pk_mul_f32 v[136:137], v[34:35], v[136:137]
	v_cvt_pk_bf16_f32 v134, v134, v135
	v_pk_mul_f32 v[140:141], v[24:25], v[140:141]
	v_pk_mul_f32 v[142:143], v[26:27], v[142:143]
	v_cvt_pk_bf16_f32 v135, v136, v137
	v_cvt_pk_bf16_f32 v136, v140, v141
	v_pk_mul_f32 v[140:141], v[28:29], s[26:27] op_sel_hi:[1,0]
	v_cvt_pk_bf16_f32 v137, v142, v143
	global_store_dwordx4 v[138:139], v[134:137], off offset:256 nt
	v_pk_mul_f32 v[142:143], v[30:31], s[26:27] op_sel_hi:[1,0]
	v_exp_f32_e32 v140, v140
	v_add_u32_e32 v134, 0xa0, v189
	v_mad_i64_i32 v[134:135], s[24:25], v134, s3, v[130:131]
	v_lshl_add_u64 v[138:139], v[134:135], 0, v[132:133]
	v_pk_mul_f32 v[134:135], v[36:37], s[26:27] op_sel_hi:[1,0]
	v_pk_mul_f32 v[136:137], v[38:39], s[26:27] op_sel_hi:[1,0]
	v_exp_f32_e32 v134, v134
	v_exp_f32_e32 v135, v135
	v_exp_f32_e32 v136, v136
	v_exp_f32_e32 v137, v137
	v_exp_f32_e32 v141, v141
	v_exp_f32_e32 v142, v142
	v_exp_f32_e32 v143, v143
	v_pk_add_f32 v[134:135], v[134:135], 1.0 op_sel_hi:[1,0]
	v_pk_add_f32 v[136:137], v[136:137], 1.0 op_sel_hi:[1,0]
	v_rcp_f32_e32 v134, v134
	v_rcp_f32_e32 v135, v135
	v_rcp_f32_e32 v136, v136
	v_rcp_f32_e32 v137, v137
	v_pk_add_f32 v[140:141], v[140:141], 1.0 op_sel_hi:[1,0]
	v_pk_add_f32 v[142:143], v[142:143], 1.0 op_sel_hi:[1,0]
	v_rcp_f32_e32 v140, v140
	v_rcp_f32_e32 v141, v141
	v_rcp_f32_e32 v142, v142
	v_rcp_f32_e32 v143, v143
	v_pk_mul_f32 v[134:135], v[36:37], v[134:135]
	v_pk_mul_f32 v[136:137], v[38:39], v[136:137]
	v_cvt_pk_bf16_f32 v134, v134, v135
	v_pk_mul_f32 v[140:141], v[28:29], v[140:141]
	v_cvt_pk_bf16_f32 v135, v136, v137
	v_pk_mul_f32 v[142:143], v[30:31], v[142:143]
	v_cvt_pk_bf16_f32 v136, v140, v141
	v_pk_mul_f32 v[140:141], v[8:9], s[26:27] op_sel_hi:[1,0]
	v_cvt_pk_bf16_f32 v137, v142, v143
	global_store_dwordx4 v[138:139], v[134:137], off nt
	v_pk_mul_f32 v[142:143], v[10:11], s[26:27] op_sel_hi:[1,0]
	v_exp_f32_e32 v140, v140
	v_pk_mul_f32 v[134:135], v[16:17], s[26:27] op_sel_hi:[1,0]
	v_pk_mul_f32 v[136:137], v[18:19], s[26:27] op_sel_hi:[1,0]
	v_exp_f32_e32 v134, v134
	v_exp_f32_e32 v135, v135
	v_exp_f32_e32 v136, v136
	v_exp_f32_e32 v137, v137
	v_exp_f32_e32 v141, v141
	v_exp_f32_e32 v142, v142
	v_exp_f32_e32 v143, v143
	v_pk_add_f32 v[134:135], v[134:135], 1.0 op_sel_hi:[1,0]
	v_pk_add_f32 v[136:137], v[136:137], 1.0 op_sel_hi:[1,0]
	v_rcp_f32_e32 v134, v134
	v_rcp_f32_e32 v135, v135
	v_rcp_f32_e32 v136, v136
	v_rcp_f32_e32 v137, v137
	v_pk_add_f32 v[140:141], v[140:141], 1.0 op_sel_hi:[1,0]
	v_pk_add_f32 v[142:143], v[142:143], 1.0 op_sel_hi:[1,0]
	v_rcp_f32_e32 v140, v140
	v_rcp_f32_e32 v141, v141
	v_rcp_f32_e32 v142, v142
	v_rcp_f32_e32 v143, v143
	v_pk_mul_f32 v[134:135], v[16:17], v[134:135]
	v_pk_mul_f32 v[136:137], v[18:19], v[136:137]
	v_cvt_pk_bf16_f32 v134, v134, v135
	v_pk_mul_f32 v[140:141], v[8:9], v[140:141]
	v_pk_mul_f32 v[142:143], v[10:11], v[142:143]
	v_cvt_pk_bf16_f32 v135, v136, v137
	v_cvt_pk_bf16_f32 v136, v140, v141
	s_nop 0
	v_cvt_pk_bf16_f32 v137, v142, v143
	global_store_dwordx4 v[138:139], v[134:137], off offset:256 nt
	s_nop 1
	v_add_u32_e32 v134, 0xb0, v189
	v_mad_i64_i32 v[130:131], s[24:25], v134, s3, v[130:131]
	v_lshl_add_u64 v[162:163], v[130:131], 0, v[132:133]
	v_pk_mul_f32 v[130:131], v[20:21], s[26:27] op_sel_hi:[1,0]
	v_pk_mul_f32 v[132:133], v[22:23], s[26:27] op_sel_hi:[1,0]
	v_exp_f32_e32 v130, v130
	v_exp_f32_e32 v131, v131
	v_exp_f32_e32 v132, v132
	v_exp_f32_e32 v133, v133
	v_pk_mul_f32 v[134:135], v[12:13], s[26:27] op_sel_hi:[1,0]
	v_pk_mul_f32 v[136:137], v[14:15], s[26:27] op_sel_hi:[1,0]
	v_exp_f32_e32 v134, v134
	v_exp_f32_e32 v135, v135
	v_exp_f32_e32 v136, v136
	v_exp_f32_e32 v137, v137
	v_pk_add_f32 v[130:131], v[130:131], 1.0 op_sel_hi:[1,0]
	v_pk_add_f32 v[132:133], v[132:133], 1.0 op_sel_hi:[1,0]
	v_rcp_f32_e32 v130, v130
	v_rcp_f32_e32 v131, v131
	v_rcp_f32_e32 v132, v132
	v_rcp_f32_e32 v133, v133
	v_pk_add_f32 v[134:135], v[134:135], 1.0 op_sel_hi:[1,0]
	v_pk_add_f32 v[136:137], v[136:137], 1.0 op_sel_hi:[1,0]
	v_rcp_f32_e32 v134, v134
	v_rcp_f32_e32 v135, v135
	v_rcp_f32_e32 v136, v136
	v_rcp_f32_e32 v137, v137
	v_pk_mul_f32 v[130:131], v[20:21], v[130:131]
	v_pk_mul_f32 v[132:133], v[22:23], v[132:133]
	v_pk_mul_f32 v[134:135], v[12:13], v[134:135]
	v_pk_mul_f32 v[136:137], v[14:15], v[136:137]
	v_cvt_pk_bf16_f32 v130, v130, v131
	v_cvt_pk_bf16_f32 v131, v132, v133
	v_cvt_pk_bf16_f32 v132, v134, v135
	v_pk_mul_f32 v[134:135], v[0:1], s[26:27] op_sel_hi:[1,0]
	v_cvt_pk_bf16_f32 v133, v136, v137
	global_store_dwordx4 v[162:163], v[130:133], off nt
	v_pk_mul_f32 v[136:137], v[2:3], s[26:27] op_sel_hi:[1,0]
	v_exp_f32_e32 v134, v134
	v_pk_mul_f32 v[130:131], v[4:5], s[26:27] op_sel_hi:[1,0]
	v_pk_mul_f32 v[132:133], v[6:7], s[26:27] op_sel_hi:[1,0]
	v_exp_f32_e32 v130, v130
	v_exp_f32_e32 v131, v131
	v_exp_f32_e32 v132, v132
	v_exp_f32_e32 v133, v133
	v_exp_f32_e32 v135, v135
	v_exp_f32_e32 v136, v136
	v_exp_f32_e32 v137, v137
	v_pk_add_f32 v[130:131], v[130:131], 1.0 op_sel_hi:[1,0]
	v_pk_add_f32 v[132:133], v[132:133], 1.0 op_sel_hi:[1,0]
	v_rcp_f32_e32 v130, v130
	v_rcp_f32_e32 v131, v131
	v_rcp_f32_e32 v132, v132
	v_rcp_f32_e32 v133, v133
	v_pk_add_f32 v[134:135], v[134:135], 1.0 op_sel_hi:[1,0]
	v_pk_add_f32 v[136:137], v[136:137], 1.0 op_sel_hi:[1,0]
	v_rcp_f32_e32 v134, v134
	v_rcp_f32_e32 v135, v135
	v_rcp_f32_e32 v136, v136
	v_rcp_f32_e32 v137, v137
	v_pk_mul_f32 v[130:131], v[4:5], v[130:131]
	v_pk_mul_f32 v[132:133], v[6:7], v[132:133]
	v_pk_mul_f32 v[134:135], v[0:1], v[134:135]
	v_pk_mul_f32 v[136:137], v[2:3], v[136:137]
	v_cvt_pk_bf16_f32 v130, v130, v131
	v_cvt_pk_bf16_f32 v131, v132, v133
	v_cvt_pk_bf16_f32 v132, v134, v135
	s_nop 0
	v_cvt_pk_bf16_f32 v133, v136, v137

.LBB0_326:
	s_and_b64 vcc, exec, s[24:25]
	s_cbranch_vccz .LBB0_328
	s_branch .Lg1ls_fast
	v_subrev_u32_e32 v130, s2, v64
	v_ashrrev_i32_e32 v131, 31, v130
	v_lshl_add_u64 v[134:135], v[130:131], 2, s[10:11]
	global_load_dwordx4 v[138:141], v[134:135], off offset:16
	global_load_dwordx4 v[142:145], v[134:135], off
	global_load_dwordx4 v[130:133], v[134:135], off offset:528
	s_nop 0
	global_load_dwordx4 v[134:137], v[134:135], off offset:512
	v_ashrrev_i32_e32 v159, 31, v64
	v_mov_b32_e32 v158, v64
	s_mov_b32 s24, 0xbfb8aa3b
	v_lshlrev_b64 v[164:165], 1, v[158:159]
	v_pk_mul_f32 v[158:159], v[126:127], s[24:25] op_sel_hi:[1,0]
	v_mov_b64_e32 v[162:163], s[8:9]
	v_exp_f32_e32 v158, v158
	v_exp_f32_e32 v159, v159
	s_movk_i32 s17, 0x2400
	v_mad_i64_i32 v[160:161], s[2:3], v189, s17, v[162:163]
	v_lshl_add_u64 v[178:179], v[160:161], 0, v[164:165]
	v_pk_add_f32 v[160:161], v[158:159], 1.0 op_sel_hi:[1,0]
	s_mov_b32 s26, 0x3f317218
	v_rcp_f32_e32 v160, v160
	v_rcp_f32_e32 v161, v161
	s_waitcnt vmcnt(0)
	v_pk_add_f32 v[158:159], v[142:143], 1.0 op_sel_hi:[1,0] neg_lo:[1,0] neg_hi:[1,0]
	s_nop 0
	v_pk_fma_f32 v[160:161], v[160:161], v[158:159], v[142:143]
	s_nop 0
	v_max_f32_e32 v161, 0xda24260, v161
	v_max_f32_e32 v160, 0xda24260, v160
	v_log_f32_e32 v160, v160
	v_log_f32_e32 v161, v161
	s_nop 0
	v_pk_mul_f32 v[170:171], v[160:161], s[26:27] op_sel_hi:[1,0]
	v_pk_mul_f32 v[160:161], v[128:129], s[24:25] op_sel_hi:[1,0]
	v_cvt_pk_bf16_f32 v170, v170, v171
	s_nop 0
	v_exp_f32_e32 v160, v160
	v_exp_f32_e32 v161, v161
	s_nop 0
	v_pk_add_f32 v[166:167], v[160:161], 1.0 op_sel_hi:[1,0]
	s_nop 0
	v_rcp_f32_e32 v166, v166
	v_rcp_f32_e32 v167, v167
	v_pk_add_f32 v[160:161], v[144:145], 1.0 op_sel_hi:[1,0] neg_lo:[1,0] neg_hi:[1,0]
	s_nop 0
	v_pk_fma_f32 v[166:167], v[166:167], v[160:161], v[144:145]
	s_nop 0
	v_max_f32_e32 v167, 0xda24260, v167
	v_max_f32_e32 v166, 0xda24260, v166
	v_log_f32_e32 v166, v166
	v_log_f32_e32 v167, v167
	s_nop 0
	v_pk_mul_f32 v[172:173], v[166:167], s[26:27] op_sel_hi:[1,0]
	v_pk_mul_f32 v[166:167], v[122:123], s[24:25] op_sel_hi:[1,0]
	v_cvt_pk_bf16_f32 v171, v172, v173
	s_nop 0
	v_exp_f32_e32 v166, v166
	v_exp_f32_e32 v167, v167
	s_nop 0
	v_pk_add_f32 v[168:169], v[166:167], 1.0 op_sel_hi:[1,0]
	s_nop 0
	v_rcp_f32_e32 v168, v168
	v_rcp_f32_e32 v169, v169
	v_pk_add_f32 v[166:167], v[138:139], 1.0 op_sel_hi:[1,0] neg_lo:[1,0] neg_hi:[1,0]
	s_nop 0
	v_pk_fma_f32 v[168:169], v[168:169], v[166:167], v[138:139]
	s_nop 0
	v_max_f32_e32 v169, 0xda24260, v169
	v_max_f32_e32 v168, 0xda24260, v168
	v_log_f32_e32 v168, v168
	v_log_f32_e32 v169, v169
	s_nop 0
	v_pk_mul_f32 v[174:175], v[168:169], s[26:27] op_sel_hi:[1,0]
	v_pk_mul_f32 v[168:169], v[124:125], s[24:25] op_sel_hi:[1,0]
	v_cvt_pk_bf16_f32 v172, v174, v175
	s_nop 0
	v_exp_f32_e32 v168, v168
	v_exp_f32_e32 v169, v169
	s_nop 0
	v_pk_add_f32 v[176:177], v[168:169], 1.0 op_sel_hi:[1,0]
	s_nop 0
	v_rcp_f32_e32 v176, v176
	v_rcp_f32_e32 v177, v177
	v_pk_add_f32 v[168:169], v[140:141], 1.0 op_sel_hi:[1,0] neg_lo:[1,0] neg_hi:[1,0]
	s_nop 0
	v_pk_fma_f32 v[176:177], v[176:177], v[168:169], v[140:141]
	s_nop 0
	v_max_f32_e32 v177, 0xda24260, v177
	v_max_f32_e32 v176, 0xda24260, v176
	v_log_f32_e32 v176, v176
	v_log_f32_e32 v177, v177
	s_nop 0
	v_pk_mul_f32 v[176:177], v[176:177], s[26:27] op_sel_hi:[1,0]
	s_nop 0
	v_cvt_pk_bf16_f32 v173, v176, v177
	global_store_dwordx4 v[178:179], v[170:173], off nt
	v_pk_add_f32 v[176:177], v[130:131], 1.0 op_sel_hi:[1,0] neg_lo:[1,0] neg_hi:[1,0]
	s_nop 0
	v_pk_mul_f32 v[170:171], v[114:115], s[24:25] op_sel_hi:[1,0]
	s_nop 0
	v_exp_f32_e32 v170, v170
	v_exp_f32_e32 v171, v171
	s_nop 0
	v_pk_add_f32 v[172:173], v[170:171], 1.0 op_sel_hi:[1,0]
	s_nop 0
	v_rcp_f32_e32 v172, v172
	v_rcp_f32_e32 v173, v173
	v_pk_add_f32 v[170:171], v[134:135], 1.0 op_sel_hi:[1,0] neg_lo:[1,0] neg_hi:[1,0]
	s_nop 0
	v_pk_fma_f32 v[172:173], v[172:173], v[170:171], v[134:135]
	s_nop 0
	v_max_f32_e32 v173, 0xda24260, v173
	v_max_f32_e32 v172, 0xda24260, v172
	v_log_f32_e32 v172, v172
	v_log_f32_e32 v173, v173
	s_nop 0
	v_pk_mul_f32 v[180:181], v[172:173], s[26:27] op_sel_hi:[1,0]
	v_pk_mul_f32 v[172:173], v[116:117], s[24:25] op_sel_hi:[1,0]
	v_cvt_pk_bf16_f32 v180, v180, v181
	s_nop 0
	v_exp_f32_e32 v172, v172
	v_exp_f32_e32 v173, v173
	s_nop 0
	v_pk_add_f32 v[174:175], v[172:173], 1.0 op_sel_hi:[1,0]
	s_nop 0
	v_rcp_f32_e32 v174, v174
	v_rcp_f32_e32 v175, v175
	v_pk_add_f32 v[172:173], v[136:137], 1.0 op_sel_hi:[1,0] neg_lo:[1,0] neg_hi:[1,0]
	s_nop 0
	v_pk_fma_f32 v[174:175], v[174:175], v[172:173], v[136:137]
	s_nop 0
	v_max_f32_e32 v175, 0xda24260, v175
	v_max_f32_e32 v174, 0xda24260, v174
	v_log_f32_e32 v174, v174
	v_log_f32_e32 v175, v175
	s_nop 0
	v_pk_mul_f32 v[182:183], v[174:175], s[26:27] op_sel_hi:[1,0]
	v_pk_mul_f32 v[174:175], v[106:107], s[24:25] op_sel_hi:[1,0]
	v_cvt_pk_bf16_f32 v181, v182, v183
	s_nop 0
	v_exp_f32_e32 v174, v174
	v_exp_f32_e32 v175, v175
	s_nop 0
	v_pk_add_f32 v[174:175], v[174:175], 1.0 op_sel_hi:[1,0]
	s_nop 0
	v_rcp_f32_e32 v174, v174
	v_rcp_f32_e32 v175, v175
	s_nop 0
	v_pk_fma_f32 v[174:175], v[174:175], v[176:177], v[130:131]
	s_nop 0
	v_max_f32_e32 v175, 0xda24260, v175
	v_max_f32_e32 v174, 0xda24260, v174
	v_log_f32_e32 v174, v174
	v_log_f32_e32 v175, v175
	s_nop 0
	v_pk_mul_f32 v[190:191], v[174:175], s[26:27] op_sel_hi:[1,0]
	v_pk_mul_f32 v[174:175], v[108:109], s[24:25] op_sel_hi:[1,0]
	v_cvt_pk_bf16_f32 v182, v190, v191
	v_pk_mul_f32 v[190:191], v[110:111], s[24:25] op_sel_hi:[1,0]
	v_exp_f32_e32 v174, v174
	v_exp_f32_e32 v175, v175
	v_exp_f32_e32 v190, v190
	v_exp_f32_e32 v191, v191
	v_pk_add_f32 v[192:193], v[174:175], 1.0 op_sel_hi:[1,0]
	s_nop 0
	v_rcp_f32_e32 v192, v192
	v_rcp_f32_e32 v193, v193
	v_pk_add_f32 v[174:175], v[132:133], 1.0 op_sel_hi:[1,0] neg_lo:[1,0] neg_hi:[1,0]
	v_pk_add_f32 v[190:191], v[190:191], 1.0 op_sel_hi:[1,0]
	v_pk_fma_f32 v[192:193], v[192:193], v[174:175], v[132:133]
	s_nop 0
	v_max_f32_e32 v193, 0xda24260, v193
	v_max_f32_e32 v192, 0xda24260, v192
	v_log_f32_e32 v192, v192
	v_log_f32_e32 v193, v193
	v_rcp_f32_e32 v190, v190
	v_rcp_f32_e32 v191, v191
	v_pk_mul_f32 v[192:193], v[192:193], s[26:27] op_sel_hi:[1,0]
	s_nop 0
	v_cvt_pk_bf16_f32 v183, v192, v193
	global_store_dwordx4 v[178:179], v[180:183], off offset:256 nt
	v_pk_mul_f32 v[192:193], v[112:113], s[24:25] op_sel_hi:[1,0]
	v_pk_fma_f32 v[190:191], v[190:191], v[166:167], v[138:139]
	v_pk_mul_f32 v[180:181], v[118:119], s[24:25] op_sel_hi:[1,0]
	v_pk_mul_f32 v[182:183], v[120:121], s[24:25] op_sel_hi:[1,0]
	v_exp_f32_e32 v180, v180
	v_exp_f32_e32 v181, v181
	v_exp_f32_e32 v182, v182
	v_exp_f32_e32 v183, v183
	v_exp_f32_e32 v192, v192
	v_exp_f32_e32 v193, v193
	v_pk_add_f32 v[180:181], v[180:181], 1.0 op_sel_hi:[1,0]
	v_pk_add_f32 v[182:183], v[182:183], 1.0 op_sel_hi:[1,0]
	v_rcp_f32_e32 v180, v180
	v_rcp_f32_e32 v181, v181
	v_rcp_f32_e32 v182, v182
	v_rcp_f32_e32 v183, v183
	v_pk_add_f32 v[192:193], v[192:193], 1.0 op_sel_hi:[1,0]
	v_pk_fma_f32 v[180:181], v[180:181], v[158:159], v[142:143]
	v_rcp_f32_e32 v192, v192
	v_rcp_f32_e32 v193, v193
	v_pk_fma_f32 v[182:183], v[182:183], v[160:161], v[144:145]
	v_max_f32_e32 v181, 0xda24260, v181
	v_max_f32_e32 v180, 0xda24260, v180
	v_max_f32_e32 v183, 0xda24260, v183
	v_max_f32_e32 v182, 0xda24260, v182
	v_pk_fma_f32 v[192:193], v[192:193], v[168:169], v[140:141]
	v_log_f32_e32 v180, v180
	v_log_f32_e32 v181, v181
	v_log_f32_e32 v182, v182
	v_log_f32_e32 v183, v183
	v_max_f32_e32 v191, 0xda24260, v191
	v_max_f32_e32 v190, 0xda24260, v190
	v_max_f32_e32 v193, 0xda24260, v193
	v_max_f32_e32 v192, 0xda24260, v192
	v_log_f32_e32 v190, v190
	v_log_f32_e32 v191, v191
	v_log_f32_e32 v192, v192
	v_log_f32_e32 v193, v193
	v_or_b32_e32 v178, 16, v189
	v_mad_i64_i32 v[178:179], s[2:3], v178, s17, v[162:163]
	v_pk_mul_f32 v[180:181], v[180:181], s[26:27] op_sel_hi:[1,0]
	v_pk_mul_f32 v[182:183], v[182:183], s[26:27] op_sel_hi:[1,0]
	v_lshl_add_u64 v[178:179], v[178:179], 0, v[164:165]
	v_pk_mul_f32 v[190:191], v[190:191], s[26:27] op_sel_hi:[1,0]
	v_pk_mul_f32 v[192:193], v[192:193], s[26:27] op_sel_hi:[1,0]
	v_cvt_pk_bf16_f32 v180, v180, v181
	v_cvt_pk_bf16_f32 v181, v182, v183
	v_cvt_pk_bf16_f32 v182, v190, v191
	v_pk_mul_f32 v[190:191], v[90:91], s[24:25] op_sel_hi:[1,0]
	v_cvt_pk_bf16_f32 v183, v192, v193
	global_store_dwordx4 v[178:179], v[180:183], off nt
	v_pk_mul_f32 v[192:193], v[92:93], s[24:25] op_sel_hi:[1,0]
	v_exp_f32_e32 v190, v190
	v_pk_mul_f32 v[180:181], v[98:99], s[24:25] op_sel_hi:[1,0]
	v_pk_mul_f32 v[182:183], v[100:101], s[24:25] op_sel_hi:[1,0]
	v_exp_f32_e32 v180, v180
	v_exp_f32_e32 v181, v181
	v_exp_f32_e32 v182, v182
	v_exp_f32_e32 v183, v183
	v_exp_f32_e32 v191, v191
	v_exp_f32_e32 v192, v192
	v_exp_f32_e32 v193, v193
	v_pk_add_f32 v[180:181], v[180:181], 1.0 op_sel_hi:[1,0]
	v_pk_add_f32 v[182:183], v[182:183], 1.0 op_sel_hi:[1,0]
	v_rcp_f32_e32 v180, v180
	v_rcp_f32_e32 v181, v181
	v_rcp_f32_e32 v182, v182
	v_rcp_f32_e32 v183, v183
	v_pk_add_f32 v[190:191], v[190:191], 1.0 op_sel_hi:[1,0]
	v_pk_add_f32 v[192:193], v[192:193], 1.0 op_sel_hi:[1,0]
	v_rcp_f32_e32 v190, v190
	v_rcp_f32_e32 v191, v191
	v_rcp_f32_e32 v192, v192
	v_rcp_f32_e32 v193, v193
	v_pk_fma_f32 v[180:181], v[180:181], v[170:171], v[134:135]
	v_pk_fma_f32 v[182:183], v[182:183], v[172:173], v[136:137]
	v_max_f32_e32 v181, 0xda24260, v181
	v_max_f32_e32 v180, 0xda24260, v180
	v_max_f32_e32 v183, 0xda24260, v183
	v_max_f32_e32 v182, 0xda24260, v182
	v_pk_fma_f32 v[190:191], v[190:191], v[176:177], v[130:131]
	v_pk_fma_f32 v[192:193], v[192:193], v[174:175], v[132:133]
	v_log_f32_e32 v180, v180
	v_log_f32_e32 v181, v181
	v_log_f32_e32 v182, v182
	v_log_f32_e32 v183, v183
	v_max_f32_e32 v191, 0xda24260, v191
	v_max_f32_e32 v190, 0xda24260, v190
	v_max_f32_e32 v193, 0xda24260, v193
	v_max_f32_e32 v192, 0xda24260, v192
	v_log_f32_e32 v190, v190
	v_log_f32_e32 v191, v191
	v_log_f32_e32 v192, v192
	v_log_f32_e32 v193, v193
	v_pk_mul_f32 v[180:181], v[180:181], s[26:27] op_sel_hi:[1,0]
	v_pk_mul_f32 v[182:183], v[182:183], s[26:27] op_sel_hi:[1,0]
	v_pk_mul_f32 v[190:191], v[190:191], s[26:27] op_sel_hi:[1,0]
	v_pk_mul_f32 v[192:193], v[192:193], s[26:27] op_sel_hi:[1,0]
	v_cvt_pk_bf16_f32 v180, v180, v181
	v_cvt_pk_bf16_f32 v181, v182, v183
	v_cvt_pk_bf16_f32 v182, v190, v191
	v_pk_mul_f32 v[190:191], v[94:95], s[24:25] op_sel_hi:[1,0]
	v_cvt_pk_bf16_f32 v183, v192, v193
	global_store_dwordx4 v[178:179], v[180:183], off offset:256 nt
	v_pk_mul_f32 v[192:193], v[96:97], s[24:25] op_sel_hi:[1,0]
	v_exp_f32_e32 v190, v190
	v_pk_mul_f32 v[180:181], v[102:103], s[24:25] op_sel_hi:[1,0]
	v_pk_mul_f32 v[182:183], v[104:105], s[24:25] op_sel_hi:[1,0]
	v_exp_f32_e32 v180, v180
	v_exp_f32_e32 v181, v181
	v_exp_f32_e32 v182, v182
	v_exp_f32_e32 v183, v183
	v_exp_f32_e32 v191, v191
	v_exp_f32_e32 v192, v192
	v_exp_f32_e32 v193, v193
	v_pk_add_f32 v[180:181], v[180:181], 1.0 op_sel_hi:[1,0]
	v_pk_add_f32 v[182:183], v[182:183], 1.0 op_sel_hi:[1,0]
	v_rcp_f32_e32 v180, v180
	v_rcp_f32_e32 v181, v181
	v_rcp_f32_e32 v182, v182
	v_rcp_f32_e32 v183, v183
	v_pk_add_f32 v[190:191], v[190:191], 1.0 op_sel_hi:[1,0]
	v_pk_add_f32 v[192:193], v[192:193], 1.0 op_sel_hi:[1,0]
	v_rcp_f32_e32 v190, v190
	v_rcp_f32_e32 v191, v191
	v_rcp_f32_e32 v192, v192
	v_rcp_f32_e32 v193, v193
	v_pk_fma_f32 v[180:181], v[180:181], v[158:159], v[142:143]
	v_pk_fma_f32 v[182:183], v[182:183], v[160:161], v[144:145]
	v_max_f32_e32 v181, 0xda24260, v181
	v_max_f32_e32 v180, 0xda24260, v180
	v_max_f32_e32 v183, 0xda24260, v183
	v_max_f32_e32 v182, 0xda24260, v182
	v_pk_fma_f32 v[190:191], v[190:191], v[166:167], v[138:139]
	v_pk_fma_f32 v[192:193], v[192:193], v[168:169], v[140:141]
	v_log_f32_e32 v180, v180
	v_log_f32_e32 v181, v181
	v_log_f32_e32 v182, v182
	v_log_f32_e32 v183, v183
	v_max_f32_e32 v191, 0xda24260, v191
	v_max_f32_e32 v190, 0xda24260, v190
	v_max_f32_e32 v193, 0xda24260, v193
	v_max_f32_e32 v192, 0xda24260, v192
	v_log_f32_e32 v190, v190
	v_log_f32_e32 v191, v191
	v_log_f32_e32 v192, v192
	v_log_f32_e32 v193, v193
	v_or_b32_e32 v178, 32, v189
	v_mad_i64_i32 v[178:179], s[2:3], v178, s17, v[162:163]
	v_pk_mul_f32 v[180:181], v[180:181], s[26:27] op_sel_hi:[1,0]
	v_pk_mul_f32 v[182:183], v[182:183], s[26:27] op_sel_hi:[1,0]
	v_lshl_add_u64 v[178:179], v[178:179], 0, v[164:165]
	v_pk_mul_f32 v[190:191], v[190:191], s[26:27] op_sel_hi:[1,0]
	v_pk_mul_f32 v[192:193], v[192:193], s[26:27] op_sel_hi:[1,0]
	v_cvt_pk_bf16_f32 v180, v180, v181
	v_cvt_pk_bf16_f32 v181, v182, v183
	v_cvt_pk_bf16_f32 v182, v190, v191
	v_pk_mul_f32 v[190:191], v[74:75], s[24:25] op_sel_hi:[1,0]
	v_cvt_pk_bf16_f32 v183, v192, v193
	global_store_dwordx4 v[178:179], v[180:183], off nt
	v_pk_mul_f32 v[192:193], v[76:77], s[24:25] op_sel_hi:[1,0]
	v_exp_f32_e32 v190, v190
	v_pk_mul_f32 v[180:181], v[82:83], s[24:25] op_sel_hi:[1,0]
	v_pk_mul_f32 v[182:183], v[84:85], s[24:25] op_sel_hi:[1,0]
	v_exp_f32_e32 v180, v180
	v_exp_f32_e32 v181, v181
	v_exp_f32_e32 v182, v182
	v_exp_f32_e32 v183, v183
	v_exp_f32_e32 v191, v191
	v_exp_f32_e32 v192, v192
	v_exp_f32_e32 v193, v193
	v_pk_add_f32 v[180:181], v[180:181], 1.0 op_sel_hi:[1,0]
	v_pk_add_f32 v[182:183], v[182:183], 1.0 op_sel_hi:[1,0]
	v_rcp_f32_e32 v180, v180
	v_rcp_f32_e32 v181, v181
	v_rcp_f32_e32 v182, v182
	v_rcp_f32_e32 v183, v183
	v_pk_add_f32 v[190:191], v[190:191], 1.0 op_sel_hi:[1,0]
	v_pk_add_f32 v[192:193], v[192:193], 1.0 op_sel_hi:[1,0]
	v_rcp_f32_e32 v190, v190
	v_rcp_f32_e32 v191, v191
	v_rcp_f32_e32 v192, v192
	v_rcp_f32_e32 v193, v193
	v_pk_fma_f32 v[180:181], v[180:181], v[170:171], v[134:135]
	v_pk_fma_f32 v[182:183], v[182:183], v[172:173], v[136:137]
	v_max_f32_e32 v181, 0xda24260, v181
	v_max_f32_e32 v180, 0xda24260, v180
	v_max_f32_e32 v183, 0xda24260, v183
	v_max_f32_e32 v182, 0xda24260, v182
	v_pk_fma_f32 v[190:191], v[190:191], v[176:177], v[130:131]
	v_pk_fma_f32 v[192:193], v[192:193], v[174:175], v[132:133]
	v_log_f32_e32 v180, v180
	v_log_f32_e32 v181, v181
	v_log_f32_e32 v182, v182
	v_log_f32_e32 v183, v183
	v_max_f32_e32 v191, 0xda24260, v191
	v_max_f32_e32 v190, 0xda24260, v190
	v_max_f32_e32 v193, 0xda24260, v193
	v_max_f32_e32 v192, 0xda24260, v192
	v_log_f32_e32 v190, v190
	v_log_f32_e32 v191, v191
	v_log_f32_e32 v192, v192
	v_log_f32_e32 v193, v193
	v_pk_mul_f32 v[180:181], v[180:181], s[26:27] op_sel_hi:[1,0]
	v_pk_mul_f32 v[182:183], v[182:183], s[26:27] op_sel_hi:[1,0]
	v_pk_mul_f32 v[190:191], v[190:191], s[26:27] op_sel_hi:[1,0]
	v_pk_mul_f32 v[192:193], v[192:193], s[26:27] op_sel_hi:[1,0]
	v_cvt_pk_bf16_f32 v180, v180, v181
	v_cvt_pk_bf16_f32 v181, v182, v183
	v_cvt_pk_bf16_f32 v182, v190, v191
	v_pk_mul_f32 v[190:191], v[78:79], s[24:25] op_sel_hi:[1,0]
	v_cvt_pk_bf16_f32 v183, v192, v193
	global_store_dwordx4 v[178:179], v[180:183], off offset:256 nt
	v_pk_mul_f32 v[192:193], v[80:81], s[24:25] op_sel_hi:[1,0]
	v_exp_f32_e32 v190, v190
	v_pk_mul_f32 v[180:181], v[86:87], s[24:25] op_sel_hi:[1,0]
	v_pk_mul_f32 v[182:183], v[88:89], s[24:25] op_sel_hi:[1,0]
	v_exp_f32_e32 v180, v180
	v_exp_f32_e32 v181, v181
	v_exp_f32_e32 v182, v182
	v_exp_f32_e32 v183, v183
	v_exp_f32_e32 v191, v191
	v_exp_f32_e32 v192, v192
	v_exp_f32_e32 v193, v193
	v_pk_add_f32 v[180:181], v[180:181], 1.0 op_sel_hi:[1,0]
	v_pk_add_f32 v[182:183], v[182:183], 1.0 op_sel_hi:[1,0]
	v_rcp_f32_e32 v180, v180
	v_rcp_f32_e32 v181, v181
	v_rcp_f32_e32 v182, v182
	v_rcp_f32_e32 v183, v183
	v_pk_add_f32 v[190:191], v[190:191], 1.0 op_sel_hi:[1,0]
	v_pk_add_f32 v[192:193], v[192:193], 1.0 op_sel_hi:[1,0]
	v_rcp_f32_e32 v190, v190
	v_rcp_f32_e32 v191, v191
	v_rcp_f32_e32 v192, v192
	v_rcp_f32_e32 v193, v193
	v_pk_fma_f32 v[180:181], v[180:181], v[158:159], v[142:143]
	v_pk_fma_f32 v[182:183], v[182:183], v[160:161], v[144:145]
	v_max_f32_e32 v181, 0xda24260, v181
	v_max_f32_e32 v180, 0xda24260, v180
	v_max_f32_e32 v183, 0xda24260, v183
	v_max_f32_e32 v182, 0xda24260, v182
	v_pk_fma_f32 v[190:191], v[190:191], v[166:167], v[138:139]
	v_pk_fma_f32 v[192:193], v[192:193], v[168:169], v[140:141]
	v_log_f32_e32 v180, v180
	v_log_f32_e32 v181, v181
	v_log_f32_e32 v182, v182
	v_log_f32_e32 v183, v183
	v_max_f32_e32 v191, 0xda24260, v191
	v_max_f32_e32 v190, 0xda24260, v190
	v_max_f32_e32 v193, 0xda24260, v193
	v_max_f32_e32 v192, 0xda24260, v192
	v_log_f32_e32 v190, v190
	v_log_f32_e32 v191, v191
	v_log_f32_e32 v192, v192
	v_log_f32_e32 v193, v193
	v_or_b32_e32 v178, 48, v189
	v_mad_i64_i32 v[178:179], s[2:3], v178, s17, v[162:163]
	v_pk_mul_f32 v[180:181], v[180:181], s[26:27] op_sel_hi:[1,0]
	v_pk_mul_f32 v[182:183], v[182:183], s[26:27] op_sel_hi:[1,0]
	v_lshl_add_u64 v[178:179], v[178:179], 0, v[164:165]
	v_pk_mul_f32 v[190:191], v[190:191], s[26:27] op_sel_hi:[1,0]
	v_pk_mul_f32 v[192:193], v[192:193], s[26:27] op_sel_hi:[1,0]
	v_cvt_pk_bf16_f32 v180, v180, v181
	v_cvt_pk_bf16_f32 v181, v182, v183
	v_cvt_pk_bf16_f32 v182, v190, v191
	v_pk_mul_f32 v[190:191], v[66:67], s[24:25] op_sel_hi:[1,0]
	v_cvt_pk_bf16_f32 v183, v192, v193
	global_store_dwordx4 v[178:179], v[180:183], off nt
	v_pk_mul_f32 v[192:193], v[68:69], s[24:25] op_sel_hi:[1,0]
	v_exp_f32_e32 v190, v190
	v_pk_mul_f32 v[180:181], v[70:71], s[24:25] op_sel_hi:[1,0]
	v_pk_mul_f32 v[182:183], v[72:73], s[24:25] op_sel_hi:[1,0]
	v_exp_f32_e32 v180, v180
	v_exp_f32_e32 v181, v181
	v_exp_f32_e32 v182, v182
	v_exp_f32_e32 v183, v183
	v_exp_f32_e32 v191, v191
	v_exp_f32_e32 v192, v192
	v_exp_f32_e32 v193, v193
	v_pk_add_f32 v[180:181], v[180:181], 1.0 op_sel_hi:[1,0]
	v_pk_add_f32 v[182:183], v[182:183], 1.0 op_sel_hi:[1,0]
	v_rcp_f32_e32 v180, v180
	v_rcp_f32_e32 v181, v181
	v_rcp_f32_e32 v182, v182
	v_rcp_f32_e32 v183, v183
	v_pk_add_f32 v[190:191], v[190:191], 1.0 op_sel_hi:[1,0]
	v_pk_add_f32 v[192:193], v[192:193], 1.0 op_sel_hi:[1,0]
	v_rcp_f32_e32 v190, v190
	v_rcp_f32_e32 v191, v191
	v_rcp_f32_e32 v192, v192
	v_rcp_f32_e32 v193, v193
	v_pk_fma_f32 v[180:181], v[180:181], v[170:171], v[134:135]
	v_pk_fma_f32 v[182:183], v[182:183], v[172:173], v[136:137]
	v_max_f32_e32 v181, 0xda24260, v181
	v_max_f32_e32 v180, 0xda24260, v180
	v_max_f32_e32 v183, 0xda24260, v183
	v_max_f32_e32 v182, 0xda24260, v182
	v_pk_fma_f32 v[190:191], v[190:191], v[176:177], v[130:131]
	v_pk_fma_f32 v[192:193], v[192:193], v[174:175], v[132:133]
	v_log_f32_e32 v180, v180
	v_log_f32_e32 v181, v181
	v_log_f32_e32 v182, v182
	v_log_f32_e32 v183, v183
	v_max_f32_e32 v191, 0xda24260, v191
	v_max_f32_e32 v190, 0xda24260, v190
	v_max_f32_e32 v193, 0xda24260, v193
	v_max_f32_e32 v192, 0xda24260, v192
	v_log_f32_e32 v190, v190
	v_log_f32_e32 v191, v191
	v_log_f32_e32 v192, v192
	v_log_f32_e32 v193, v193
	v_pk_mul_f32 v[180:181], v[180:181], s[26:27] op_sel_hi:[1,0]
	v_pk_mul_f32 v[182:183], v[182:183], s[26:27] op_sel_hi:[1,0]
	v_pk_mul_f32 v[190:191], v[190:191], s[26:27] op_sel_hi:[1,0]
	v_pk_mul_f32 v[192:193], v[192:193], s[26:27] op_sel_hi:[1,0]
	v_cvt_pk_bf16_f32 v180, v180, v181
	v_cvt_pk_bf16_f32 v181, v182, v183
	v_cvt_pk_bf16_f32 v182, v190, v191
	v_pk_mul_f32 v[190:191], v[56:57], s[24:25] op_sel_hi:[1,0]
	v_cvt_pk_bf16_f32 v183, v192, v193
	global_store_dwordx4 v[178:179], v[180:183], off offset:256 nt
	v_pk_mul_f32 v[192:193], v[58:59], s[24:25] op_sel_hi:[1,0]
	v_exp_f32_e32 v190, v190
	v_pk_mul_f32 v[180:181], v[60:61], s[24:25] op_sel_hi:[1,0]
	v_pk_mul_f32 v[182:183], v[62:63], s[24:25] op_sel_hi:[1,0]
	v_exp_f32_e32 v180, v180
	v_exp_f32_e32 v181, v181
	v_exp_f32_e32 v182, v182
	v_exp_f32_e32 v183, v183
	v_exp_f32_e32 v191, v191
	v_exp_f32_e32 v192, v192
	v_exp_f32_e32 v193, v193
	v_pk_add_f32 v[180:181], v[180:181], 1.0 op_sel_hi:[1,0]
	v_pk_add_f32 v[182:183], v[182:183], 1.0 op_sel_hi:[1,0]
	v_rcp_f32_e32 v180, v180
	v_rcp_f32_e32 v181, v181
	v_rcp_f32_e32 v182, v182
	v_rcp_f32_e32 v183, v183
	v_pk_add_f32 v[190:191], v[190:191], 1.0 op_sel_hi:[1,0]
	v_pk_add_f32 v[192:193], v[192:193], 1.0 op_sel_hi:[1,0]
	v_rcp_f32_e32 v190, v190
	v_rcp_f32_e32 v191, v191
	v_rcp_f32_e32 v192, v192
	v_rcp_f32_e32 v193, v193
	v_pk_fma_f32 v[180:181], v[180:181], v[158:159], v[142:143]
	v_pk_fma_f32 v[182:183], v[182:183], v[160:161], v[144:145]
	v_max_f32_e32 v181, 0xda24260, v181
	v_max_f32_e32 v180, 0xda24260, v180
	v_max_f32_e32 v183, 0xda24260, v183
	v_max_f32_e32 v182, 0xda24260, v182
	v_pk_fma_f32 v[190:191], v[190:191], v[166:167], v[138:139]
	v_pk_fma_f32 v[192:193], v[192:193], v[168:169], v[140:141]
	v_log_f32_e32 v180, v180
	v_log_f32_e32 v181, v181
	v_log_f32_e32 v182, v182
	v_log_f32_e32 v183, v183
	v_max_f32_e32 v191, 0xda24260, v191
	v_max_f32_e32 v190, 0xda24260, v190
	v_max_f32_e32 v193, 0xda24260, v193
	v_max_f32_e32 v192, 0xda24260, v192
	v_log_f32_e32 v190, v190
	v_log_f32_e32 v191, v191
	v_log_f32_e32 v192, v192
	v_log_f32_e32 v193, v193
	v_add_u32_e32 v178, 0x80, v189
	v_mad_i64_i32 v[178:179], s[2:3], v178, s17, v[162:163]
	v_pk_mul_f32 v[180:181], v[180:181], s[26:27] op_sel_hi:[1,0]
	v_pk_mul_f32 v[182:183], v[182:183], s[26:27] op_sel_hi:[1,0]
	v_lshl_add_u64 v[178:179], v[178:179], 0, v[164:165]
	v_pk_mul_f32 v[190:191], v[190:191], s[26:27] op_sel_hi:[1,0]
	v_pk_mul_f32 v[192:193], v[192:193], s[26:27] op_sel_hi:[1,0]
	v_cvt_pk_bf16_f32 v180, v180, v181
	v_cvt_pk_bf16_f32 v181, v182, v183
	v_cvt_pk_bf16_f32 v182, v190, v191
	v_pk_mul_f32 v[190:191], v[40:41], s[24:25] op_sel_hi:[1,0]
	v_cvt_pk_bf16_f32 v183, v192, v193
	global_store_dwordx4 v[178:179], v[180:183], off nt
	v_pk_mul_f32 v[192:193], v[42:43], s[24:25] op_sel_hi:[1,0]
	v_exp_f32_e32 v190, v190
	v_pk_mul_f32 v[180:181], v[48:49], s[24:25] op_sel_hi:[1,0]
	v_pk_mul_f32 v[182:183], v[50:51], s[24:25] op_sel_hi:[1,0]
	v_exp_f32_e32 v180, v180
	v_exp_f32_e32 v181, v181
	v_exp_f32_e32 v182, v182
	v_exp_f32_e32 v183, v183
	v_exp_f32_e32 v191, v191
	v_exp_f32_e32 v192, v192
	v_exp_f32_e32 v193, v193
	v_pk_add_f32 v[180:181], v[180:181], 1.0 op_sel_hi:[1,0]
	v_pk_add_f32 v[182:183], v[182:183], 1.0 op_sel_hi:[1,0]
	v_rcp_f32_e32 v180, v180
	v_rcp_f32_e32 v181, v181
	v_rcp_f32_e32 v182, v182
	v_rcp_f32_e32 v183, v183
	v_pk_add_f32 v[190:191], v[190:191], 1.0 op_sel_hi:[1,0]
	v_pk_add_f32 v[192:193], v[192:193], 1.0 op_sel_hi:[1,0]
	v_rcp_f32_e32 v190, v190
	v_rcp_f32_e32 v191, v191
	v_rcp_f32_e32 v192, v192
	v_rcp_f32_e32 v193, v193
	v_pk_fma_f32 v[180:181], v[180:181], v[170:171], v[134:135]
	v_pk_fma_f32 v[182:183], v[182:183], v[172:173], v[136:137]
	v_max_f32_e32 v181, 0xda24260, v181
	v_max_f32_e32 v180, 0xda24260, v180
	v_max_f32_e32 v183, 0xda24260, v183
	v_max_f32_e32 v182, 0xda24260, v182
	v_pk_fma_f32 v[190:191], v[190:191], v[176:177], v[130:131]
	v_pk_fma_f32 v[192:193], v[192:193], v[174:175], v[132:133]
	v_log_f32_e32 v180, v180
	v_log_f32_e32 v181, v181
	v_log_f32_e32 v182, v182
	v_log_f32_e32 v183, v183
	v_max_f32_e32 v191, 0xda24260, v191
	v_max_f32_e32 v190, 0xda24260, v190
	v_max_f32_e32 v193, 0xda24260, v193
	v_max_f32_e32 v192, 0xda24260, v192
	v_log_f32_e32 v190, v190
	v_log_f32_e32 v191, v191
	v_log_f32_e32 v192, v192
	v_log_f32_e32 v193, v193
	v_pk_mul_f32 v[180:181], v[180:181], s[26:27] op_sel_hi:[1,0]
	v_pk_mul_f32 v[182:183], v[182:183], s[26:27] op_sel_hi:[1,0]
	v_pk_mul_f32 v[190:191], v[190:191], s[26:27] op_sel_hi:[1,0]
	v_pk_mul_f32 v[192:193], v[192:193], s[26:27] op_sel_hi:[1,0]
	v_cvt_pk_bf16_f32 v180, v180, v181
	v_cvt_pk_bf16_f32 v181, v182, v183
	v_cvt_pk_bf16_f32 v182, v190, v191
	v_pk_mul_f32 v[190:191], v[44:45], s[24:25] op_sel_hi:[1,0]
	v_cvt_pk_bf16_f32 v183, v192, v193
	global_store_dwordx4 v[178:179], v[180:183], off offset:256 nt
	v_pk_mul_f32 v[192:193], v[46:47], s[24:25] op_sel_hi:[1,0]
	v_exp_f32_e32 v190, v190
	v_pk_mul_f32 v[180:181], v[52:53], s[24:25] op_sel_hi:[1,0]
	v_pk_mul_f32 v[182:183], v[54:55], s[24:25] op_sel_hi:[1,0]
	v_exp_f32_e32 v180, v180
	v_exp_f32_e32 v181, v181
	v_exp_f32_e32 v182, v182
	v_exp_f32_e32 v183, v183
	v_exp_f32_e32 v191, v191
	v_exp_f32_e32 v192, v192
	v_exp_f32_e32 v193, v193
	v_pk_add_f32 v[180:181], v[180:181], 1.0 op_sel_hi:[1,0]
	v_pk_add_f32 v[182:183], v[182:183], 1.0 op_sel_hi:[1,0]
	v_rcp_f32_e32 v180, v180
	v_rcp_f32_e32 v181, v181
	v_rcp_f32_e32 v182, v182
	v_rcp_f32_e32 v183, v183
	v_pk_add_f32 v[190:191], v[190:191], 1.0 op_sel_hi:[1,0]
	v_pk_add_f32 v[192:193], v[192:193], 1.0 op_sel_hi:[1,0]
	v_rcp_f32_e32 v190, v190
	v_rcp_f32_e32 v191, v191
	v_rcp_f32_e32 v192, v192
	v_rcp_f32_e32 v193, v193
	v_pk_fma_f32 v[180:181], v[180:181], v[158:159], v[142:143]
	v_pk_fma_f32 v[182:183], v[182:183], v[160:161], v[144:145]
	v_max_f32_e32 v181, 0xda24260, v181
	v_max_f32_e32 v180, 0xda24260, v180
	v_max_f32_e32 v183, 0xda24260, v183
	v_max_f32_e32 v182, 0xda24260, v182
	v_pk_fma_f32 v[190:191], v[190:191], v[166:167], v[138:139]
	v_pk_fma_f32 v[192:193], v[192:193], v[168:169], v[140:141]
	v_log_f32_e32 v180, v180
	v_log_f32_e32 v181, v181
	v_log_f32_e32 v182, v182
	v_log_f32_e32 v183, v183
	v_max_f32_e32 v191, 0xda24260, v191
	v_max_f32_e32 v190, 0xda24260, v190
	v_max_f32_e32 v193, 0xda24260, v193
	v_max_f32_e32 v192, 0xda24260, v192
	v_log_f32_e32 v190, v190
	v_log_f32_e32 v191, v191
	v_log_f32_e32 v192, v192
	v_log_f32_e32 v193, v193
	v_add_u32_e32 v178, 0x90, v189
	v_mad_i64_i32 v[178:179], s[2:3], v178, s17, v[162:163]
	v_pk_mul_f32 v[180:181], v[180:181], s[26:27] op_sel_hi:[1,0]
	v_pk_mul_f32 v[182:183], v[182:183], s[26:27] op_sel_hi:[1,0]
	v_lshl_add_u64 v[178:179], v[178:179], 0, v[164:165]
	v_pk_mul_f32 v[190:191], v[190:191], s[26:27] op_sel_hi:[1,0]
	v_pk_mul_f32 v[192:193], v[192:193], s[26:27] op_sel_hi:[1,0]
	v_cvt_pk_bf16_f32 v180, v180, v181
	v_cvt_pk_bf16_f32 v181, v182, v183
	v_cvt_pk_bf16_f32 v182, v190, v191
	v_pk_mul_f32 v[190:191], v[24:25], s[24:25] op_sel_hi:[1,0]
	v_cvt_pk_bf16_f32 v183, v192, v193
	global_store_dwordx4 v[178:179], v[180:183], off nt
	v_pk_mul_f32 v[192:193], v[26:27], s[24:25] op_sel_hi:[1,0]
	v_exp_f32_e32 v190, v190
	v_pk_mul_f32 v[180:181], v[32:33], s[24:25] op_sel_hi:[1,0]
	v_pk_mul_f32 v[182:183], v[34:35], s[24:25] op_sel_hi:[1,0]
	v_exp_f32_e32 v180, v180
	v_exp_f32_e32 v181, v181
	v_exp_f32_e32 v182, v182
	v_exp_f32_e32 v183, v183
	v_exp_f32_e32 v191, v191
	v_exp_f32_e32 v192, v192
	v_exp_f32_e32 v193, v193
	v_pk_add_f32 v[180:181], v[180:181], 1.0 op_sel_hi:[1,0]
	v_pk_add_f32 v[182:183], v[182:183], 1.0 op_sel_hi:[1,0]
	v_rcp_f32_e32 v180, v180
	v_rcp_f32_e32 v181, v181
	v_rcp_f32_e32 v182, v182
	v_rcp_f32_e32 v183, v183
	v_pk_add_f32 v[190:191], v[190:191], 1.0 op_sel_hi:[1,0]
	v_pk_add_f32 v[192:193], v[192:193], 1.0 op_sel_hi:[1,0]
	v_rcp_f32_e32 v190, v190
	v_rcp_f32_e32 v191, v191
	v_rcp_f32_e32 v192, v192
	v_rcp_f32_e32 v193, v193
	v_pk_fma_f32 v[180:181], v[180:181], v[170:171], v[134:135]
	v_pk_fma_f32 v[182:183], v[182:183], v[172:173], v[136:137]
	v_max_f32_e32 v181, 0xda24260, v181
	v_max_f32_e32 v180, 0xda24260, v180
	v_max_f32_e32 v183, 0xda24260, v183
	v_max_f32_e32 v182, 0xda24260, v182
	v_pk_fma_f32 v[190:191], v[190:191], v[176:177], v[130:131]
	v_pk_fma_f32 v[192:193], v[192:193], v[174:175], v[132:133]
	v_log_f32_e32 v180, v180
	v_log_f32_e32 v181, v181
	v_log_f32_e32 v182, v182
	v_log_f32_e32 v183, v183
	v_max_f32_e32 v191, 0xda24260, v191
	v_max_f32_e32 v190, 0xda24260, v190
	v_max_f32_e32 v193, 0xda24260, v193
	v_max_f32_e32 v192, 0xda24260, v192
	v_log_f32_e32 v190, v190
	v_log_f32_e32 v191, v191
	v_log_f32_e32 v192, v192
	v_log_f32_e32 v193, v193
	v_pk_mul_f32 v[180:181], v[180:181], s[26:27] op_sel_hi:[1,0]
	v_pk_mul_f32 v[182:183], v[182:183], s[26:27] op_sel_hi:[1,0]
	v_pk_mul_f32 v[190:191], v[190:191], s[26:27] op_sel_hi:[1,0]
	v_pk_mul_f32 v[192:193], v[192:193], s[26:27] op_sel_hi:[1,0]
	v_cvt_pk_bf16_f32 v180, v180, v181
	v_cvt_pk_bf16_f32 v181, v182, v183
	v_cvt_pk_bf16_f32 v182, v190, v191
	v_pk_mul_f32 v[190:191], v[28:29], s[24:25] op_sel_hi:[1,0]
	v_cvt_pk_bf16_f32 v183, v192, v193
	global_store_dwordx4 v[178:179], v[180:183], off offset:256 nt
	v_pk_mul_f32 v[192:193], v[30:31], s[24:25] op_sel_hi:[1,0]
	v_exp_f32_e32 v190, v190
	v_pk_mul_f32 v[180:181], v[36:37], s[24:25] op_sel_hi:[1,0]
	v_pk_mul_f32 v[182:183], v[38:39], s[24:25] op_sel_hi:[1,0]
	v_exp_f32_e32 v180, v180
	v_exp_f32_e32 v181, v181
	v_exp_f32_e32 v182, v182
	v_exp_f32_e32 v183, v183
	v_exp_f32_e32 v191, v191
	v_exp_f32_e32 v192, v192
	v_exp_f32_e32 v193, v193
	v_pk_add_f32 v[180:181], v[180:181], 1.0 op_sel_hi:[1,0]
	v_pk_add_f32 v[182:183], v[182:183], 1.0 op_sel_hi:[1,0]
	v_rcp_f32_e32 v180, v180
	v_rcp_f32_e32 v181, v181
	v_rcp_f32_e32 v182, v182
	v_rcp_f32_e32 v183, v183
	v_pk_add_f32 v[190:191], v[190:191], 1.0 op_sel_hi:[1,0]
	v_pk_add_f32 v[192:193], v[192:193], 1.0 op_sel_hi:[1,0]
	v_rcp_f32_e32 v190, v190
	v_rcp_f32_e32 v191, v191
	v_rcp_f32_e32 v192, v192
	v_rcp_f32_e32 v193, v193
	v_pk_fma_f32 v[180:181], v[180:181], v[158:159], v[142:143]
	v_pk_fma_f32 v[182:183], v[182:183], v[160:161], v[144:145]
	v_max_f32_e32 v181, 0xda24260, v181
	v_max_f32_e32 v180, 0xda24260, v180
	v_max_f32_e32 v183, 0xda24260, v183
	v_max_f32_e32 v182, 0xda24260, v182
	v_pk_fma_f32 v[190:191], v[190:191], v[166:167], v[138:139]
	v_pk_fma_f32 v[192:193], v[192:193], v[168:169], v[140:141]
	v_log_f32_e32 v180, v180
	v_log_f32_e32 v181, v181
	v_log_f32_e32 v182, v182
	v_log_f32_e32 v183, v183
	v_max_f32_e32 v191, 0xda24260, v191
	v_max_f32_e32 v190, 0xda24260, v190
	v_max_f32_e32 v193, 0xda24260, v193
	v_max_f32_e32 v192, 0xda24260, v192
	v_log_f32_e32 v190, v190
	v_log_f32_e32 v191, v191
	v_log_f32_e32 v192, v192
	v_log_f32_e32 v193, v193
	v_add_u32_e32 v178, 0xa0, v189
	v_mad_i64_i32 v[178:179], s[2:3], v178, s17, v[162:163]
	v_pk_mul_f32 v[180:181], v[180:181], s[26:27] op_sel_hi:[1,0]
	v_pk_mul_f32 v[182:183], v[182:183], s[26:27] op_sel_hi:[1,0]
	v_lshl_add_u64 v[178:179], v[178:179], 0, v[164:165]
	v_pk_mul_f32 v[190:191], v[190:191], s[26:27] op_sel_hi:[1,0]
	v_pk_mul_f32 v[192:193], v[192:193], s[26:27] op_sel_hi:[1,0]
	v_cvt_pk_bf16_f32 v180, v180, v181
	v_cvt_pk_bf16_f32 v181, v182, v183
	v_cvt_pk_bf16_f32 v182, v190, v191
	v_pk_mul_f32 v[190:191], v[8:9], s[24:25] op_sel_hi:[1,0]
	v_cvt_pk_bf16_f32 v183, v192, v193
	global_store_dwordx4 v[178:179], v[180:183], off nt
	v_pk_mul_f32 v[192:193], v[10:11], s[24:25] op_sel_hi:[1,0]
	v_exp_f32_e32 v190, v190
	v_pk_mul_f32 v[180:181], v[16:17], s[24:25] op_sel_hi:[1,0]
	v_pk_mul_f32 v[182:183], v[18:19], s[24:25] op_sel_hi:[1,0]
	v_exp_f32_e32 v180, v180
	v_exp_f32_e32 v181, v181
	v_exp_f32_e32 v182, v182
	v_exp_f32_e32 v183, v183
	v_exp_f32_e32 v191, v191
	v_exp_f32_e32 v192, v192
	v_exp_f32_e32 v193, v193
	v_pk_add_f32 v[180:181], v[180:181], 1.0 op_sel_hi:[1,0]
	v_pk_add_f32 v[182:183], v[182:183], 1.0 op_sel_hi:[1,0]
	v_rcp_f32_e32 v180, v180
	v_rcp_f32_e32 v181, v181
	v_rcp_f32_e32 v182, v182
	v_rcp_f32_e32 v183, v183
	v_pk_add_f32 v[190:191], v[190:191], 1.0 op_sel_hi:[1,0]
	v_pk_add_f32 v[192:193], v[192:193], 1.0 op_sel_hi:[1,0]
	v_rcp_f32_e32 v190, v190
	v_rcp_f32_e32 v191, v191
	v_rcp_f32_e32 v192, v192
	v_rcp_f32_e32 v193, v193
	v_pk_fma_f32 v[180:181], v[180:181], v[170:171], v[134:135]
	v_pk_fma_f32 v[182:183], v[182:183], v[172:173], v[136:137]
	v_max_f32_e32 v181, 0xda24260, v181
	v_max_f32_e32 v180, 0xda24260, v180
	v_max_f32_e32 v183, 0xda24260, v183
	v_max_f32_e32 v182, 0xda24260, v182
	v_pk_fma_f32 v[190:191], v[190:191], v[176:177], v[130:131]
	v_pk_fma_f32 v[192:193], v[192:193], v[174:175], v[132:133]
	v_log_f32_e32 v180, v180
	v_log_f32_e32 v181, v181
	v_log_f32_e32 v182, v182
	v_log_f32_e32 v183, v183
	v_max_f32_e32 v191, 0xda24260, v191
	v_max_f32_e32 v190, 0xda24260, v190
	v_max_f32_e32 v193, 0xda24260, v193
	v_max_f32_e32 v192, 0xda24260, v192
	v_log_f32_e32 v190, v190
	v_log_f32_e32 v191, v191
	v_log_f32_e32 v192, v192
	v_log_f32_e32 v193, v193
	v_pk_mul_f32 v[180:181], v[180:181], s[26:27] op_sel_hi:[1,0]
	v_pk_mul_f32 v[182:183], v[182:183], s[26:27] op_sel_hi:[1,0]
	v_pk_mul_f32 v[190:191], v[190:191], s[26:27] op_sel_hi:[1,0]
	v_pk_mul_f32 v[192:193], v[192:193], s[26:27] op_sel_hi:[1,0]
	v_cvt_pk_bf16_f32 v180, v180, v181
	v_cvt_pk_bf16_f32 v181, v182, v183
	v_cvt_pk_bf16_f32 v182, v190, v191
	s_nop 0
	v_cvt_pk_bf16_f32 v183, v192, v193
	global_store_dwordx4 v[178:179], v[180:183], off offset:256 nt
	v_add_u32_e32 v178, 0xb0, v189
	v_mad_i64_i32 v[162:163], s[2:3], v178, s17, v[162:163]
	v_lshl_add_u64 v[162:163], v[162:163], 0, v[164:165]
	v_pk_mul_f32 v[164:165], v[20:21], s[24:25] op_sel_hi:[1,0]
	s_nop 0
	v_exp_f32_e32 v164, v164
	v_exp_f32_e32 v165, v165
	s_nop 0
	v_pk_add_f32 v[164:165], v[164:165], 1.0 op_sel_hi:[1,0]
	s_nop 0
	v_rcp_f32_e32 v164, v164
	v_rcp_f32_e32 v165, v165
	s_nop 0
	v_pk_fma_f32 v[142:143], v[164:165], v[158:159], v[142:143]
	v_pk_mul_f32 v[158:159], v[22:23], s[24:25] op_sel_hi:[1,0]
	v_max_f32_e32 v143, 0xda24260, v143
	v_exp_f32_e32 v158, v158
	v_exp_f32_e32 v159, v159
	v_max_f32_e32 v142, 0xda24260, v142
	v_log_f32_e32 v142, v142
	v_log_f32_e32 v143, v143
	v_pk_add_f32 v[158:159], v[158:159], 1.0 op_sel_hi:[1,0]
	v_pk_mul_f32 v[142:143], v[142:143], s[26:27] op_sel_hi:[1,0]
	v_rcp_f32_e32 v158, v158
	v_rcp_f32_e32 v159, v159
	s_nop 0
	v_pk_fma_f32 v[144:145], v[158:159], v[160:161], v[144:145]
	v_pk_mul_f32 v[158:159], v[12:13], s[24:25] op_sel_hi:[1,0]
	v_max_f32_e32 v145, 0xda24260, v145
	v_exp_f32_e32 v158, v158
	v_exp_f32_e32 v159, v159
	v_max_f32_e32 v144, 0xda24260, v144
	v_log_f32_e32 v144, v144
	v_log_f32_e32 v145, v145
	v_pk_add_f32 v[158:159], v[158:159], 1.0 op_sel_hi:[1,0]
	v_pk_mul_f32 v[144:145], v[144:145], s[26:27] op_sel_hi:[1,0]
	v_rcp_f32_e32 v158, v158
	v_rcp_f32_e32 v159, v159
	s_nop 0
	v_pk_fma_f32 v[138:139], v[158:159], v[166:167], v[138:139]
	s_nop 0
	v_max_f32_e32 v139, 0xda24260, v139
	v_max_f32_e32 v138, 0xda24260, v138
	v_log_f32_e32 v138, v138
	v_log_f32_e32 v139, v139
	s_nop 0
	v_pk_mul_f32 v[158:159], v[138:139], s[26:27] op_sel_hi:[1,0]
	v_pk_mul_f32 v[138:139], v[14:15], s[24:25] op_sel_hi:[1,0]
	s_nop 0
	v_exp_f32_e32 v138, v138
	v_exp_f32_e32 v139, v139
	s_nop 0
	v_pk_add_f32 v[138:139], v[138:139], 1.0 op_sel_hi:[1,0]
	s_nop 0
	v_rcp_f32_e32 v138, v138
	v_rcp_f32_e32 v139, v139
	s_nop 0
	v_pk_fma_f32 v[138:139], v[138:139], v[168:169], v[140:141]
	s_nop 0
	v_max_f32_e32 v139, 0xda24260, v139
	v_max_f32_e32 v138, 0xda24260, v138
	v_log_f32_e32 v138, v138
	v_log_f32_e32 v139, v139
	s_nop 0
	v_pk_mul_f32 v[160:161], v[138:139], s[26:27] op_sel_hi:[1,0]
	v_cvt_pk_bf16_f32 v138, v142, v143
	v_cvt_pk_bf16_f32 v139, v144, v145
	v_cvt_pk_bf16_f32 v140, v158, v159
	s_nop 0
	v_cvt_pk_bf16_f32 v141, v160, v161
	global_store_dwordx4 v[162:163], v[138:141], off nt
	s_nop 1
	v_pk_mul_f32 v[138:139], v[4:5], s[24:25] op_sel_hi:[1,0]
	s_nop 0
	v_exp_f32_e32 v138, v138
	v_exp_f32_e32 v139, v139
	s_nop 0
	v_pk_add_f32 v[138:139], v[138:139], 1.0 op_sel_hi:[1,0]
	s_nop 0
	v_rcp_f32_e32 v138, v138
	v_rcp_f32_e32 v139, v139
	s_nop 0
	v_pk_fma_f32 v[134:135], v[138:139], v[170:171], v[134:135]
	v_pk_mul_f32 v[138:139], v[6:7], s[24:25] op_sel_hi:[1,0]
	v_max_f32_e32 v135, 0xda24260, v135
	v_exp_f32_e32 v138, v138
	v_exp_f32_e32 v139, v139
	v_max_f32_e32 v134, 0xda24260, v134
	v_log_f32_e32 v134, v134
	v_log_f32_e32 v135, v135
	v_pk_add_f32 v[138:139], v[138:139], 1.0 op_sel_hi:[1,0]
	v_pk_mul_f32 v[134:135], v[134:135], s[26:27] op_sel_hi:[1,0]
	v_rcp_f32_e32 v138, v138
	v_rcp_f32_e32 v139, v139
	s_nop 0
	v_pk_fma_f32 v[136:137], v[138:139], v[172:173], v[136:137]
	v_pk_mul_f32 v[138:139], v[0:1], s[24:25] op_sel_hi:[1,0]
	v_max_f32_e32 v137, 0xda24260, v137
	v_exp_f32_e32 v138, v138
	v_exp_f32_e32 v139, v139
	v_max_f32_e32 v136, 0xda24260, v136
	v_log_f32_e32 v136, v136
	v_log_f32_e32 v137, v137
	v_pk_add_f32 v[138:139], v[138:139], 1.0 op_sel_hi:[1,0]
	v_pk_mul_f32 v[136:137], v[136:137], s[26:27] op_sel_hi:[1,0]
	v_rcp_f32_e32 v138, v138
	v_rcp_f32_e32 v139, v139
	s_nop 0
	v_pk_fma_f32 v[130:131], v[138:139], v[176:177], v[130:131]
	s_nop 0
	v_max_f32_e32 v131, 0xda24260, v131
	v_max_f32_e32 v130, 0xda24260, v130
	v_log_f32_e32 v130, v130
	v_log_f32_e32 v131, v131
	s_nop 0
	v_pk_mul_f32 v[138:139], v[130:131], s[26:27] op_sel_hi:[1,0]
	v_pk_mul_f32 v[130:131], v[2:3], s[24:25] op_sel_hi:[1,0]
	s_nop 0
	v_exp_f32_e32 v130, v130
	v_exp_f32_e32 v131, v131
	s_nop 0
	v_pk_add_f32 v[130:131], v[130:131], 1.0 op_sel_hi:[1,0]
	s_nop 0
	v_rcp_f32_e32 v130, v130
	v_rcp_f32_e32 v131, v131
	s_nop 0
	v_pk_fma_f32 v[130:131], v[130:131], v[174:175], v[132:133]
	s_nop 0
	v_max_f32_e32 v131, 0xda24260, v131
	v_max_f32_e32 v130, 0xda24260, v130
	v_log_f32_e32 v130, v130
	v_log_f32_e32 v131, v131
	s_nop 0
	v_pk_mul_f32 v[140:141], v[130:131], s[26:27] op_sel_hi:[1,0]
	v_cvt_pk_bf16_f32 v130, v134, v135
	v_cvt_pk_bf16_f32 v131, v136, v137
	v_cvt_pk_bf16_f32 v132, v138, v139
	s_nop 0
	v_cvt_pk_bf16_f32 v133, v140, v141

.LBB0_329:
	s_andn2_b64 vcc, exec, s[6:7]
	s_mov_b64 s[6:7], -1
	global_store_dwordx4 v[162:163], v[130:133], off offset:256 nt
	s_cbranch_vccnz .LBB0_302

.Lg1ls_fast:
	s_lshl_b32 s2, s2, 9
	v_subrev_u32_e32 v130, s2, v64
	v_ashrrev_i32_e32 v131, 31, v130
	v_lshl_add_u64 v[134:135], v[130:131], 2, s[10:11]
	global_load_dwordx4 v[138:141], v[134:135], off offset:16
	global_load_dwordx4 v[142:145], v[134:135], off
	global_load_dwordx4 v[130:133], v[134:135], off offset:528
	s_nop 0
	global_load_dwordx4 v[134:137], v[134:135], off offset:512
	v_ashrrev_i32_e32 v169, 31, v64
	v_mov_b32_e32 v168, v64
	s_mov_b32 s24, 0xbfb8aa3b
	v_lshlrev_b64 v[168:169], 1, v[168:169]
	v_mov_b64_e32 v[166:167], s[8:9]
	s_movk_i32 s17, 0x2400
	s_mov_b32 s26, 0x3f317218
	s_waitcnt vmcnt(0)
	v_pk_add_f32 v[212:213], v[142:143], 1.0 op_sel_hi:[1,0] neg_lo:[1,0] neg_hi:[1,0]
	v_pk_add_f32 v[214:215], v[144:145], 1.0 op_sel_hi:[1,0] neg_lo:[1,0] neg_hi:[1,0]
	v_pk_add_f32 v[216:217], v[138:139], 1.0 op_sel_hi:[1,0] neg_lo:[1,0] neg_hi:[1,0]
	v_pk_add_f32 v[218:219], v[140:141], 1.0 op_sel_hi:[1,0] neg_lo:[1,0] neg_hi:[1,0]
	v_pk_add_f32 v[220:221], v[134:135], 1.0 op_sel_hi:[1,0] neg_lo:[1,0] neg_hi:[1,0]
	v_pk_add_f32 v[222:223], v[136:137], 1.0 op_sel_hi:[1,0] neg_lo:[1,0] neg_hi:[1,0]
	v_pk_add_f32 v[224:225], v[130:131], 1.0 op_sel_hi:[1,0] neg_lo:[1,0] neg_hi:[1,0]
	v_pk_add_f32 v[226:227], v[132:133], 1.0 op_sel_hi:[1,0] neg_lo:[1,0] neg_hi:[1,0]
	v_mov_b32_e32 v170, v189
	v_mad_i64_i32 v[170:171], s[2:3], v170, s17, v[166:167]
	v_lshl_add_u64 v[170:171], v[170:171], 0, v[168:169]
	v_pk_mul_f32 v[172:173], v[126:127], s[24:25] op_sel_hi:[1,0]
	v_pk_mul_f32 v[174:175], v[128:129], s[24:25] op_sel_hi:[1,0]
	v_pk_mul_f32 v[176:177], v[122:123], s[24:25] op_sel_hi:[1,0]
	v_pk_mul_f32 v[178:179], v[124:125], s[24:25] op_sel_hi:[1,0]
	v_exp_f32_e32 v172, v172
	v_exp_f32_e32 v173, v173
	v_exp_f32_e32 v174, v174
	v_exp_f32_e32 v175, v175
	v_exp_f32_e32 v176, v176
	v_exp_f32_e32 v177, v177
	v_exp_f32_e32 v178, v178
	v_exp_f32_e32 v179, v179
	v_pk_add_f32 v[172:173], v[172:173], 1.0 op_sel_hi:[1,0]
	v_pk_add_f32 v[174:175], v[174:175], 1.0 op_sel_hi:[1,0]
	v_pk_add_f32 v[176:177], v[176:177], 1.0 op_sel_hi:[1,0]
	v_pk_add_f32 v[178:179], v[178:179], 1.0 op_sel_hi:[1,0]
	v_rcp_f32_e32 v172, v172
	v_rcp_f32_e32 v173, v173
	v_rcp_f32_e32 v174, v174
	v_rcp_f32_e32 v175, v175
	v_rcp_f32_e32 v176, v176
	v_rcp_f32_e32 v177, v177
	v_rcp_f32_e32 v178, v178
	v_rcp_f32_e32 v179, v179
	v_pk_fma_f32 v[172:173], v[172:173], v[212:213], v[142:143]
	v_pk_fma_f32 v[174:175], v[174:175], v[214:215], v[144:145]
	v_pk_fma_f32 v[176:177], v[176:177], v[216:217], v[138:139]
	v_pk_fma_f32 v[178:179], v[178:179], v[218:219], v[140:141]
	v_max_f32_e32 v173, 0xda24260, v173
	v_max_f32_e32 v172, 0xda24260, v172
	v_max_f32_e32 v175, 0xda24260, v175
	v_max_f32_e32 v174, 0xda24260, v174
	v_max_f32_e32 v177, 0xda24260, v177
	v_max_f32_e32 v176, 0xda24260, v176
	v_max_f32_e32 v179, 0xda24260, v179
	v_max_f32_e32 v178, 0xda24260, v178
	v_log_f32_e32 v172, v172
	v_log_f32_e32 v173, v173
	v_log_f32_e32 v174, v174
	v_log_f32_e32 v175, v175
	v_log_f32_e32 v176, v176
	v_log_f32_e32 v177, v177
	v_log_f32_e32 v178, v178
	v_log_f32_e32 v179, v179
	v_pk_mul_f32 v[172:173], v[172:173], s[26:27] op_sel_hi:[1,0]
	v_pk_mul_f32 v[174:175], v[174:175], s[26:27] op_sel_hi:[1,0]
	v_pk_mul_f32 v[176:177], v[176:177], s[26:27] op_sel_hi:[1,0]
	v_pk_mul_f32 v[178:179], v[178:179], s[26:27] op_sel_hi:[1,0]
	v_cvt_pk_bf16_f32 v180, v172, v173
	v_cvt_pk_bf16_f32 v181, v174, v175
	v_cvt_pk_bf16_f32 v182, v176, v177
	v_cvt_pk_bf16_f32 v183, v178, v179
	global_store_dwordx4 v[170:171], v[180:183], off nt
	v_pk_mul_f32 v[172:173], v[114:115], s[24:25] op_sel_hi:[1,0]
	v_pk_mul_f32 v[174:175], v[116:117], s[24:25] op_sel_hi:[1,0]
	v_pk_mul_f32 v[176:177], v[106:107], s[24:25] op_sel_hi:[1,0]
	v_pk_mul_f32 v[178:179], v[108:109], s[24:25] op_sel_hi:[1,0]
	v_exp_f32_e32 v172, v172
	v_exp_f32_e32 v173, v173
	v_exp_f32_e32 v174, v174
	v_exp_f32_e32 v175, v175
	v_exp_f32_e32 v176, v176
	v_exp_f32_e32 v177, v177
	v_exp_f32_e32 v178, v178
	v_exp_f32_e32 v179, v179
	v_pk_add_f32 v[172:173], v[172:173], 1.0 op_sel_hi:[1,0]
	v_pk_add_f32 v[174:175], v[174:175], 1.0 op_sel_hi:[1,0]
	v_pk_add_f32 v[176:177], v[176:177], 1.0 op_sel_hi:[1,0]
	v_pk_add_f32 v[178:179], v[178:179], 1.0 op_sel_hi:[1,0]
	v_rcp_f32_e32 v172, v172
	v_rcp_f32_e32 v173, v173
	v_rcp_f32_e32 v174, v174
	v_rcp_f32_e32 v175, v175
	v_rcp_f32_e32 v176, v176
	v_rcp_f32_e32 v177, v177
	v_rcp_f32_e32 v178, v178
	v_rcp_f32_e32 v179, v179
	v_pk_fma_f32 v[172:173], v[172:173], v[220:221], v[134:135]
	v_pk_fma_f32 v[174:175], v[174:175], v[222:223], v[136:137]
	v_pk_fma_f32 v[176:177], v[176:177], v[224:225], v[130:131]
	v_pk_fma_f32 v[178:179], v[178:179], v[226:227], v[132:133]
	v_max_f32_e32 v173, 0xda24260, v173
	v_max_f32_e32 v172, 0xda24260, v172
	v_max_f32_e32 v175, 0xda24260, v175
	v_max_f32_e32 v174, 0xda24260, v174
	v_max_f32_e32 v177, 0xda24260, v177
	v_max_f32_e32 v176, 0xda24260, v176
	v_max_f32_e32 v179, 0xda24260, v179
	v_max_f32_e32 v178, 0xda24260, v178
	v_log_f32_e32 v172, v172
	v_log_f32_e32 v173, v173
	v_log_f32_e32 v174, v174
	v_log_f32_e32 v175, v175
	v_log_f32_e32 v176, v176
	v_log_f32_e32 v177, v177
	v_log_f32_e32 v178, v178
	v_log_f32_e32 v179, v179
	v_pk_mul_f32 v[172:173], v[172:173], s[26:27] op_sel_hi:[1,0]
	v_pk_mul_f32 v[174:175], v[174:175], s[26:27] op_sel_hi:[1,0]
	v_pk_mul_f32 v[176:177], v[176:177], s[26:27] op_sel_hi:[1,0]
	v_pk_mul_f32 v[178:179], v[178:179], s[26:27] op_sel_hi:[1,0]
	v_cvt_pk_bf16_f32 v180, v172, v173
	v_cvt_pk_bf16_f32 v181, v174, v175
	v_cvt_pk_bf16_f32 v182, v176, v177
	v_cvt_pk_bf16_f32 v183, v178, v179
	global_store_dwordx4 v[170:171], v[180:183], off offset:256 nt
	v_add_u32_e32 v170, 16, v189
	v_mad_i64_i32 v[170:171], s[2:3], v170, s17, v[166:167]
	v_lshl_add_u64 v[170:171], v[170:171], 0, v[168:169]
	v_pk_mul_f32 v[172:173], v[118:119], s[24:25] op_sel_hi:[1,0]
	v_pk_mul_f32 v[174:175], v[120:121], s[24:25] op_sel_hi:[1,0]
	v_pk_mul_f32 v[176:177], v[110:111], s[24:25] op_sel_hi:[1,0]
	v_pk_mul_f32 v[178:179], v[112:113], s[24:25] op_sel_hi:[1,0]
	v_exp_f32_e32 v172, v172
	v_exp_f32_e32 v173, v173
	v_exp_f32_e32 v174, v174
	v_exp_f32_e32 v175, v175
	v_exp_f32_e32 v176, v176
	v_exp_f32_e32 v177, v177
	v_exp_f32_e32 v178, v178
	v_exp_f32_e32 v179, v179
	v_pk_add_f32 v[172:173], v[172:173], 1.0 op_sel_hi:[1,0]
	v_pk_add_f32 v[174:175], v[174:175], 1.0 op_sel_hi:[1,0]
	v_pk_add_f32 v[176:177], v[176:177], 1.0 op_sel_hi:[1,0]
	v_pk_add_f32 v[178:179], v[178:179], 1.0 op_sel_hi:[1,0]
	v_rcp_f32_e32 v172, v172
	v_rcp_f32_e32 v173, v173
	v_rcp_f32_e32 v174, v174
	v_rcp_f32_e32 v175, v175
	v_rcp_f32_e32 v176, v176
	v_rcp_f32_e32 v177, v177
	v_rcp_f32_e32 v178, v178
	v_rcp_f32_e32 v179, v179
	v_pk_fma_f32 v[172:173], v[172:173], v[212:213], v[142:143]
	v_pk_fma_f32 v[174:175], v[174:175], v[214:215], v[144:145]
	v_pk_fma_f32 v[176:177], v[176:177], v[216:217], v[138:139]
	v_pk_fma_f32 v[178:179], v[178:179], v[218:219], v[140:141]
	v_max_f32_e32 v173, 0xda24260, v173
	v_max_f32_e32 v172, 0xda24260, v172
	v_max_f32_e32 v175, 0xda24260, v175
	v_max_f32_e32 v174, 0xda24260, v174
	v_max_f32_e32 v177, 0xda24260, v177
	v_max_f32_e32 v176, 0xda24260, v176
	v_max_f32_e32 v179, 0xda24260, v179
	v_max_f32_e32 v178, 0xda24260, v178
	v_log_f32_e32 v172, v172
	v_log_f32_e32 v173, v173
	v_log_f32_e32 v174, v174
	v_log_f32_e32 v175, v175
	v_log_f32_e32 v176, v176
	v_log_f32_e32 v177, v177
	v_log_f32_e32 v178, v178
	v_log_f32_e32 v179, v179
	v_pk_mul_f32 v[172:173], v[172:173], s[26:27] op_sel_hi:[1,0]
	v_pk_mul_f32 v[174:175], v[174:175], s[26:27] op_sel_hi:[1,0]
	v_pk_mul_f32 v[176:177], v[176:177], s[26:27] op_sel_hi:[1,0]
	v_pk_mul_f32 v[178:179], v[178:179], s[26:27] op_sel_hi:[1,0]
	v_cvt_pk_bf16_f32 v180, v172, v173
	v_cvt_pk_bf16_f32 v181, v174, v175
	v_cvt_pk_bf16_f32 v182, v176, v177
	v_cvt_pk_bf16_f32 v183, v178, v179
	global_store_dwordx4 v[170:171], v[180:183], off nt
	v_pk_mul_f32 v[172:173], v[98:99], s[24:25] op_sel_hi:[1,0]
	v_pk_mul_f32 v[174:175], v[100:101], s[24:25] op_sel_hi:[1,0]
	v_pk_mul_f32 v[176:177], v[90:91], s[24:25] op_sel_hi:[1,0]
	v_pk_mul_f32 v[178:179], v[92:93], s[24:25] op_sel_hi:[1,0]
	v_exp_f32_e32 v172, v172
	v_exp_f32_e32 v173, v173
	v_exp_f32_e32 v174, v174
	v_exp_f32_e32 v175, v175
	v_exp_f32_e32 v176, v176
	v_exp_f32_e32 v177, v177
	v_exp_f32_e32 v178, v178
	v_exp_f32_e32 v179, v179
	v_pk_add_f32 v[172:173], v[172:173], 1.0 op_sel_hi:[1,0]
	v_pk_add_f32 v[174:175], v[174:175], 1.0 op_sel_hi:[1,0]
	v_pk_add_f32 v[176:177], v[176:177], 1.0 op_sel_hi:[1,0]
	v_pk_add_f32 v[178:179], v[178:179], 1.0 op_sel_hi:[1,0]
	v_rcp_f32_e32 v172, v172
	v_rcp_f32_e32 v173, v173
	v_rcp_f32_e32 v174, v174
	v_rcp_f32_e32 v175, v175
	v_rcp_f32_e32 v176, v176
	v_rcp_f32_e32 v177, v177
	v_rcp_f32_e32 v178, v178
	v_rcp_f32_e32 v179, v179
	v_pk_fma_f32 v[172:173], v[172:173], v[220:221], v[134:135]
	v_pk_fma_f32 v[174:175], v[174:175], v[222:223], v[136:137]
	v_pk_fma_f32 v[176:177], v[176:177], v[224:225], v[130:131]
	v_pk_fma_f32 v[178:179], v[178:179], v[226:227], v[132:133]
	v_max_f32_e32 v173, 0xda24260, v173
	v_max_f32_e32 v172, 0xda24260, v172
	v_max_f32_e32 v175, 0xda24260, v175
	v_max_f32_e32 v174, 0xda24260, v174
	v_max_f32_e32 v177, 0xda24260, v177
	v_max_f32_e32 v176, 0xda24260, v176
	v_max_f32_e32 v179, 0xda24260, v179
	v_max_f32_e32 v178, 0xda24260, v178
	v_log_f32_e32 v172, v172
	v_log_f32_e32 v173, v173
	v_log_f32_e32 v174, v174
	v_log_f32_e32 v175, v175
	v_log_f32_e32 v176, v176
	v_log_f32_e32 v177, v177
	v_log_f32_e32 v178, v178
	v_log_f32_e32 v179, v179
	v_pk_mul_f32 v[172:173], v[172:173], s[26:27] op_sel_hi:[1,0]
	v_pk_mul_f32 v[174:175], v[174:175], s[26:27] op_sel_hi:[1,0]
	v_pk_mul_f32 v[176:177], v[176:177], s[26:27] op_sel_hi:[1,0]
	v_pk_mul_f32 v[178:179], v[178:179], s[26:27] op_sel_hi:[1,0]
	v_cvt_pk_bf16_f32 v180, v172, v173
	v_cvt_pk_bf16_f32 v181, v174, v175
	v_cvt_pk_bf16_f32 v182, v176, v177
	v_cvt_pk_bf16_f32 v183, v178, v179
	global_store_dwordx4 v[170:171], v[180:183], off offset:256 nt
	v_add_u32_e32 v170, 32, v189
	v_mad_i64_i32 v[170:171], s[2:3], v170, s17, v[166:167]
	v_lshl_add_u64 v[170:171], v[170:171], 0, v[168:169]
	v_pk_mul_f32 v[172:173], v[102:103], s[24:25] op_sel_hi:[1,0]
	v_pk_mul_f32 v[174:175], v[104:105], s[24:25] op_sel_hi:[1,0]
	v_pk_mul_f32 v[176:177], v[94:95], s[24:25] op_sel_hi:[1,0]
	v_pk_mul_f32 v[178:179], v[96:97], s[24:25] op_sel_hi:[1,0]
	v_exp_f32_e32 v172, v172
	v_exp_f32_e32 v173, v173
	v_exp_f32_e32 v174, v174
	v_exp_f32_e32 v175, v175
	v_exp_f32_e32 v176, v176
	v_exp_f32_e32 v177, v177
	v_exp_f32_e32 v178, v178
	v_exp_f32_e32 v179, v179
	v_pk_add_f32 v[172:173], v[172:173], 1.0 op_sel_hi:[1,0]
	v_pk_add_f32 v[174:175], v[174:175], 1.0 op_sel_hi:[1,0]
	v_pk_add_f32 v[176:177], v[176:177], 1.0 op_sel_hi:[1,0]
	v_pk_add_f32 v[178:179], v[178:179], 1.0 op_sel_hi:[1,0]
	v_rcp_f32_e32 v172, v172
	v_rcp_f32_e32 v173, v173
	v_rcp_f32_e32 v174, v174
	v_rcp_f32_e32 v175, v175
	v_rcp_f32_e32 v176, v176
	v_rcp_f32_e32 v177, v177
	v_rcp_f32_e32 v178, v178
	v_rcp_f32_e32 v179, v179
	v_pk_fma_f32 v[172:173], v[172:173], v[212:213], v[142:143]
	v_pk_fma_f32 v[174:175], v[174:175], v[214:215], v[144:145]
	v_pk_fma_f32 v[176:177], v[176:177], v[216:217], v[138:139]
	v_pk_fma_f32 v[178:179], v[178:179], v[218:219], v[140:141]
	v_max_f32_e32 v173, 0xda24260, v173
	v_max_f32_e32 v172, 0xda24260, v172
	v_max_f32_e32 v175, 0xda24260, v175
	v_max_f32_e32 v174, 0xda24260, v174
	v_max_f32_e32 v177, 0xda24260, v177
	v_max_f32_e32 v176, 0xda24260, v176
	v_max_f32_e32 v179, 0xda24260, v179
	v_max_f32_e32 v178, 0xda24260, v178
	v_log_f32_e32 v172, v172
	v_log_f32_e32 v173, v173
	v_log_f32_e32 v174, v174
	v_log_f32_e32 v175, v175
	v_log_f32_e32 v176, v176
	v_log_f32_e32 v177, v177
	v_log_f32_e32 v178, v178
	v_log_f32_e32 v179, v179
	v_pk_mul_f32 v[172:173], v[172:173], s[26:27] op_sel_hi:[1,0]
	v_pk_mul_f32 v[174:175], v[174:175], s[26:27] op_sel_hi:[1,0]
	v_pk_mul_f32 v[176:177], v[176:177], s[26:27] op_sel_hi:[1,0]
	v_pk_mul_f32 v[178:179], v[178:179], s[26:27] op_sel_hi:[1,0]
	v_cvt_pk_bf16_f32 v180, v172, v173
	v_cvt_pk_bf16_f32 v181, v174, v175
	v_cvt_pk_bf16_f32 v182, v176, v177
	v_cvt_pk_bf16_f32 v183, v178, v179
	global_store_dwordx4 v[170:171], v[180:183], off nt
	v_pk_mul_f32 v[172:173], v[82:83], s[24:25] op_sel_hi:[1,0]
	v_pk_mul_f32 v[174:175], v[84:85], s[24:25] op_sel_hi:[1,0]
	v_pk_mul_f32 v[176:177], v[74:75], s[24:25] op_sel_hi:[1,0]
	v_pk_mul_f32 v[178:179], v[76:77], s[24:25] op_sel_hi:[1,0]
	v_exp_f32_e32 v172, v172
	v_exp_f32_e32 v173, v173
	v_exp_f32_e32 v174, v174
	v_exp_f32_e32 v175, v175
	v_exp_f32_e32 v176, v176
	v_exp_f32_e32 v177, v177
	v_exp_f32_e32 v178, v178
	v_exp_f32_e32 v179, v179
	v_pk_add_f32 v[172:173], v[172:173], 1.0 op_sel_hi:[1,0]
	v_pk_add_f32 v[174:175], v[174:175], 1.0 op_sel_hi:[1,0]
	v_pk_add_f32 v[176:177], v[176:177], 1.0 op_sel_hi:[1,0]
	v_pk_add_f32 v[178:179], v[178:179], 1.0 op_sel_hi:[1,0]
	v_rcp_f32_e32 v172, v172
	v_rcp_f32_e32 v173, v173
	v_rcp_f32_e32 v174, v174
	v_rcp_f32_e32 v175, v175
	v_rcp_f32_e32 v176, v176
	v_rcp_f32_e32 v177, v177
	v_rcp_f32_e32 v178, v178
	v_rcp_f32_e32 v179, v179
	v_pk_fma_f32 v[172:173], v[172:173], v[220:221], v[134:135]
	v_pk_fma_f32 v[174:175], v[174:175], v[222:223], v[136:137]
	v_pk_fma_f32 v[176:177], v[176:177], v[224:225], v[130:131]
	v_pk_fma_f32 v[178:179], v[178:179], v[226:227], v[132:133]
	v_max_f32_e32 v173, 0xda24260, v173
	v_max_f32_e32 v172, 0xda24260, v172
	v_max_f32_e32 v175, 0xda24260, v175
	v_max_f32_e32 v174, 0xda24260, v174
	v_max_f32_e32 v177, 0xda24260, v177
	v_max_f32_e32 v176, 0xda24260, v176
	v_max_f32_e32 v179, 0xda24260, v179
	v_max_f32_e32 v178, 0xda24260, v178
	v_log_f32_e32 v172, v172
	v_log_f32_e32 v173, v173
	v_log_f32_e32 v174, v174
	v_log_f32_e32 v175, v175
	v_log_f32_e32 v176, v176
	v_log_f32_e32 v177, v177
	v_log_f32_e32 v178, v178
	v_log_f32_e32 v179, v179
	v_pk_mul_f32 v[172:173], v[172:173], s[26:27] op_sel_hi:[1,0]
	v_pk_mul_f32 v[174:175], v[174:175], s[26:27] op_sel_hi:[1,0]
	v_pk_mul_f32 v[176:177], v[176:177], s[26:27] op_sel_hi:[1,0]
	v_pk_mul_f32 v[178:179], v[178:179], s[26:27] op_sel_hi:[1,0]
	v_cvt_pk_bf16_f32 v180, v172, v173
	v_cvt_pk_bf16_f32 v181, v174, v175
	v_cvt_pk_bf16_f32 v182, v176, v177
	v_cvt_pk_bf16_f32 v183, v178, v179
	global_store_dwordx4 v[170:171], v[180:183], off offset:256 nt
	v_add_u32_e32 v170, 48, v189
	v_mad_i64_i32 v[170:171], s[2:3], v170, s17, v[166:167]
	v_lshl_add_u64 v[170:171], v[170:171], 0, v[168:169]
	v_pk_mul_f32 v[172:173], v[86:87], s[24:25] op_sel_hi:[1,0]
	v_pk_mul_f32 v[174:175], v[88:89], s[24:25] op_sel_hi:[1,0]
	v_pk_mul_f32 v[176:177], v[78:79], s[24:25] op_sel_hi:[1,0]
	v_pk_mul_f32 v[178:179], v[80:81], s[24:25] op_sel_hi:[1,0]
	v_exp_f32_e32 v172, v172
	v_exp_f32_e32 v173, v173
	v_exp_f32_e32 v174, v174
	v_exp_f32_e32 v175, v175
	v_exp_f32_e32 v176, v176
	v_exp_f32_e32 v177, v177
	v_exp_f32_e32 v178, v178
	v_exp_f32_e32 v179, v179
	v_pk_add_f32 v[172:173], v[172:173], 1.0 op_sel_hi:[1,0]
	v_pk_add_f32 v[174:175], v[174:175], 1.0 op_sel_hi:[1,0]
	v_pk_add_f32 v[176:177], v[176:177], 1.0 op_sel_hi:[1,0]
	v_pk_add_f32 v[178:179], v[178:179], 1.0 op_sel_hi:[1,0]
	v_rcp_f32_e32 v172, v172
	v_rcp_f32_e32 v173, v173
	v_rcp_f32_e32 v174, v174
	v_rcp_f32_e32 v175, v175
	v_rcp_f32_e32 v176, v176
	v_rcp_f32_e32 v177, v177
	v_rcp_f32_e32 v178, v178
	v_rcp_f32_e32 v179, v179
	v_pk_fma_f32 v[172:173], v[172:173], v[212:213], v[142:143]
	v_pk_fma_f32 v[174:175], v[174:175], v[214:215], v[144:145]
	v_pk_fma_f32 v[176:177], v[176:177], v[216:217], v[138:139]
	v_pk_fma_f32 v[178:179], v[178:179], v[218:219], v[140:141]
	v_max_f32_e32 v173, 0xda24260, v173
	v_max_f32_e32 v172, 0xda24260, v172
	v_max_f32_e32 v175, 0xda24260, v175
	v_max_f32_e32 v174, 0xda24260, v174
	v_max_f32_e32 v177, 0xda24260, v177
	v_max_f32_e32 v176, 0xda24260, v176
	v_max_f32_e32 v179, 0xda24260, v179
	v_max_f32_e32 v178, 0xda24260, v178
	v_log_f32_e32 v172, v172
	v_log_f32_e32 v173, v173
	v_log_f32_e32 v174, v174
	v_log_f32_e32 v175, v175
	v_log_f32_e32 v176, v176
	v_log_f32_e32 v177, v177
	v_log_f32_e32 v178, v178
	v_log_f32_e32 v179, v179
	v_pk_mul_f32 v[172:173], v[172:173], s[26:27] op_sel_hi:[1,0]
	v_pk_mul_f32 v[174:175], v[174:175], s[26:27] op_sel_hi:[1,0]
	v_pk_mul_f32 v[176:177], v[176:177], s[26:27] op_sel_hi:[1,0]
	v_pk_mul_f32 v[178:179], v[178:179], s[26:27] op_sel_hi:[1,0]
	v_cvt_pk_bf16_f32 v180, v172, v173
	v_cvt_pk_bf16_f32 v181, v174, v175
	v_cvt_pk_bf16_f32 v182, v176, v177
	v_cvt_pk_bf16_f32 v183, v178, v179
	global_store_dwordx4 v[170:171], v[180:183], off nt
	v_pk_mul_f32 v[172:173], v[70:71], s[24:25] op_sel_hi:[1,0]
	v_pk_mul_f32 v[174:175], v[72:73], s[24:25] op_sel_hi:[1,0]
	v_pk_mul_f32 v[176:177], v[66:67], s[24:25] op_sel_hi:[1,0]
	v_pk_mul_f32 v[178:179], v[68:69], s[24:25] op_sel_hi:[1,0]
	v_exp_f32_e32 v172, v172
	v_exp_f32_e32 v173, v173
	v_exp_f32_e32 v174, v174
	v_exp_f32_e32 v175, v175
	v_exp_f32_e32 v176, v176
	v_exp_f32_e32 v177, v177
	v_exp_f32_e32 v178, v178
	v_exp_f32_e32 v179, v179
	v_pk_add_f32 v[172:173], v[172:173], 1.0 op_sel_hi:[1,0]
	v_pk_add_f32 v[174:175], v[174:175], 1.0 op_sel_hi:[1,0]
	v_pk_add_f32 v[176:177], v[176:177], 1.0 op_sel_hi:[1,0]
	v_pk_add_f32 v[178:179], v[178:179], 1.0 op_sel_hi:[1,0]
	v_rcp_f32_e32 v172, v172
	v_rcp_f32_e32 v173, v173
	v_rcp_f32_e32 v174, v174
	v_rcp_f32_e32 v175, v175
	v_rcp_f32_e32 v176, v176
	v_rcp_f32_e32 v177, v177
	v_rcp_f32_e32 v178, v178
	v_rcp_f32_e32 v179, v179
	v_pk_fma_f32 v[172:173], v[172:173], v[220:221], v[134:135]
	v_pk_fma_f32 v[174:175], v[174:175], v[222:223], v[136:137]
	v_pk_fma_f32 v[176:177], v[176:177], v[224:225], v[130:131]
	v_pk_fma_f32 v[178:179], v[178:179], v[226:227], v[132:133]
	v_max_f32_e32 v173, 0xda24260, v173
	v_max_f32_e32 v172, 0xda24260, v172
	v_max_f32_e32 v175, 0xda24260, v175
	v_max_f32_e32 v174, 0xda24260, v174
	v_max_f32_e32 v177, 0xda24260, v177
	v_max_f32_e32 v176, 0xda24260, v176
	v_max_f32_e32 v179, 0xda24260, v179
	v_max_f32_e32 v178, 0xda24260, v178
	v_log_f32_e32 v172, v172
	v_log_f32_e32 v173, v173
	v_log_f32_e32 v174, v174
	v_log_f32_e32 v175, v175
	v_log_f32_e32 v176, v176
	v_log_f32_e32 v177, v177
	v_log_f32_e32 v178, v178
	v_log_f32_e32 v179, v179
	v_pk_mul_f32 v[172:173], v[172:173], s[26:27] op_sel_hi:[1,0]
	v_pk_mul_f32 v[174:175], v[174:175], s[26:27] op_sel_hi:[1,0]
	v_pk_mul_f32 v[176:177], v[176:177], s[26:27] op_sel_hi:[1,0]
	v_pk_mul_f32 v[178:179], v[178:179], s[26:27] op_sel_hi:[1,0]
	v_cvt_pk_bf16_f32 v180, v172, v173
	v_cvt_pk_bf16_f32 v181, v174, v175
	v_cvt_pk_bf16_f32 v182, v176, v177
	v_cvt_pk_bf16_f32 v183, v178, v179
	global_store_dwordx4 v[170:171], v[180:183], off offset:256 nt
	v_add_u32_e32 v170, 128, v189
	v_mad_i64_i32 v[170:171], s[2:3], v170, s17, v[166:167]
	v_lshl_add_u64 v[170:171], v[170:171], 0, v[168:169]
	v_pk_mul_f32 v[172:173], v[60:61], s[24:25] op_sel_hi:[1,0]
	v_pk_mul_f32 v[174:175], v[62:63], s[24:25] op_sel_hi:[1,0]
	v_pk_mul_f32 v[176:177], v[56:57], s[24:25] op_sel_hi:[1,0]
	v_pk_mul_f32 v[178:179], v[58:59], s[24:25] op_sel_hi:[1,0]
	v_exp_f32_e32 v172, v172
	v_exp_f32_e32 v173, v173
	v_exp_f32_e32 v174, v174
	v_exp_f32_e32 v175, v175
	v_exp_f32_e32 v176, v176
	v_exp_f32_e32 v177, v177
	v_exp_f32_e32 v178, v178
	v_exp_f32_e32 v179, v179
	v_pk_add_f32 v[172:173], v[172:173], 1.0 op_sel_hi:[1,0]
	v_pk_add_f32 v[174:175], v[174:175], 1.0 op_sel_hi:[1,0]
	v_pk_add_f32 v[176:177], v[176:177], 1.0 op_sel_hi:[1,0]
	v_pk_add_f32 v[178:179], v[178:179], 1.0 op_sel_hi:[1,0]
	v_rcp_f32_e32 v172, v172
	v_rcp_f32_e32 v173, v173
	v_rcp_f32_e32 v174, v174
	v_rcp_f32_e32 v175, v175
	v_rcp_f32_e32 v176, v176
	v_rcp_f32_e32 v177, v177
	v_rcp_f32_e32 v178, v178
	v_rcp_f32_e32 v179, v179
	v_pk_fma_f32 v[172:173], v[172:173], v[212:213], v[142:143]
	v_pk_fma_f32 v[174:175], v[174:175], v[214:215], v[144:145]
	v_pk_fma_f32 v[176:177], v[176:177], v[216:217], v[138:139]
	v_pk_fma_f32 v[178:179], v[178:179], v[218:219], v[140:141]
	v_max_f32_e32 v173, 0xda24260, v173
	v_max_f32_e32 v172, 0xda24260, v172
	v_max_f32_e32 v175, 0xda24260, v175
	v_max_f32_e32 v174, 0xda24260, v174
	v_max_f32_e32 v177, 0xda24260, v177
	v_max_f32_e32 v176, 0xda24260, v176
	v_max_f32_e32 v179, 0xda24260, v179
	v_max_f32_e32 v178, 0xda24260, v178
	v_log_f32_e32 v172, v172
	v_log_f32_e32 v173, v173
	v_log_f32_e32 v174, v174
	v_log_f32_e32 v175, v175
	v_log_f32_e32 v176, v176
	v_log_f32_e32 v177, v177
	v_log_f32_e32 v178, v178
	v_log_f32_e32 v179, v179
	v_pk_mul_f32 v[172:173], v[172:173], s[26:27] op_sel_hi:[1,0]
	v_pk_mul_f32 v[174:175], v[174:175], s[26:27] op_sel_hi:[1,0]
	v_pk_mul_f32 v[176:177], v[176:177], s[26:27] op_sel_hi:[1,0]
	v_pk_mul_f32 v[178:179], v[178:179], s[26:27] op_sel_hi:[1,0]
	v_cvt_pk_bf16_f32 v180, v172, v173
	v_cvt_pk_bf16_f32 v181, v174, v175
	v_cvt_pk_bf16_f32 v182, v176, v177
	v_cvt_pk_bf16_f32 v183, v178, v179
	global_store_dwordx4 v[170:171], v[180:183], off nt
	v_pk_mul_f32 v[172:173], v[48:49], s[24:25] op_sel_hi:[1,0]
	v_pk_mul_f32 v[174:175], v[50:51], s[24:25] op_sel_hi:[1,0]
	v_pk_mul_f32 v[176:177], v[40:41], s[24:25] op_sel_hi:[1,0]
	v_pk_mul_f32 v[178:179], v[42:43], s[24:25] op_sel_hi:[1,0]
	v_exp_f32_e32 v172, v172
	v_exp_f32_e32 v173, v173
	v_exp_f32_e32 v174, v174
	v_exp_f32_e32 v175, v175
	v_exp_f32_e32 v176, v176
	v_exp_f32_e32 v177, v177
	v_exp_f32_e32 v178, v178
	v_exp_f32_e32 v179, v179
	v_pk_add_f32 v[172:173], v[172:173], 1.0 op_sel_hi:[1,0]
	v_pk_add_f32 v[174:175], v[174:175], 1.0 op_sel_hi:[1,0]
	v_pk_add_f32 v[176:177], v[176:177], 1.0 op_sel_hi:[1,0]
	v_pk_add_f32 v[178:179], v[178:179], 1.0 op_sel_hi:[1,0]
	v_rcp_f32_e32 v172, v172
	v_rcp_f32_e32 v173, v173
	v_rcp_f32_e32 v174, v174
	v_rcp_f32_e32 v175, v175
	v_rcp_f32_e32 v176, v176
	v_rcp_f32_e32 v177, v177
	v_rcp_f32_e32 v178, v178
	v_rcp_f32_e32 v179, v179
	v_pk_fma_f32 v[172:173], v[172:173], v[220:221], v[134:135]
	v_pk_fma_f32 v[174:175], v[174:175], v[222:223], v[136:137]
	v_pk_fma_f32 v[176:177], v[176:177], v[224:225], v[130:131]
	v_pk_fma_f32 v[178:179], v[178:179], v[226:227], v[132:133]
	v_max_f32_e32 v173, 0xda24260, v173
	v_max_f32_e32 v172, 0xda24260, v172
	v_max_f32_e32 v175, 0xda24260, v175
	v_max_f32_e32 v174, 0xda24260, v174
	v_max_f32_e32 v177, 0xda24260, v177
	v_max_f32_e32 v176, 0xda24260, v176
	v_max_f32_e32 v179, 0xda24260, v179
	v_max_f32_e32 v178, 0xda24260, v178
	v_log_f32_e32 v172, v172
	v_log_f32_e32 v173, v173
	v_log_f32_e32 v174, v174
	v_log_f32_e32 v175, v175
	v_log_f32_e32 v176, v176
	v_log_f32_e32 v177, v177
	v_log_f32_e32 v178, v178
	v_log_f32_e32 v179, v179
	v_pk_mul_f32 v[172:173], v[172:173], s[26:27] op_sel_hi:[1,0]
	v_pk_mul_f32 v[174:175], v[174:175], s[26:27] op_sel_hi:[1,0]
	v_pk_mul_f32 v[176:177], v[176:177], s[26:27] op_sel_hi:[1,0]
	v_pk_mul_f32 v[178:179], v[178:179], s[26:27] op_sel_hi:[1,0]
	v_cvt_pk_bf16_f32 v180, v172, v173
	v_cvt_pk_bf16_f32 v181, v174, v175
	v_cvt_pk_bf16_f32 v182, v176, v177
	v_cvt_pk_bf16_f32 v183, v178, v179
	global_store_dwordx4 v[170:171], v[180:183], off offset:256 nt
	v_add_u32_e32 v170, 144, v189
	v_mad_i64_i32 v[170:171], s[2:3], v170, s17, v[166:167]
	v_lshl_add_u64 v[170:171], v[170:171], 0, v[168:169]
	v_pk_mul_f32 v[172:173], v[52:53], s[24:25] op_sel_hi:[1,0]
	v_pk_mul_f32 v[174:175], v[54:55], s[24:25] op_sel_hi:[1,0]
	v_pk_mul_f32 v[176:177], v[44:45], s[24:25] op_sel_hi:[1,0]
	v_pk_mul_f32 v[178:179], v[46:47], s[24:25] op_sel_hi:[1,0]
	v_exp_f32_e32 v172, v172
	v_exp_f32_e32 v173, v173
	v_exp_f32_e32 v174, v174
	v_exp_f32_e32 v175, v175
	v_exp_f32_e32 v176, v176
	v_exp_f32_e32 v177, v177
	v_exp_f32_e32 v178, v178
	v_exp_f32_e32 v179, v179
	v_pk_add_f32 v[172:173], v[172:173], 1.0 op_sel_hi:[1,0]
	v_pk_add_f32 v[174:175], v[174:175], 1.0 op_sel_hi:[1,0]
	v_pk_add_f32 v[176:177], v[176:177], 1.0 op_sel_hi:[1,0]
	v_pk_add_f32 v[178:179], v[178:179], 1.0 op_sel_hi:[1,0]
	v_rcp_f32_e32 v172, v172
	v_rcp_f32_e32 v173, v173
	v_rcp_f32_e32 v174, v174
	v_rcp_f32_e32 v175, v175
	v_rcp_f32_e32 v176, v176
	v_rcp_f32_e32 v177, v177
	v_rcp_f32_e32 v178, v178
	v_rcp_f32_e32 v179, v179
	v_pk_fma_f32 v[172:173], v[172:173], v[212:213], v[142:143]
	v_pk_fma_f32 v[174:175], v[174:175], v[214:215], v[144:145]
	v_pk_fma_f32 v[176:177], v[176:177], v[216:217], v[138:139]
	v_pk_fma_f32 v[178:179], v[178:179], v[218:219], v[140:141]
	v_max_f32_e32 v173, 0xda24260, v173
	v_max_f32_e32 v172, 0xda24260, v172
	v_max_f32_e32 v175, 0xda24260, v175
	v_max_f32_e32 v174, 0xda24260, v174
	v_max_f32_e32 v177, 0xda24260, v177
	v_max_f32_e32 v176, 0xda24260, v176
	v_max_f32_e32 v179, 0xda24260, v179
	v_max_f32_e32 v178, 0xda24260, v178
	v_log_f32_e32 v172, v172
	v_log_f32_e32 v173, v173
	v_log_f32_e32 v174, v174
	v_log_f32_e32 v175, v175
	v_log_f32_e32 v176, v176
	v_log_f32_e32 v177, v177
	v_log_f32_e32 v178, v178
	v_log_f32_e32 v179, v179
	v_pk_mul_f32 v[172:173], v[172:173], s[26:27] op_sel_hi:[1,0]
	v_pk_mul_f32 v[174:175], v[174:175], s[26:27] op_sel_hi:[1,0]
	v_pk_mul_f32 v[176:177], v[176:177], s[26:27] op_sel_hi:[1,0]
	v_pk_mul_f32 v[178:179], v[178:179], s[26:27] op_sel_hi:[1,0]
	v_cvt_pk_bf16_f32 v180, v172, v173
	v_cvt_pk_bf16_f32 v181, v174, v175
	v_cvt_pk_bf16_f32 v182, v176, v177
	v_cvt_pk_bf16_f32 v183, v178, v179
	global_store_dwordx4 v[170:171], v[180:183], off nt
	v_pk_mul_f32 v[172:173], v[32:33], s[24:25] op_sel_hi:[1,0]
	v_pk_mul_f32 v[174:175], v[34:35], s[24:25] op_sel_hi:[1,0]
	v_pk_mul_f32 v[176:177], v[24:25], s[24:25] op_sel_hi:[1,0]
	v_pk_mul_f32 v[178:179], v[26:27], s[24:25] op_sel_hi:[1,0]
	v_exp_f32_e32 v172, v172
	v_exp_f32_e32 v173, v173
	v_exp_f32_e32 v174, v174
	v_exp_f32_e32 v175, v175
	v_exp_f32_e32 v176, v176
	v_exp_f32_e32 v177, v177
	v_exp_f32_e32 v178, v178
	v_exp_f32_e32 v179, v179
	v_pk_add_f32 v[172:173], v[172:173], 1.0 op_sel_hi:[1,0]
	v_pk_add_f32 v[174:175], v[174:175], 1.0 op_sel_hi:[1,0]
	v_pk_add_f32 v[176:177], v[176:177], 1.0 op_sel_hi:[1,0]
	v_pk_add_f32 v[178:179], v[178:179], 1.0 op_sel_hi:[1,0]
	v_rcp_f32_e32 v172, v172
	v_rcp_f32_e32 v173, v173
	v_rcp_f32_e32 v174, v174
	v_rcp_f32_e32 v175, v175
	v_rcp_f32_e32 v176, v176
	v_rcp_f32_e32 v177, v177
	v_rcp_f32_e32 v178, v178
	v_rcp_f32_e32 v179, v179
	v_pk_fma_f32 v[172:173], v[172:173], v[220:221], v[134:135]
	v_pk_fma_f32 v[174:175], v[174:175], v[222:223], v[136:137]
	v_pk_fma_f32 v[176:177], v[176:177], v[224:225], v[130:131]
	v_pk_fma_f32 v[178:179], v[178:179], v[226:227], v[132:133]
	v_max_f32_e32 v173, 0xda24260, v173
	v_max_f32_e32 v172, 0xda24260, v172
	v_max_f32_e32 v175, 0xda24260, v175
	v_max_f32_e32 v174, 0xda24260, v174
	v_max_f32_e32 v177, 0xda24260, v177
	v_max_f32_e32 v176, 0xda24260, v176
	v_max_f32_e32 v179, 0xda24260, v179
	v_max_f32_e32 v178, 0xda24260, v178
	v_log_f32_e32 v172, v172
	v_log_f32_e32 v173, v173
	v_log_f32_e32 v174, v174
	v_log_f32_e32 v175, v175
	v_log_f32_e32 v176, v176
	v_log_f32_e32 v177, v177
	v_log_f32_e32 v178, v178
	v_log_f32_e32 v179, v179
	v_pk_mul_f32 v[172:173], v[172:173], s[26:27] op_sel_hi:[1,0]
	v_pk_mul_f32 v[174:175], v[174:175], s[26:27] op_sel_hi:[1,0]
	v_pk_mul_f32 v[176:177], v[176:177], s[26:27] op_sel_hi:[1,0]
	v_pk_mul_f32 v[178:179], v[178:179], s[26:27] op_sel_hi:[1,0]
	v_cvt_pk_bf16_f32 v180, v172, v173
	v_cvt_pk_bf16_f32 v181, v174, v175
	v_cvt_pk_bf16_f32 v182, v176, v177
	v_cvt_pk_bf16_f32 v183, v178, v179
	global_store_dwordx4 v[170:171], v[180:183], off offset:256 nt
	v_add_u32_e32 v170, 160, v189
	v_mad_i64_i32 v[170:171], s[2:3], v170, s17, v[166:167]
	v_lshl_add_u64 v[170:171], v[170:171], 0, v[168:169]
	v_pk_mul_f32 v[172:173], v[36:37], s[24:25] op_sel_hi:[1,0]
	v_pk_mul_f32 v[174:175], v[38:39], s[24:25] op_sel_hi:[1,0]
	v_pk_mul_f32 v[176:177], v[28:29], s[24:25] op_sel_hi:[1,0]
	v_pk_mul_f32 v[178:179], v[30:31], s[24:25] op_sel_hi:[1,0]
	v_exp_f32_e32 v172, v172
	v_exp_f32_e32 v173, v173
	v_exp_f32_e32 v174, v174
	v_exp_f32_e32 v175, v175
	v_exp_f32_e32 v176, v176
	v_exp_f32_e32 v177, v177
	v_exp_f32_e32 v178, v178
	v_exp_f32_e32 v179, v179
	v_pk_add_f32 v[172:173], v[172:173], 1.0 op_sel_hi:[1,0]
	v_pk_add_f32 v[174:175], v[174:175], 1.0 op_sel_hi:[1,0]
	v_pk_add_f32 v[176:177], v[176:177], 1.0 op_sel_hi:[1,0]
	v_pk_add_f32 v[178:179], v[178:179], 1.0 op_sel_hi:[1,0]
	v_rcp_f32_e32 v172, v172
	v_rcp_f32_e32 v173, v173
	v_rcp_f32_e32 v174, v174
	v_rcp_f32_e32 v175, v175
	v_rcp_f32_e32 v176, v176
	v_rcp_f32_e32 v177, v177
	v_rcp_f32_e32 v178, v178
	v_rcp_f32_e32 v179, v179
	v_pk_fma_f32 v[172:173], v[172:173], v[212:213], v[142:143]
	v_pk_fma_f32 v[174:175], v[174:175], v[214:215], v[144:145]
	v_pk_fma_f32 v[176:177], v[176:177], v[216:217], v[138:139]
	v_pk_fma_f32 v[178:179], v[178:179], v[218:219], v[140:141]
	v_max_f32_e32 v173, 0xda24260, v173
	v_max_f32_e32 v172, 0xda24260, v172
	v_max_f32_e32 v175, 0xda24260, v175
	v_max_f32_e32 v174, 0xda24260, v174
	v_max_f32_e32 v177, 0xda24260, v177
	v_max_f32_e32 v176, 0xda24260, v176
	v_max_f32_e32 v179, 0xda24260, v179
	v_max_f32_e32 v178, 0xda24260, v178
	v_log_f32_e32 v172, v172
	v_log_f32_e32 v173, v173
	v_log_f32_e32 v174, v174
	v_log_f32_e32 v175, v175
	v_log_f32_e32 v176, v176
	v_log_f32_e32 v177, v177
	v_log_f32_e32 v178, v178
	v_log_f32_e32 v179, v179
	v_pk_mul_f32 v[172:173], v[172:173], s[26:27] op_sel_hi:[1,0]
	v_pk_mul_f32 v[174:175], v[174:175], s[26:27] op_sel_hi:[1,0]
	v_pk_mul_f32 v[176:177], v[176:177], s[26:27] op_sel_hi:[1,0]
	v_pk_mul_f32 v[178:179], v[178:179], s[26:27] op_sel_hi:[1,0]
	v_cvt_pk_bf16_f32 v180, v172, v173
	v_cvt_pk_bf16_f32 v181, v174, v175
	v_cvt_pk_bf16_f32 v182, v176, v177
	v_cvt_pk_bf16_f32 v183, v178, v179
	global_store_dwordx4 v[170:171], v[180:183], off nt
	v_pk_mul_f32 v[172:173], v[16:17], s[24:25] op_sel_hi:[1,0]
	v_pk_mul_f32 v[174:175], v[18:19], s[24:25] op_sel_hi:[1,0]
	v_pk_mul_f32 v[176:177], v[8:9], s[24:25] op_sel_hi:[1,0]
	v_pk_mul_f32 v[178:179], v[10:11], s[24:25] op_sel_hi:[1,0]
	v_exp_f32_e32 v172, v172
	v_exp_f32_e32 v173, v173
	v_exp_f32_e32 v174, v174
	v_exp_f32_e32 v175, v175
	v_exp_f32_e32 v176, v176
	v_exp_f32_e32 v177, v177
	v_exp_f32_e32 v178, v178
	v_exp_f32_e32 v179, v179
	v_pk_add_f32 v[172:173], v[172:173], 1.0 op_sel_hi:[1,0]
	v_pk_add_f32 v[174:175], v[174:175], 1.0 op_sel_hi:[1,0]
	v_pk_add_f32 v[176:177], v[176:177], 1.0 op_sel_hi:[1,0]
	v_pk_add_f32 v[178:179], v[178:179], 1.0 op_sel_hi:[1,0]
	v_rcp_f32_e32 v172, v172
	v_rcp_f32_e32 v173, v173
	v_rcp_f32_e32 v174, v174
	v_rcp_f32_e32 v175, v175
	v_rcp_f32_e32 v176, v176
	v_rcp_f32_e32 v177, v177
	v_rcp_f32_e32 v178, v178
	v_rcp_f32_e32 v179, v179
	v_pk_fma_f32 v[172:173], v[172:173], v[220:221], v[134:135]
	v_pk_fma_f32 v[174:175], v[174:175], v[222:223], v[136:137]
	v_pk_fma_f32 v[176:177], v[176:177], v[224:225], v[130:131]
	v_pk_fma_f32 v[178:179], v[178:179], v[226:227], v[132:133]
	v_max_f32_e32 v173, 0xda24260, v173
	v_max_f32_e32 v172, 0xda24260, v172
	v_max_f32_e32 v175, 0xda24260, v175
	v_max_f32_e32 v174, 0xda24260, v174
	v_max_f32_e32 v177, 0xda24260, v177
	v_max_f32_e32 v176, 0xda24260, v176
	v_max_f32_e32 v179, 0xda24260, v179
	v_max_f32_e32 v178, 0xda24260, v178
	v_log_f32_e32 v172, v172
	v_log_f32_e32 v173, v173
	v_log_f32_e32 v174, v174
	v_log_f32_e32 v175, v175
	v_log_f32_e32 v176, v176
	v_log_f32_e32 v177, v177
	v_log_f32_e32 v178, v178
	v_log_f32_e32 v179, v179
	v_pk_mul_f32 v[172:173], v[172:173], s[26:27] op_sel_hi:[1,0]
	v_pk_mul_f32 v[174:175], v[174:175], s[26:27] op_sel_hi:[1,0]
	v_pk_mul_f32 v[176:177], v[176:177], s[26:27] op_sel_hi:[1,0]
	v_pk_mul_f32 v[178:179], v[178:179], s[26:27] op_sel_hi:[1,0]
	v_cvt_pk_bf16_f32 v180, v172, v173
	v_cvt_pk_bf16_f32 v181, v174, v175
	v_cvt_pk_bf16_f32 v182, v176, v177
	v_cvt_pk_bf16_f32 v183, v178, v179
	global_store_dwordx4 v[170:171], v[180:183], off offset:256 nt
	v_add_u32_e32 v162, 176, v189
	v_mad_i64_i32 v[162:163], s[2:3], v162, s17, v[166:167]
	v_lshl_add_u64 v[162:163], v[162:163], 0, v[168:169]
	v_pk_mul_f32 v[172:173], v[20:21], s[24:25] op_sel_hi:[1,0]
	v_pk_mul_f32 v[174:175], v[22:23], s[24:25] op_sel_hi:[1,0]
	v_pk_mul_f32 v[176:177], v[12:13], s[24:25] op_sel_hi:[1,0]
	v_pk_mul_f32 v[178:179], v[14:15], s[24:25] op_sel_hi:[1,0]
	v_exp_f32_e32 v172, v172
	v_exp_f32_e32 v173, v173
	v_exp_f32_e32 v174, v174
	v_exp_f32_e32 v175, v175
	v_exp_f32_e32 v176, v176
	v_exp_f32_e32 v177, v177
	v_exp_f32_e32 v178, v178
	v_exp_f32_e32 v179, v179
	v_pk_add_f32 v[172:173], v[172:173], 1.0 op_sel_hi:[1,0]
	v_pk_add_f32 v[174:175], v[174:175], 1.0 op_sel_hi:[1,0]
	v_pk_add_f32 v[176:177], v[176:177], 1.0 op_sel_hi:[1,0]
	v_pk_add_f32 v[178:179], v[178:179], 1.0 op_sel_hi:[1,0]
	v_rcp_f32_e32 v172, v172
	v_rcp_f32_e32 v173, v173
	v_rcp_f32_e32 v174, v174
	v_rcp_f32_e32 v175, v175
	v_rcp_f32_e32 v176, v176
	v_rcp_f32_e32 v177, v177
	v_rcp_f32_e32 v178, v178
	v_rcp_f32_e32 v179, v179
	v_pk_fma_f32 v[172:173], v[172:173], v[212:213], v[142:143]
	v_pk_fma_f32 v[174:175], v[174:175], v[214:215], v[144:145]
	v_pk_fma_f32 v[176:177], v[176:177], v[216:217], v[138:139]
	v_pk_fma_f32 v[178:179], v[178:179], v[218:219], v[140:141]
	v_max_f32_e32 v173, 0xda24260, v173
	v_max_f32_e32 v172, 0xda24260, v172
	v_max_f32_e32 v175, 0xda24260, v175
	v_max_f32_e32 v174, 0xda24260, v174
	v_max_f32_e32 v177, 0xda24260, v177
	v_max_f32_e32 v176, 0xda24260, v176
	v_max_f32_e32 v179, 0xda24260, v179
	v_max_f32_e32 v178, 0xda24260, v178
	v_log_f32_e32 v172, v172
	v_log_f32_e32 v173, v173
	v_log_f32_e32 v174, v174
	v_log_f32_e32 v175, v175
	v_log_f32_e32 v176, v176
	v_log_f32_e32 v177, v177
	v_log_f32_e32 v178, v178
	v_log_f32_e32 v179, v179
	v_pk_mul_f32 v[172:173], v[172:173], s[26:27] op_sel_hi:[1,0]
	v_pk_mul_f32 v[174:175], v[174:175], s[26:27] op_sel_hi:[1,0]
	v_pk_mul_f32 v[176:177], v[176:177], s[26:27] op_sel_hi:[1,0]
	v_pk_mul_f32 v[178:179], v[178:179], s[26:27] op_sel_hi:[1,0]
	v_cvt_pk_bf16_f32 v180, v172, v173
	v_cvt_pk_bf16_f32 v181, v174, v175
	v_cvt_pk_bf16_f32 v182, v176, v177
	v_cvt_pk_bf16_f32 v183, v178, v179
	global_store_dwordx4 v[162:163], v[180:183], off nt
	v_pk_mul_f32 v[172:173], v[4:5], s[24:25] op_sel_hi:[1,0]
	v_pk_mul_f32 v[174:175], v[6:7], s[24:25] op_sel_hi:[1,0]
	v_pk_mul_f32 v[176:177], v[0:1], s[24:25] op_sel_hi:[1,0]
	v_pk_mul_f32 v[178:179], v[2:3], s[24:25] op_sel_hi:[1,0]
	v_exp_f32_e32 v172, v172
	v_exp_f32_e32 v173, v173
	v_exp_f32_e32 v174, v174
	v_exp_f32_e32 v175, v175
	v_exp_f32_e32 v176, v176
	v_exp_f32_e32 v177, v177
	v_exp_f32_e32 v178, v178
	v_exp_f32_e32 v179, v179
	v_pk_add_f32 v[172:173], v[172:173], 1.0 op_sel_hi:[1,0]
	v_pk_add_f32 v[174:175], v[174:175], 1.0 op_sel_hi:[1,0]
	v_pk_add_f32 v[176:177], v[176:177], 1.0 op_sel_hi:[1,0]
	v_pk_add_f32 v[178:179], v[178:179], 1.0 op_sel_hi:[1,0]
	v_rcp_f32_e32 v172, v172
	v_rcp_f32_e32 v173, v173
	v_rcp_f32_e32 v174, v174
	v_rcp_f32_e32 v175, v175
	v_rcp_f32_e32 v176, v176
	v_rcp_f32_e32 v177, v177
	v_rcp_f32_e32 v178, v178
	v_rcp_f32_e32 v179, v179
	v_pk_fma_f32 v[172:173], v[172:173], v[220:221], v[134:135]
	v_pk_fma_f32 v[174:175], v[174:175], v[222:223], v[136:137]
	v_pk_fma_f32 v[176:177], v[176:177], v[224:225], v[130:131]
	v_pk_fma_f32 v[178:179], v[178:179], v[226:227], v[132:133]
	v_max_f32_e32 v173, 0xda24260, v173
	v_max_f32_e32 v172, 0xda24260, v172
	v_max_f32_e32 v175, 0xda24260, v175
	v_max_f32_e32 v174, 0xda24260, v174
	v_max_f32_e32 v177, 0xda24260, v177
	v_max_f32_e32 v176, 0xda24260, v176
	v_max_f32_e32 v179, 0xda24260, v179
	v_max_f32_e32 v178, 0xda24260, v178
	v_log_f32_e32 v172, v172
	v_log_f32_e32 v173, v173
	v_log_f32_e32 v174, v174
	v_log_f32_e32 v175, v175
	v_log_f32_e32 v176, v176
	v_log_f32_e32 v177, v177
	v_log_f32_e32 v178, v178
	v_log_f32_e32 v179, v179
	v_pk_mul_f32 v[172:173], v[172:173], s[26:27] op_sel_hi:[1,0]
	v_pk_mul_f32 v[174:175], v[174:175], s[26:27] op_sel_hi:[1,0]
	v_pk_mul_f32 v[176:177], v[176:177], s[26:27] op_sel_hi:[1,0]
	v_pk_mul_f32 v[178:179], v[178:179], s[26:27] op_sel_hi:[1,0]
	v_cvt_pk_bf16_f32 v180, v172, v173
	v_cvt_pk_bf16_f32 v181, v174, v175
	v_cvt_pk_bf16_f32 v182, v176, v177
	v_cvt_pk_bf16_f32 v183, v178, v179
	v_mov_b32_e32 v130, v180
	v_mov_b32_e32 v131, v181
	v_mov_b32_e32 v132, v182
	v_mov_b32_e32 v133, v183
	s_branch .LBB0_328
